# K-loop: pre-MFMA barrier placed after the first MFMA of each block (first MFMA queues behind partner half's last); setprio removed
# speedup vs baseline: 1.0750x; 1.0750x over previous
; #define PG8_STAGE(bufoff, gbase, voff) do { _Pragma("unroll") for (int _i = 0; _i < 2; ++_i) \
;         __builtin_amdgcn_global_load_lds((const unsigned*)((const char*)(gbase) + (voff)[_i]), (PG8_LAS unsigned*)(lds + (bufoff) + ldsw + _i * 8192), 16, 0, 0); } while (0)
; #define PG8_LDA(dst, b, h) do { _Pragma("unroll") for (int m = 0; m < 4; ++m) _Pragma("unroll") for (int k = 0; k < 2; ++k) dst[m][k] = *(const PG8_LAS bf16x8*)(lds + PG8_SA(b, h) + aoff + m * 2048 + k * 1024); } while (0)
; #define PG8_LDB(dst, b, h) do { _Pragma("unroll") for (int n = 0; n < 2; ++n) _Pragma("unroll") for (int k = 0; k < 2; ++k) dst[n][k] = *(const PG8_LAS bf16x8*)(lds + PG8_SB(b, h) + boff + n * 2048 + k * 1024); } while (0)
; #define PG8_MMA(ai, bj, At, Bt) do { __builtin_amdgcn_s_setprio(1); _Pragma("unroll") for (int m = 0; m < 4; ++m) _Pragma("unroll") for (int n = 0; n < 2; ++n) _Pragma("unroll") for (int k = 0; k < 2; ++k) \
;         acc[ai][bj][m][n] = __builtin_amdgcn_mfma_f32_16x16x32_bf16(Bt[n][k], At[m][k], acc[ai][bj][m][n], 0, 0, 0); __builtin_amdgcn_s_setprio(0); } while (0)
; #define PG8_BAR __builtin_amdgcn_s_barrier()
; template <class Epi, class Sched, bool ALIGN_EPI = false>
; __device__ __forceinline__ void gemm_phase(PG8_LAS unsigned char* lds, const Gemm g, const Sched& S, const Epi& E) {
;     ...
;             const bool last = (t == nt - 2);
;             const char* a1 = cA + (size_t)(t + 1) * kstep;
;             const char* a2 = last ? nA : cA + (size_t)(t + 2) * kstep; const char* b2 = last ? nB : cB + (size_t)(t + 2) * kstep;
;             const char* a3 = a2 + kstep; const char* b3 = b2 + kstep;
;             unsigned w0[2], w1[2];
; #pragma unroll
;             for (int i = 0; i < 2; ++i) { w0[i] = (Sched::GATHER && last) ? vn0[i] : vc0[i]; w1[i] = (Sched::GATHER && last) ? vn1[i] : vc1[i]; }
;             if (last && has_next) S.a_ready(nxt);
;             PG8_LDB(B0, 0, 0); PG8_LDB(B1, 0, 1); PG8_SCHED; PG8_LDA(At, 0, 0); PG8_STAGE(PG8_SA(1, 1), a1 + hstepA, vc1);
;             PG8_WAIT_V(8); PG8_WAIT_L(0); PG8_BAR; PG8_MMA(0, 0, At, B0); PG8_MMA(0, 1, At, B1); PG8_BAR; PG8_SCHED;
;             PG8_LDA(At, 0, 1); PG8_STAGE(PG8_SB(0, 0), b2, voffB); PG8_STAGE(PG8_SB(0, 1), b2 + hstep, voffB); PG8_STAGE(PG8_SA(0, 0), a2, w0);
;             PG8_WAIT_V(8); PG8_WAIT_L(0); PG8_BAR; PG8_MMA(1, 0, At, B0); PG8_MMA(1, 1, At, B1); PG8_BAR; PG8_SCHED;
.LBB0_247:
	ds_read_b128 v[132:135], v191
	ds_read_b128 v[136:139], v191 offset:1024
	ds_read_b128 v[140:143], v191 offset:2048
	ds_read_b128 v[144:147], v191 offset:3072
	ds_read_b128 v[148:151], v193
	ds_read_b128 v[152:155], v193 offset:1024
	ds_read_b128 v[156:159], v193 offset:2048
	ds_read_b128 v[196:199], v193 offset:3072
	s_add_u32 s52, s50, 0xfff80080
	s_addc_u32 s53, s51, -1
	s_cmp_eq_u32 s80, 28
	s_cselect_b32 s55, s9, s53
	s_cselect_b32 s54, s76, s52
	s_cselect_b32 s53, s45, s79
	s_cselect_b32 s52, s77, s78
	v_lshl_add_u64 v[160:161], s[50:51], 0, v[172:173]
	s_add_i32 m0, s59, 0xc000
	ds_read_b128 v[204:207], v195
	ds_read_b128 v[210:213], v195 offset:1024
	ds_read_b128 v[214:217], v195 offset:2048
	ds_read_b128 v[218:221], v195 offset:3072
	ds_read_b128 v[222:225], v195 offset:4096
	ds_read_b128 v[226:229], v195 offset:5120
	ds_read_b128 v[230:233], v195 offset:6144
	ds_read_b128 v[234:237], v195 offset:7168
	global_load_lds_dwordx4 v[160:161], off
	v_lshl_add_u64 v[160:161], s[50:51], 0, v[174:175]
	s_add_i32 m0, s59, 0xe000
	s_nop 0
	global_load_lds_dwordx4 v[160:161], off
	s_waitcnt vmcnt(8)
	s_waitcnt lgkmcnt(0)
	v_mfma_f32_16x16x32_bf16 v[126:129], v[132:135], v[204:207], v[126:129]
	s_barrier
	v_mfma_f32_16x16x32_bf16 v[122:125], v[140:143], v[204:207], v[122:125]
	v_mfma_f32_16x16x32_bf16 v[110:113], v[132:135], v[214:217], v[110:113]
	v_mfma_f32_16x16x32_bf16 v[106:109], v[140:143], v[214:217], v[106:109]
	v_mfma_f32_16x16x32_bf16 v[94:97], v[132:135], v[222:225], v[94:97]
	v_mfma_f32_16x16x32_bf16 v[90:93], v[140:143], v[222:225], v[90:93]
	v_mfma_f32_16x16x32_bf16 v[78:81], v[132:135], v[230:233], v[78:81]
	v_mfma_f32_16x16x32_bf16 v[74:77], v[140:143], v[230:233], v[74:77]
	v_mfma_f32_16x16x32_bf16 v[126:129], v[136:139], v[210:213], v[126:129]
	v_mfma_f32_16x16x32_bf16 v[122:125], v[144:147], v[210:213], v[122:125]
	v_mfma_f32_16x16x32_bf16 v[110:113], v[136:139], v[218:221], v[110:113]
	v_mfma_f32_16x16x32_bf16 v[106:109], v[144:147], v[218:221], v[106:109]
	v_mfma_f32_16x16x32_bf16 v[94:97], v[136:139], v[226:229], v[94:97]
	v_mfma_f32_16x16x32_bf16 v[90:93], v[144:147], v[226:229], v[90:93]
	v_mfma_f32_16x16x32_bf16 v[78:81], v[136:139], v[234:237], v[78:81]
	v_mfma_f32_16x16x32_bf16 v[74:77], v[144:147], v[234:237], v[74:77]
	v_mfma_f32_16x16x32_bf16 v[118:121], v[148:151], v[204:207], v[118:121]
	v_mfma_f32_16x16x32_bf16 v[114:117], v[156:159], v[204:207], v[114:117]
	v_mfma_f32_16x16x32_bf16 v[102:105], v[148:151], v[214:217], v[102:105]
	v_mfma_f32_16x16x32_bf16 v[98:101], v[156:159], v[214:217], v[98:101]
	v_mfma_f32_16x16x32_bf16 v[86:89], v[148:151], v[222:225], v[86:89]
	v_mfma_f32_16x16x32_bf16 v[82:85], v[156:159], v[222:225], v[82:85]
	v_mfma_f32_16x16x32_bf16 v[70:73], v[148:151], v[230:233], v[70:73]
	v_mfma_f32_16x16x32_bf16 v[66:69], v[156:159], v[230:233], v[66:69]
	v_mfma_f32_16x16x32_bf16 v[118:121], v[152:155], v[210:213], v[118:121]
	v_mfma_f32_16x16x32_bf16 v[114:117], v[196:199], v[210:213], v[114:117]
	v_mfma_f32_16x16x32_bf16 v[102:105], v[152:155], v[218:221], v[102:105]
	v_mfma_f32_16x16x32_bf16 v[98:101], v[196:199], v[218:221], v[98:101]
	v_mfma_f32_16x16x32_bf16 v[86:89], v[152:155], v[226:229], v[86:89]
	v_mfma_f32_16x16x32_bf16 v[82:85], v[196:199], v[226:229], v[82:85]
	v_mfma_f32_16x16x32_bf16 v[70:73], v[152:155], v[234:237], v[70:73]
	v_mfma_f32_16x16x32_bf16 v[66:69], v[196:199], v[234:237], v[66:69]
	s_barrier
	s_add_i32 s81, s67, s57
	v_lshl_add_u64 v[160:161], s[52:53], 0, v[164:165]
	s_mov_b32 m0, s81
	ds_read_b128 v[204:207], v195 offset:16384
	ds_read_b128 v[210:213], v195 offset:17408
	ds_read_b128 v[214:217], v195 offset:18432
	ds_read_b128 v[218:221], v195 offset:19456
	ds_read_b128 v[222:225], v195 offset:20480
	ds_read_b128 v[226:229], v195 offset:21504
	ds_read_b128 v[230:233], v195 offset:22528
	ds_read_b128 v[234:237], v195 offset:23552
	global_load_lds_dwordx4 v[160:161], off
	s_add_i32 m0, s81, 0x2000
	s_add_u32 s82, s52, 0x80000
	v_lshl_add_u64 v[200:201], s[52:53], 0, v[168:169]
	s_addc_u32 s83, s53, 0
	s_add_i32 s81, s68, s57
	global_load_lds_dwordx4 v[200:201], off
	v_lshl_add_u64 v[238:239], s[82:83], 0, v[164:165]
	s_mov_b32 m0, s81
	v_lshl_add_u64 v[240:241], s[54:55], 0, v[166:167]
	global_load_lds_dwordx4 v[238:239], off
	v_lshl_add_u64 v[238:239], s[82:83], 0, v[168:169]
	s_add_i32 m0, s81, 0x2000
	s_nop 0
	global_load_lds_dwordx4 v[238:239], off
	v_lshl_add_u64 v[238:239], s[54:55], 0, v[162:163]
	s_mov_b32 m0, s59
	s_nop 0
	global_load_lds_dwordx4 v[238:239], off
	s_mov_b32 m0, s60
	s_nop 0
	global_load_lds_dwordx4 v[240:241], off
	s_waitcnt vmcnt(8)
	s_waitcnt lgkmcnt(0)
	v_mfma_f32_16x16x32_bf16 v[54:57], v[132:135], v[204:207], v[54:57]
	s_barrier
; #define PG8_STAGE(bufoff, gbase, voff) do { _Pragma("unroll") for (int _i = 0; _i < 2; ++_i) \
;         __builtin_amdgcn_global_load_lds((const unsigned*)((const char*)(gbase) + (voff)[_i]), (PG8_LAS unsigned*)(lds + (bufoff) + ldsw + _i * 8192), 16, 0, 0); } while (0)
; #define PG8_LDA(dst, b, h) do { _Pragma("unroll") for (int m = 0; m < 4; ++m) _Pragma("unroll") for (int k = 0; k < 2; ++k) dst[m][k] = *(const PG8_LAS bf16x8*)(lds + PG8_SA(b, h) + aoff + m * 2048 + k * 1024); } while (0)
; #define PG8_LDB(dst, b, h) do { _Pragma("unroll") for (int n = 0; n < 2; ++n) _Pragma("unroll") for (int k = 0; k < 2; ++k) dst[n][k] = *(const PG8_LAS bf16x8*)(lds + PG8_SB(b, h) + boff + n * 2048 + k * 1024); } while (0)
; #define PG8_MMA(ai, bj, At, Bt) do { __builtin_amdgcn_s_setprio(1); _Pragma("unroll") for (int m = 0; m < 4; ++m) _Pragma("unroll") for (int n = 0; n < 2; ++n) _Pragma("unroll") for (int k = 0; k < 2; ++k) \
;         acc[ai][bj][m][n] = __builtin_amdgcn_mfma_f32_16x16x32_bf16(Bt[n][k], At[m][k], acc[ai][bj][m][n], 0, 0, 0); __builtin_amdgcn_s_setprio(0); } while (0)
; #define PG8_WAIT_V(n) asm volatile("s_waitcnt vmcnt(" #n ")" ::: "memory")
; #define PG8_WAIT_L(n) asm volatile("s_waitcnt lgkmcnt(" #n ")" ::: "memory")
; #define PG8_BAR __builtin_amdgcn_s_barrier()
; #define PG8_SCHED __builtin_amdgcn_sched_barrier(0)
; template <class Epi, class Sched, bool ALIGN_EPI = false>
; __device__ __forceinline__ void gemm_phase(PG8_LAS unsigned char* lds, const Gemm g, const Sched& S, const Epi& E) {
;     ...
;             PG8_WAIT_V(8); PG8_WAIT_L(0); PG8_BAR; PG8_MMA(1, 0, At, B0); PG8_MMA(1, 1, At, B1); PG8_BAR; PG8_SCHED;
;             PG8_LDB(B0, 1, 0); PG8_LDB(B1, 1, 1); PG8_SCHED; PG8_LDA(At, 1, 0); PG8_STAGE(PG8_SA(0, 1), a2 + hstepA, w1);
;             PG8_WAIT_V(8); PG8_WAIT_L(0); PG8_BAR; PG8_MMA(0, 0, At, B0); PG8_MMA(0, 1, At, B1); PG8_BAR; PG8_SCHED;
	v_mfma_f32_16x16x32_bf16 v[50:53], v[140:143], v[204:207], v[50:53]
	v_mfma_f32_16x16x32_bf16 v[38:41], v[132:135], v[214:217], v[38:41]
	v_mfma_f32_16x16x32_bf16 v[34:37], v[140:143], v[214:217], v[34:37]
	v_mfma_f32_16x16x32_bf16 v[22:25], v[132:135], v[222:225], v[22:25]
	v_mfma_f32_16x16x32_bf16 v[18:21], v[140:143], v[222:225], v[18:21]
	v_mfma_f32_16x16x32_bf16 v[6:9], v[132:135], v[230:233], v[6:9]
	v_mfma_f32_16x16x32_bf16 v[2:5], v[140:143], v[230:233], v[2:5]
	v_mfma_f32_16x16x32_bf16 v[54:57], v[136:139], v[210:213], v[54:57]
	v_mfma_f32_16x16x32_bf16 v[50:53], v[144:147], v[210:213], v[50:53]
	v_mfma_f32_16x16x32_bf16 v[38:41], v[136:139], v[218:221], v[38:41]
	v_mfma_f32_16x16x32_bf16 v[34:37], v[144:147], v[218:221], v[34:37]
	v_mfma_f32_16x16x32_bf16 v[22:25], v[136:139], v[226:229], v[22:25]
	v_mfma_f32_16x16x32_bf16 v[18:21], v[144:147], v[226:229], v[18:21]
	v_mfma_f32_16x16x32_bf16 v[6:9], v[136:139], v[234:237], v[6:9]
	v_mfma_f32_16x16x32_bf16 v[2:5], v[144:147], v[234:237], v[2:5]
	v_mfma_f32_16x16x32_bf16 v[58:61], v[148:151], v[204:207], v[58:61]
	v_mfma_f32_16x16x32_bf16 v[62:65], v[156:159], v[204:207], v[62:65]
	v_mfma_f32_16x16x32_bf16 v[42:45], v[148:151], v[214:217], v[42:45]
	v_mfma_f32_16x16x32_bf16 v[46:49], v[156:159], v[214:217], v[46:49]
	v_mfma_f32_16x16x32_bf16 v[26:29], v[148:151], v[222:225], v[26:29]
	v_mfma_f32_16x16x32_bf16 v[30:33], v[156:159], v[222:225], v[30:33]
	v_mfma_f32_16x16x32_bf16 v[10:13], v[148:151], v[230:233], v[10:13]
	v_mfma_f32_16x16x32_bf16 v[14:17], v[156:159], v[230:233], v[14:17]
	v_mfma_f32_16x16x32_bf16 v[58:61], v[152:155], v[210:213], v[58:61]
	v_mfma_f32_16x16x32_bf16 v[62:65], v[196:199], v[210:213], v[62:65]
	v_mfma_f32_16x16x32_bf16 v[42:45], v[152:155], v[218:221], v[42:45]
	v_mfma_f32_16x16x32_bf16 v[46:49], v[196:199], v[218:221], v[46:49]
	v_mfma_f32_16x16x32_bf16 v[26:29], v[152:155], v[226:229], v[26:29]
	v_mfma_f32_16x16x32_bf16 v[30:33], v[196:199], v[226:229], v[30:33]
	v_mfma_f32_16x16x32_bf16 v[10:13], v[152:155], v[234:237], v[10:13]
	v_mfma_f32_16x16x32_bf16 v[14:17], v[196:199], v[234:237], v[14:17]
	s_barrier
	s_add_i32 s81, 0, 0x18000
	v_add_u32_e32 v131, s81, v181
	s_add_i32 s82, 0, 0x1c000
	ds_read_b128 v[132:135], v131
	ds_read_b128 v[136:139], v131 offset:1024
	ds_read_b128 v[140:143], v131 offset:2048
	ds_read_b128 v[144:147], v131 offset:3072
	v_add_u32_e32 v131, s82, v181
	ds_read_b128 v[148:151], v131
	ds_read_b128 v[152:155], v131 offset:1024
	ds_read_b128 v[156:159], v131 offset:2048
	ds_read_b128 v[196:199], v131 offset:3072
	s_add_u32 s54, s54, 0x80000
	s_addc_u32 s55, s55, 0
	s_mov_b32 m0, s61
	v_lshl_add_u64 v[242:243], s[54:55], 0, v[162:163]
	ds_read_b128 v[204:207], v195 offset:32768
	ds_read_b128 v[210:213], v195 offset:33792
	ds_read_b128 v[214:217], v195 offset:34816
	ds_read_b128 v[218:221], v195 offset:35840
	ds_read_b128 v[222:225], v195 offset:36864
	ds_read_b128 v[226:229], v195 offset:37888
	ds_read_b128 v[230:233], v195 offset:38912
	ds_read_b128 v[234:237], v195 offset:39936
	global_load_lds_dwordx4 v[242:243], off
	v_lshl_add_u64 v[242:243], s[54:55], 0, v[166:167]
	s_mov_b32 m0, s62
	s_nop 0
	global_load_lds_dwordx4 v[242:243], off
	s_waitcnt vmcnt(8)
	s_waitcnt lgkmcnt(0)
	v_mfma_f32_16x16x32_bf16 v[126:129], v[132:135], v[204:207], v[126:129]
	s_barrier
	v_mfma_f32_16x16x32_bf16 v[122:125], v[140:143], v[204:207], v[122:125]
	v_mfma_f32_16x16x32_bf16 v[110:113], v[132:135], v[214:217], v[110:113]
	v_mfma_f32_16x16x32_bf16 v[106:109], v[140:143], v[214:217], v[106:109]
	v_mfma_f32_16x16x32_bf16 v[94:97], v[132:135], v[222:225], v[94:97]
	v_mfma_f32_16x16x32_bf16 v[90:93], v[140:143], v[222:225], v[90:93]
	v_mfma_f32_16x16x32_bf16 v[78:81], v[132:135], v[230:233], v[78:81]
	v_mfma_f32_16x16x32_bf16 v[74:77], v[140:143], v[230:233], v[74:77]
	v_mfma_f32_16x16x32_bf16 v[126:129], v[136:139], v[210:213], v[126:129]
	v_mfma_f32_16x16x32_bf16 v[122:125], v[144:147], v[210:213], v[122:125]
	v_mfma_f32_16x16x32_bf16 v[110:113], v[136:139], v[218:221], v[110:113]
	v_mfma_f32_16x16x32_bf16 v[106:109], v[144:147], v[218:221], v[106:109]
	v_mfma_f32_16x16x32_bf16 v[94:97], v[136:139], v[226:229], v[94:97]
	v_mfma_f32_16x16x32_bf16 v[90:93], v[144:147], v[226:229], v[90:93]
	v_mfma_f32_16x16x32_bf16 v[78:81], v[136:139], v[234:237], v[78:81]
	v_mfma_f32_16x16x32_bf16 v[74:77], v[144:147], v[234:237], v[74:77]
	v_mfma_f32_16x16x32_bf16 v[118:121], v[148:151], v[204:207], v[118:121]
	v_mfma_f32_16x16x32_bf16 v[114:117], v[156:159], v[204:207], v[114:117]
	v_mfma_f32_16x16x32_bf16 v[102:105], v[148:151], v[214:217], v[102:105]
	v_mfma_f32_16x16x32_bf16 v[98:101], v[156:159], v[214:217], v[98:101]
	v_mfma_f32_16x16x32_bf16 v[86:89], v[148:151], v[222:225], v[86:89]
	v_mfma_f32_16x16x32_bf16 v[82:85], v[156:159], v[222:225], v[82:85]
	v_mfma_f32_16x16x32_bf16 v[70:73], v[148:151], v[230:233], v[70:73]
	v_mfma_f32_16x16x32_bf16 v[66:69], v[156:159], v[230:233], v[66:69]
	v_mfma_f32_16x16x32_bf16 v[118:121], v[152:155], v[210:213], v[118:121]
	v_mfma_f32_16x16x32_bf16 v[114:117], v[196:199], v[210:213], v[114:117]
	v_mfma_f32_16x16x32_bf16 v[102:105], v[152:155], v[218:221], v[102:105]
	v_mfma_f32_16x16x32_bf16 v[98:101], v[196:199], v[218:221], v[98:101]
	v_mfma_f32_16x16x32_bf16 v[86:89], v[152:155], v[226:229], v[86:89]
	v_mfma_f32_16x16x32_bf16 v[82:85], v[196:199], v[226:229], v[82:85]
	v_mfma_f32_16x16x32_bf16 v[70:73], v[152:155], v[234:237], v[70:73]
	v_mfma_f32_16x16x32_bf16 v[66:69], v[196:199], v[234:237], v[66:69]
	s_barrier
; #define PG8_STAGE(bufoff, gbase, voff) do { _Pragma("unroll") for (int _i = 0; _i < 2; ++_i) \
;         __builtin_amdgcn_global_load_lds((const unsigned*)((const char*)(gbase) + (voff)[_i]), (PG8_LAS unsigned*)(lds + (bufoff) + ldsw + _i * 8192), 16, 0, 0); } while (0)
; #define PG8_LDA(dst, b, h) do { _Pragma("unroll") for (int m = 0; m < 4; ++m) _Pragma("unroll") for (int k = 0; k < 2; ++k) dst[m][k] = *(const PG8_LAS bf16x8*)(lds + PG8_SA(b, h) + aoff + m * 2048 + k * 1024); } while (0)
; #define PG8_MMA(ai, bj, At, Bt) do { __builtin_amdgcn_s_setprio(1); _Pragma("unroll") for (int m = 0; m < 4; ++m) _Pragma("unroll") for (int n = 0; n < 2; ++n) _Pragma("unroll") for (int k = 0; k < 2; ++k) \
;         acc[ai][bj][m][n] = __builtin_amdgcn_mfma_f32_16x16x32_bf16(Bt[n][k], At[m][k], acc[ai][bj][m][n], 0, 0, 0); __builtin_amdgcn_s_setprio(0); } while (0)
; #define PG8_WAIT_V(n) asm volatile("s_waitcnt vmcnt(" #n ")" ::: "memory")
; #define PG8_WAIT_L(n) asm volatile("s_waitcnt lgkmcnt(" #n ")" ::: "memory")
; #define PG8_BAR __builtin_amdgcn_s_barrier()
; #define PG8_SCHED __builtin_amdgcn_sched_barrier(0)
; template <class Epi, class Sched, bool ALIGN_EPI = false>
; __device__ __forceinline__ void gemm_phase(PG8_LAS unsigned char* lds, const Gemm g, const Sched& S, const Epi& E) {
;     ...
;             PG8_LDA(At, 1, 1); PG8_STAGE(PG8_SB(1, 0), b3, voffB); PG8_STAGE(PG8_SB(1, 1), b3 + hstep, voffB); PG8_STAGE(PG8_SA(1, 0), a3, w0);
;             PG8_WAIT_V(8); PG8_WAIT_L(0); PG8_BAR; PG8_MMA(1, 0, At, B0); PG8_MMA(1, 1, At, B1); PG8_BAR; PG8_SCHED;
;             if constexpr (Epi::KSCALE) { if (((t + 2) & 7) == 0 && t + 2 < nt) { E.kscale(acc, pf, ((t + 2) >> 3) - 1, wr, fr); PG8_SCHED; } }
;         }
	s_add_i32 s54, s81, s57
	v_lshl_add_u64 v[160:161], v[160:161], 0, s[20:21]
	s_mov_b32 m0, s54
	ds_read_b128 v[204:207], v195 offset:49152
	ds_read_b128 v[210:213], v195 offset:50176
	ds_read_b128 v[214:217], v195 offset:51200
	ds_read_b128 v[218:221], v195 offset:52224
	ds_read_b128 v[222:225], v195 offset:53248
	ds_read_b128 v[226:229], v195 offset:54272
	ds_read_b128 v[230:233], v195 offset:55296
	ds_read_b128 v[234:237], v195 offset:56320
	global_load_lds_dwordx4 v[160:161], off
	s_add_i32 m0, s54, 0x2000
	s_add_u32 s52, s52, 0x80080
	v_lshl_add_u64 v[160:161], v[200:201], 0, s[20:21]
	s_addc_u32 s53, s53, 0
	s_add_i32 s54, s82, s57
	global_load_lds_dwordx4 v[160:161], off
	v_lshl_add_u64 v[160:161], s[52:53], 0, v[164:165]
	s_mov_b32 m0, s54
	s_nop 0
	global_load_lds_dwordx4 v[160:161], off
	v_lshl_add_u64 v[160:161], s[52:53], 0, v[168:169]
	s_add_i32 m0, s54, 0x2000
	s_nop 0
	global_load_lds_dwordx4 v[160:161], off
	v_lshl_add_u64 v[160:161], v[238:239], 0, s[20:21]
	s_mov_b32 m0, s65
	s_nop 0
	global_load_lds_dwordx4 v[160:161], off
	v_lshl_add_u64 v[160:161], v[240:241], 0, s[20:21]
	s_mov_b32 m0, s66
	s_nop 0
	global_load_lds_dwordx4 v[160:161], off
	s_waitcnt vmcnt(8)
	s_waitcnt lgkmcnt(0)
	v_mfma_f32_16x16x32_bf16 v[54:57], v[132:135], v[204:207], v[54:57]
	s_barrier
	v_mfma_f32_16x16x32_bf16 v[50:53], v[140:143], v[204:207], v[50:53]
	v_mfma_f32_16x16x32_bf16 v[38:41], v[132:135], v[214:217], v[38:41]
	v_mfma_f32_16x16x32_bf16 v[34:37], v[140:143], v[214:217], v[34:37]
	v_mfma_f32_16x16x32_bf16 v[22:25], v[132:135], v[222:225], v[22:25]
	v_mfma_f32_16x16x32_bf16 v[18:21], v[140:143], v[222:225], v[18:21]
	v_mfma_f32_16x16x32_bf16 v[6:9], v[132:135], v[230:233], v[6:9]
	v_mfma_f32_16x16x32_bf16 v[2:5], v[140:143], v[230:233], v[2:5]
	v_mfma_f32_16x16x32_bf16 v[54:57], v[136:139], v[210:213], v[54:57]
	v_mfma_f32_16x16x32_bf16 v[50:53], v[144:147], v[210:213], v[50:53]
	v_mfma_f32_16x16x32_bf16 v[38:41], v[136:139], v[218:221], v[38:41]
	v_mfma_f32_16x16x32_bf16 v[34:37], v[144:147], v[218:221], v[34:37]
	v_mfma_f32_16x16x32_bf16 v[22:25], v[136:139], v[226:229], v[22:25]
	v_mfma_f32_16x16x32_bf16 v[18:21], v[144:147], v[226:229], v[18:21]
	v_mfma_f32_16x16x32_bf16 v[6:9], v[136:139], v[234:237], v[6:9]
	v_mfma_f32_16x16x32_bf16 v[2:5], v[144:147], v[234:237], v[2:5]
	v_mfma_f32_16x16x32_bf16 v[58:61], v[148:151], v[204:207], v[58:61]
	v_mfma_f32_16x16x32_bf16 v[62:65], v[156:159], v[204:207], v[62:65]
	v_mfma_f32_16x16x32_bf16 v[42:45], v[148:151], v[214:217], v[42:45]
	v_mfma_f32_16x16x32_bf16 v[46:49], v[156:159], v[214:217], v[46:49]
	v_mfma_f32_16x16x32_bf16 v[26:29], v[148:151], v[222:225], v[26:29]
	v_mfma_f32_16x16x32_bf16 v[30:33], v[156:159], v[222:225], v[30:33]
	v_mfma_f32_16x16x32_bf16 v[10:13], v[148:151], v[230:233], v[10:13]
	v_mfma_f32_16x16x32_bf16 v[14:17], v[156:159], v[230:233], v[14:17]
	v_mfma_f32_16x16x32_bf16 v[58:61], v[152:155], v[210:213], v[58:61]
	v_mfma_f32_16x16x32_bf16 v[62:65], v[196:199], v[210:213], v[62:65]
	v_mfma_f32_16x16x32_bf16 v[42:45], v[152:155], v[218:221], v[42:45]
	v_mfma_f32_16x16x32_bf16 v[46:49], v[196:199], v[218:221], v[46:49]
	v_mfma_f32_16x16x32_bf16 v[26:29], v[152:155], v[226:229], v[26:29]
	v_mfma_f32_16x16x32_bf16 v[30:33], v[196:199], v[226:229], v[30:33]
	v_mfma_f32_16x16x32_bf16 v[10:13], v[152:155], v[234:237], v[10:13]
	v_mfma_f32_16x16x32_bf16 v[14:17], v[196:199], v[234:237], v[14:17]
	s_barrier
	s_add_i32 s80, s80, 2
	s_add_u32 s50, s50, 0x100
	s_addc_u32 s51, s51, 0
	s_add_u32 s78, s78, 0x100
	s_addc_u32 s79, s79, 0
	s_cmp_gt_u32 s80, 29
	s_cbranch_scc0 .LBB0_247
	s_and_b64 vcc, exec, s[22:23]
	s_cbranch_vccz .LBB0_250
	s_barrier

; #define PG8_STAGE(bufoff, gbase, voff) do { _Pragma("unroll") for (int _i = 0; _i < 2; ++_i) \
;         __builtin_amdgcn_global_load_lds((const unsigned*)((const char*)(gbase) + (voff)[_i]), (PG8_LAS unsigned*)(lds + (bufoff) + ldsw + _i * 8192), 16, 0, 0); } while (0)
; #define PG8_LDA(dst, b, h) do { _Pragma("unroll") for (int m = 0; m < 4; ++m) _Pragma("unroll") for (int k = 0; k < 2; ++k) dst[m][k] = *(const PG8_LAS bf16x8*)(lds + PG8_SA(b, h) + aoff + m * 2048 + k * 1024); } while (0)
; #define PG8_LDB(dst, b, h) do { _Pragma("unroll") for (int n = 0; n < 2; ++n) _Pragma("unroll") for (int k = 0; k < 2; ++k) dst[n][k] = *(const PG8_LAS bf16x8*)(lds + PG8_SB(b, h) + boff + n * 2048 + k * 1024); } while (0)
; #define PG8_MMA(ai, bj, At, Bt) do { __builtin_amdgcn_s_setprio(1); _Pragma("unroll") for (int m = 0; m < 4; ++m) _Pragma("unroll") for (int n = 0; n < 2; ++n) _Pragma("unroll") for (int k = 0; k < 2; ++k) \
;         acc[ai][bj][m][n] = __builtin_amdgcn_mfma_f32_16x16x32_bf16(Bt[n][k], At[m][k], acc[ai][bj][m][n], 0, 0, 0); __builtin_amdgcn_s_setprio(0); } while (0)
; #define PG8_BAR __builtin_amdgcn_s_barrier()
; template <class Epi, class Sched, bool ALIGN_EPI = false>
; __device__ __forceinline__ void gemm_phase(PG8_LAS unsigned char* lds, const Gemm g, const Sched& S, const Epi& E) {
;     ...
;             const bool last = (t == nt - 2);
;             const char* a1 = cA + (size_t)(t + 1) * kstep;
;             const char* a2 = last ? nA : cA + (size_t)(t + 2) * kstep; const char* b2 = last ? nB : cB + (size_t)(t + 2) * kstep;
;             const char* a3 = a2 + kstep; const char* b3 = b2 + kstep;
;             unsigned w0[2], w1[2];
; #pragma unroll
;             for (int i = 0; i < 2; ++i) { w0[i] = (Sched::GATHER && last) ? vn0[i] : vc0[i]; w1[i] = (Sched::GATHER && last) ? vn1[i] : vc1[i]; }
;             if (last && has_next) S.a_ready(nxt);
;             PG8_LDB(B0, 0, 0); PG8_LDB(B1, 0, 1); PG8_SCHED; PG8_LDA(At, 0, 0); PG8_STAGE(PG8_SA(1, 1), a1 + hstepA, vc1);
;             PG8_WAIT_V(8); PG8_WAIT_L(0); PG8_BAR; PG8_MMA(0, 0, At, B0); PG8_MMA(0, 1, At, B1); PG8_BAR; PG8_SCHED;
;             PG8_LDA(At, 0, 1); PG8_STAGE(PG8_SB(0, 0), b2, voffB); PG8_STAGE(PG8_SB(0, 1), b2 + hstep, voffB); PG8_STAGE(PG8_SA(0, 0), a2, w0);
;             PG8_WAIT_V(8); PG8_WAIT_L(0); PG8_BAR; PG8_MMA(1, 0, At, B0); PG8_MMA(1, 1, At, B1); PG8_BAR; PG8_SCHED;
.LBB0_504:
	v_add_u32_e32 v3, s74, v178
	s_add_u32 s54, s50, s52
	ds_read_b128 v[138:141], v3
	ds_read_b128 v[162:165], v3 offset:1024
	ds_read_b128 v[166:169], v3 offset:2048
	ds_read_b128 v[170:173], v3 offset:3072
	v_add_u32_e32 v3, s75, v178
	s_addc_u32 s55, s51, s53
	ds_read_b128 v[186:189], v3
	s_waitcnt lgkmcnt(0)
	ds_read_b128 v[190:193], v3 offset:1024
	ds_read_b128 v[194:197], v3 offset:2048
	ds_read_b128 v[198:201], v3 offset:3072
	s_add_u32 s54, s54, 0x100
	s_addc_u32 s55, s55, 0
	s_add_u32 s82, s79, s52
	s_addc_u32 s83, s80, s53
	s_cmpk_eq_i32 s52, 0xf00
	s_cselect_b32 s57, s47, s55
	s_cselect_b32 s56, s49, s54
	s_cselect_b32 s55, s45, s83
	s_cselect_b32 s54, s78, s82
	v_lshl_add_u64 v[142:143], v[132:133], 0, s[52:53]
	s_add_i32 m0, s62, 0xc000
	ds_read_b128 v[202:205], v184
	ds_read_b128 v[206:209], v184 offset:1024
	ds_read_b128 v[210:213], v184 offset:2048
	ds_read_b128 v[214:217], v184 offset:3072
	ds_read_b128 v[218:221], v184 offset:4096
	ds_read_b128 v[222:225], v184 offset:5120
	ds_read_b128 v[226:229], v184 offset:6144
	ds_read_b128 v[230:233], v184 offset:7168
	global_load_lds_dwordx4 v[142:143], off
	v_lshl_add_u64 v[142:143], v[134:135], 0, s[52:53]
	s_add_i32 m0, s62, 0xe000
	s_nop 0
	global_load_lds_dwordx4 v[142:143], off
	s_waitcnt vmcnt(8)
	s_waitcnt lgkmcnt(0)
	v_mfma_f32_16x16x32_bf16 v[128:131], v[138:141], v[202:205], v[128:131]
	s_barrier
	v_mfma_f32_16x16x32_bf16 v[124:127], v[166:169], v[202:205], v[124:127]
	v_mfma_f32_16x16x32_bf16 v[120:123], v[138:141], v[210:213], v[120:123]
	v_mfma_f32_16x16x32_bf16 v[112:115], v[166:169], v[210:213], v[112:115]
	v_mfma_f32_16x16x32_bf16 v[96:99], v[138:141], v[218:221], v[96:99]
	v_mfma_f32_16x16x32_bf16 v[92:95], v[166:169], v[218:221], v[92:95]
	v_mfma_f32_16x16x32_bf16 v[80:83], v[138:141], v[226:229], v[80:83]
	v_mfma_f32_16x16x32_bf16 v[76:79], v[166:169], v[226:229], v[76:79]
	v_mfma_f32_16x16x32_bf16 v[128:131], v[162:165], v[206:209], v[128:131]
	v_mfma_f32_16x16x32_bf16 v[124:127], v[170:173], v[206:209], v[124:127]
	v_mfma_f32_16x16x32_bf16 v[120:123], v[162:165], v[214:217], v[120:123]
	v_mfma_f32_16x16x32_bf16 v[112:115], v[170:173], v[214:217], v[112:115]
	v_mfma_f32_16x16x32_bf16 v[96:99], v[162:165], v[222:225], v[96:99]
	v_mfma_f32_16x16x32_bf16 v[92:95], v[170:173], v[222:225], v[92:95]
	v_mfma_f32_16x16x32_bf16 v[80:83], v[162:165], v[230:233], v[80:83]
	v_mfma_f32_16x16x32_bf16 v[76:79], v[170:173], v[230:233], v[76:79]
	v_mfma_f32_16x16x32_bf16 v[116:119], v[186:189], v[202:205], v[116:119]
	v_mfma_f32_16x16x32_bf16 v[108:111], v[194:197], v[202:205], v[108:111]
	v_mfma_f32_16x16x32_bf16 v[104:107], v[186:189], v[210:213], v[104:107]
	v_mfma_f32_16x16x32_bf16 v[100:103], v[194:197], v[210:213], v[100:103]
	v_mfma_f32_16x16x32_bf16 v[88:91], v[186:189], v[218:221], v[88:91]
	v_mfma_f32_16x16x32_bf16 v[84:87], v[194:197], v[218:221], v[84:87]
	v_mfma_f32_16x16x32_bf16 v[72:75], v[186:189], v[226:229], v[72:75]
	v_mfma_f32_16x16x32_bf16 v[68:71], v[194:197], v[226:229], v[68:71]
	v_mfma_f32_16x16x32_bf16 v[116:119], v[190:193], v[206:209], v[116:119]
	v_mfma_f32_16x16x32_bf16 v[108:111], v[198:201], v[206:209], v[108:111]
	v_mfma_f32_16x16x32_bf16 v[104:107], v[190:193], v[214:217], v[104:107]
	v_mfma_f32_16x16x32_bf16 v[100:103], v[198:201], v[214:217], v[100:103]
	v_mfma_f32_16x16x32_bf16 v[88:91], v[190:193], v[222:225], v[88:91]
	v_mfma_f32_16x16x32_bf16 v[84:87], v[198:201], v[222:225], v[84:87]
	v_mfma_f32_16x16x32_bf16 v[72:75], v[190:193], v[230:233], v[72:75]
	v_mfma_f32_16x16x32_bf16 v[68:71], v[198:201], v[230:233], v[68:71]
	s_barrier
	s_add_i32 s82, s74, s61
	v_lshl_add_u64 v[142:143], s[54:55], 0, v[146:147]
	s_mov_b32 m0, s82
	ds_read_b128 v[202:205], v184 offset:16384
	ds_read_b128 v[206:209], v184 offset:17408
	ds_read_b128 v[210:213], v184 offset:18432
	ds_read_b128 v[214:217], v184 offset:19456
	ds_read_b128 v[218:221], v184 offset:20480
	ds_read_b128 v[222:225], v184 offset:21504
	ds_read_b128 v[226:229], v184 offset:22528
	ds_read_b128 v[230:233], v184 offset:23552
	global_load_lds_dwordx4 v[142:143], off
	s_add_i32 m0, s82, 0x2000
	s_add_u32 s82, s54, 0x80000
	v_lshl_add_u64 v[174:175], s[54:55], 0, v[150:151]
	s_addc_u32 s83, s55, 0
	s_add_i32 s84, s75, s61
	global_load_lds_dwordx4 v[174:175], off
	v_lshl_add_u64 v[234:235], s[82:83], 0, v[146:147]
	s_mov_b32 m0, s84
	v_lshl_add_u64 v[236:237], s[56:57], 0, v[148:149]
	global_load_lds_dwordx4 v[234:235], off
	v_lshl_add_u64 v[234:235], s[82:83], 0, v[150:151]
	s_add_i32 m0, s84, 0x2000
	s_nop 0
	global_load_lds_dwordx4 v[234:235], off
	v_lshl_add_u64 v[234:235], s[56:57], 0, v[144:145]
	s_mov_b32 m0, s62
	s_nop 0
	global_load_lds_dwordx4 v[234:235], off
	s_mov_b32 m0, s63
	s_nop 0
	global_load_lds_dwordx4 v[236:237], off
	s_waitcnt vmcnt(8)
	s_waitcnt lgkmcnt(0)
	v_mfma_f32_16x16x32_bf16 v[64:67], v[138:141], v[202:205], v[64:67]
	s_barrier
; #define PG8_STAGE(bufoff, gbase, voff) do { _Pragma("unroll") for (int _i = 0; _i < 2; ++_i) \
;         __builtin_amdgcn_global_load_lds((const unsigned*)((const char*)(gbase) + (voff)[_i]), (PG8_LAS unsigned*)(lds + (bufoff) + ldsw + _i * 8192), 16, 0, 0); } while (0)
; #define PG8_LDA(dst, b, h) do { _Pragma("unroll") for (int m = 0; m < 4; ++m) _Pragma("unroll") for (int k = 0; k < 2; ++k) dst[m][k] = *(const PG8_LAS bf16x8*)(lds + PG8_SA(b, h) + aoff + m * 2048 + k * 1024); } while (0)
; #define PG8_LDB(dst, b, h) do { _Pragma("unroll") for (int n = 0; n < 2; ++n) _Pragma("unroll") for (int k = 0; k < 2; ++k) dst[n][k] = *(const PG8_LAS bf16x8*)(lds + PG8_SB(b, h) + boff + n * 2048 + k * 1024); } while (0)
; #define PG8_MMA(ai, bj, At, Bt) do { __builtin_amdgcn_s_setprio(1); _Pragma("unroll") for (int m = 0; m < 4; ++m) _Pragma("unroll") for (int n = 0; n < 2; ++n) _Pragma("unroll") for (int k = 0; k < 2; ++k) \
;         acc[ai][bj][m][n] = __builtin_amdgcn_mfma_f32_16x16x32_bf16(Bt[n][k], At[m][k], acc[ai][bj][m][n], 0, 0, 0); __builtin_amdgcn_s_setprio(0); } while (0)
; #define PG8_WAIT_V(n) asm volatile("s_waitcnt vmcnt(" #n ")" ::: "memory")
; #define PG8_WAIT_L(n) asm volatile("s_waitcnt lgkmcnt(" #n ")" ::: "memory")
; #define PG8_BAR __builtin_amdgcn_s_barrier()
; #define PG8_SCHED __builtin_amdgcn_sched_barrier(0)
; template <class Epi, class Sched, bool ALIGN_EPI = false>
; __device__ __forceinline__ void gemm_phase(PG8_LAS unsigned char* lds, const Gemm g, const Sched& S, const Epi& E) {
;     ...
;             PG8_WAIT_V(8); PG8_WAIT_L(0); PG8_BAR; PG8_MMA(1, 0, At, B0); PG8_MMA(1, 1, At, B1); PG8_BAR; PG8_SCHED;
;             PG8_LDB(B0, 1, 0); PG8_LDB(B1, 1, 1); PG8_SCHED; PG8_LDA(At, 1, 0); PG8_STAGE(PG8_SA(0, 1), a2 + hstepA, w1);
;             PG8_WAIT_V(8); PG8_WAIT_L(0); PG8_BAR; PG8_MMA(0, 0, At, B0); PG8_MMA(0, 1, At, B1); PG8_BAR; PG8_SCHED;
	v_mfma_f32_16x16x32_bf16 v[60:63], v[166:169], v[202:205], v[60:63]
	v_mfma_f32_16x16x32_bf16 v[48:51], v[138:141], v[210:213], v[48:51]
	v_mfma_f32_16x16x32_bf16 v[44:47], v[166:169], v[210:213], v[44:47]
	v_mfma_f32_16x16x32_bf16 v[32:35], v[138:141], v[218:221], v[32:35]
	v_mfma_f32_16x16x32_bf16 v[28:31], v[166:169], v[218:221], v[28:31]
	v_mfma_f32_16x16x32_bf16 v[16:19], v[138:141], v[226:229], v[16:19]
	v_mfma_f32_16x16x32_bf16 v[12:15], v[166:169], v[226:229], v[12:15]
	v_mfma_f32_16x16x32_bf16 v[64:67], v[162:165], v[206:209], v[64:67]
	v_mfma_f32_16x16x32_bf16 v[60:63], v[170:173], v[206:209], v[60:63]
	v_mfma_f32_16x16x32_bf16 v[48:51], v[162:165], v[214:217], v[48:51]
	v_mfma_f32_16x16x32_bf16 v[44:47], v[170:173], v[214:217], v[44:47]
	v_mfma_f32_16x16x32_bf16 v[32:35], v[162:165], v[222:225], v[32:35]
	v_mfma_f32_16x16x32_bf16 v[28:31], v[170:173], v[222:225], v[28:31]
	v_mfma_f32_16x16x32_bf16 v[16:19], v[162:165], v[230:233], v[16:19]
	v_mfma_f32_16x16x32_bf16 v[12:15], v[170:173], v[230:233], v[12:15]
	v_mfma_f32_16x16x32_bf16 v[56:59], v[186:189], v[202:205], v[56:59]
	v_mfma_f32_16x16x32_bf16 v[52:55], v[194:197], v[202:205], v[52:55]
	v_mfma_f32_16x16x32_bf16 v[40:43], v[186:189], v[210:213], v[40:43]
	v_mfma_f32_16x16x32_bf16 v[36:39], v[194:197], v[210:213], v[36:39]
	v_mfma_f32_16x16x32_bf16 v[24:27], v[186:189], v[218:221], v[24:27]
	v_mfma_f32_16x16x32_bf16 v[20:23], v[194:197], v[218:221], v[20:23]
	v_mfma_f32_16x16x32_bf16 v[8:11], v[186:189], v[226:229], v[8:11]
	v_mfma_f32_16x16x32_bf16 v[4:7], v[194:197], v[226:229], v[4:7]
	v_mfma_f32_16x16x32_bf16 v[56:59], v[190:193], v[206:209], v[56:59]
	v_mfma_f32_16x16x32_bf16 v[52:55], v[198:201], v[206:209], v[52:55]
	v_mfma_f32_16x16x32_bf16 v[40:43], v[190:193], v[214:217], v[40:43]
	v_mfma_f32_16x16x32_bf16 v[36:39], v[198:201], v[214:217], v[36:39]
	v_mfma_f32_16x16x32_bf16 v[24:27], v[190:193], v[222:225], v[24:27]
	v_mfma_f32_16x16x32_bf16 v[20:23], v[198:201], v[222:225], v[20:23]
	v_mfma_f32_16x16x32_bf16 v[8:11], v[190:193], v[230:233], v[8:11]
	v_mfma_f32_16x16x32_bf16 v[4:7], v[198:201], v[230:233], v[4:7]
	s_barrier
	s_add_i32 s82, 0, 0x18000
	v_add_u32_e32 v3, s82, v178
	s_add_i32 s83, 0, 0x1c000
	ds_read_b128 v[138:141], v3
	ds_read_b128 v[162:165], v3 offset:1024
	ds_read_b128 v[166:169], v3 offset:2048
	ds_read_b128 v[170:173], v3 offset:3072
	v_add_u32_e32 v3, s83, v178
	ds_read_b128 v[186:189], v3
	ds_read_b128 v[190:193], v3 offset:1024
	ds_read_b128 v[194:197], v3 offset:2048
	ds_read_b128 v[198:201], v3 offset:3072
	s_add_u32 s56, s56, 0x80000
	s_addc_u32 s57, s57, 0
	s_mov_b32 m0, s64
	v_lshl_add_u64 v[238:239], s[56:57], 0, v[144:145]
	ds_read_b128 v[202:205], v184 offset:32768
	ds_read_b128 v[206:209], v184 offset:33792
	ds_read_b128 v[210:213], v184 offset:34816
	ds_read_b128 v[214:217], v184 offset:35840
	ds_read_b128 v[218:221], v184 offset:36864
	ds_read_b128 v[222:225], v184 offset:37888
	ds_read_b128 v[226:229], v184 offset:38912
	ds_read_b128 v[230:233], v184 offset:39936
	global_load_lds_dwordx4 v[238:239], off
	v_lshl_add_u64 v[238:239], s[56:57], 0, v[148:149]
	s_mov_b32 m0, s65
	s_nop 0
	global_load_lds_dwordx4 v[238:239], off
	s_waitcnt vmcnt(8)
	s_waitcnt lgkmcnt(0)
	v_mfma_f32_16x16x32_bf16 v[128:131], v[138:141], v[202:205], v[128:131]
	s_barrier
	v_mfma_f32_16x16x32_bf16 v[124:127], v[166:169], v[202:205], v[124:127]
	v_mfma_f32_16x16x32_bf16 v[120:123], v[138:141], v[210:213], v[120:123]
	v_mfma_f32_16x16x32_bf16 v[112:115], v[166:169], v[210:213], v[112:115]
	v_mfma_f32_16x16x32_bf16 v[96:99], v[138:141], v[218:221], v[96:99]
	v_mfma_f32_16x16x32_bf16 v[92:95], v[166:169], v[218:221], v[92:95]
	v_mfma_f32_16x16x32_bf16 v[80:83], v[138:141], v[226:229], v[80:83]
	v_mfma_f32_16x16x32_bf16 v[76:79], v[166:169], v[226:229], v[76:79]
	v_mfma_f32_16x16x32_bf16 v[128:131], v[162:165], v[206:209], v[128:131]
	v_mfma_f32_16x16x32_bf16 v[124:127], v[170:173], v[206:209], v[124:127]
	v_mfma_f32_16x16x32_bf16 v[120:123], v[162:165], v[214:217], v[120:123]
	v_mfma_f32_16x16x32_bf16 v[112:115], v[170:173], v[214:217], v[112:115]
	v_mfma_f32_16x16x32_bf16 v[96:99], v[162:165], v[222:225], v[96:99]
	v_mfma_f32_16x16x32_bf16 v[92:95], v[170:173], v[222:225], v[92:95]
	v_mfma_f32_16x16x32_bf16 v[80:83], v[162:165], v[230:233], v[80:83]
	v_mfma_f32_16x16x32_bf16 v[76:79], v[170:173], v[230:233], v[76:79]
	v_mfma_f32_16x16x32_bf16 v[116:119], v[186:189], v[202:205], v[116:119]
	v_mfma_f32_16x16x32_bf16 v[108:111], v[194:197], v[202:205], v[108:111]
	v_mfma_f32_16x16x32_bf16 v[104:107], v[186:189], v[210:213], v[104:107]
	v_mfma_f32_16x16x32_bf16 v[100:103], v[194:197], v[210:213], v[100:103]
	v_mfma_f32_16x16x32_bf16 v[88:91], v[186:189], v[218:221], v[88:91]
	v_mfma_f32_16x16x32_bf16 v[84:87], v[194:197], v[218:221], v[84:87]
	v_mfma_f32_16x16x32_bf16 v[72:75], v[186:189], v[226:229], v[72:75]
	v_mfma_f32_16x16x32_bf16 v[68:71], v[194:197], v[226:229], v[68:71]
	v_mfma_f32_16x16x32_bf16 v[116:119], v[190:193], v[206:209], v[116:119]
	v_mfma_f32_16x16x32_bf16 v[108:111], v[198:201], v[206:209], v[108:111]
	v_mfma_f32_16x16x32_bf16 v[104:107], v[190:193], v[214:217], v[104:107]
	v_mfma_f32_16x16x32_bf16 v[100:103], v[198:201], v[214:217], v[100:103]
	v_mfma_f32_16x16x32_bf16 v[88:91], v[190:193], v[222:225], v[88:91]
	v_mfma_f32_16x16x32_bf16 v[84:87], v[198:201], v[222:225], v[84:87]
	v_mfma_f32_16x16x32_bf16 v[72:75], v[190:193], v[230:233], v[72:75]
	v_mfma_f32_16x16x32_bf16 v[68:71], v[198:201], v[230:233], v[68:71]
	s_barrier
; #define PG8_STAGE(bufoff, gbase, voff) do { _Pragma("unroll") for (int _i = 0; _i < 2; ++_i) \
;         __builtin_amdgcn_global_load_lds((const unsigned*)((const char*)(gbase) + (voff)[_i]), (PG8_LAS unsigned*)(lds + (bufoff) + ldsw + _i * 8192), 16, 0, 0); } while (0)
; #define PG8_LDA(dst, b, h) do { _Pragma("unroll") for (int m = 0; m < 4; ++m) _Pragma("unroll") for (int k = 0; k < 2; ++k) dst[m][k] = *(const PG8_LAS bf16x8*)(lds + PG8_SA(b, h) + aoff + m * 2048 + k * 1024); } while (0)
; #define PG8_MMA(ai, bj, At, Bt) do { __builtin_amdgcn_s_setprio(1); _Pragma("unroll") for (int m = 0; m < 4; ++m) _Pragma("unroll") for (int n = 0; n < 2; ++n) _Pragma("unroll") for (int k = 0; k < 2; ++k) \
;         acc[ai][bj][m][n] = __builtin_amdgcn_mfma_f32_16x16x32_bf16(Bt[n][k], At[m][k], acc[ai][bj][m][n], 0, 0, 0); __builtin_amdgcn_s_setprio(0); } while (0)
; #define PG8_WAIT_V(n) asm volatile("s_waitcnt vmcnt(" #n ")" ::: "memory")
; #define PG8_WAIT_L(n) asm volatile("s_waitcnt lgkmcnt(" #n ")" ::: "memory")
; #define PG8_BAR __builtin_amdgcn_s_barrier()
; #define PG8_SCHED __builtin_amdgcn_sched_barrier(0)
; template <class Epi, class Sched, bool ALIGN_EPI = false>
; __device__ __forceinline__ void gemm_phase(PG8_LAS unsigned char* lds, const Gemm g, const Sched& S, const Epi& E) {
;     ...
;             PG8_LDA(At, 1, 1); PG8_STAGE(PG8_SB(1, 0), b3, voffB); PG8_STAGE(PG8_SB(1, 1), b3 + hstep, voffB); PG8_STAGE(PG8_SA(1, 0), a3, w0);
;             PG8_WAIT_V(8); PG8_WAIT_L(0); PG8_BAR; PG8_MMA(1, 0, At, B0); PG8_MMA(1, 1, At, B1); PG8_BAR; PG8_SCHED;
;             if constexpr (Epi::KSCALE) { if (((t + 2) & 7) == 0 && t + 2 < nt) { E.kscale(acc, pf, ((t + 2) >> 3) - 1, wr, fr); PG8_SCHED; } }
;         }
	s_add_i32 s56, s82, s61
	v_lshl_add_u64 v[142:143], v[142:143], 0, s[18:19]
	s_mov_b32 m0, s56
	ds_read_b128 v[202:205], v184 offset:49152
	ds_read_b128 v[206:209], v184 offset:50176
	ds_read_b128 v[210:213], v184 offset:51200
	ds_read_b128 v[214:217], v184 offset:52224
	ds_read_b128 v[218:221], v184 offset:53248
	ds_read_b128 v[222:225], v184 offset:54272
	ds_read_b128 v[226:229], v184 offset:55296
	ds_read_b128 v[230:233], v184 offset:56320
	global_load_lds_dwordx4 v[142:143], off
	s_add_i32 m0, s56, 0x2000
	s_add_u32 s54, s54, 0x80080
	v_lshl_add_u64 v[142:143], v[174:175], 0, s[18:19]
	s_addc_u32 s55, s55, 0
	s_add_i32 s56, s83, s61
	global_load_lds_dwordx4 v[142:143], off
	v_lshl_add_u64 v[142:143], s[54:55], 0, v[146:147]
	s_mov_b32 m0, s56
	s_nop 0
	global_load_lds_dwordx4 v[142:143], off
	v_lshl_add_u64 v[142:143], s[54:55], 0, v[150:151]
	s_add_i32 m0, s56, 0x2000
	s_nop 0
	global_load_lds_dwordx4 v[142:143], off
	v_lshl_add_u64 v[142:143], v[234:235], 0, s[18:19]
	s_mov_b32 m0, s68
	s_nop 0
	global_load_lds_dwordx4 v[142:143], off
	v_lshl_add_u64 v[142:143], v[236:237], 0, s[18:19]
	s_mov_b32 m0, s69
	s_nop 0
	global_load_lds_dwordx4 v[142:143], off
	s_waitcnt vmcnt(8)
	s_waitcnt lgkmcnt(0)
	v_mfma_f32_16x16x32_bf16 v[64:67], v[138:141], v[202:205], v[64:67]
	s_barrier
	v_mfma_f32_16x16x32_bf16 v[60:63], v[166:169], v[202:205], v[60:63]
	v_mfma_f32_16x16x32_bf16 v[48:51], v[138:141], v[210:213], v[48:51]
	v_mfma_f32_16x16x32_bf16 v[44:47], v[166:169], v[210:213], v[44:47]
	v_mfma_f32_16x16x32_bf16 v[32:35], v[138:141], v[218:221], v[32:35]
	v_mfma_f32_16x16x32_bf16 v[28:31], v[166:169], v[218:221], v[28:31]
	v_mfma_f32_16x16x32_bf16 v[16:19], v[138:141], v[226:229], v[16:19]
	v_mfma_f32_16x16x32_bf16 v[12:15], v[166:169], v[226:229], v[12:15]
	v_mfma_f32_16x16x32_bf16 v[64:67], v[162:165], v[206:209], v[64:67]
	v_mfma_f32_16x16x32_bf16 v[60:63], v[170:173], v[206:209], v[60:63]
	v_mfma_f32_16x16x32_bf16 v[48:51], v[162:165], v[214:217], v[48:51]
	v_mfma_f32_16x16x32_bf16 v[44:47], v[170:173], v[214:217], v[44:47]
	v_mfma_f32_16x16x32_bf16 v[32:35], v[162:165], v[222:225], v[32:35]
	v_mfma_f32_16x16x32_bf16 v[28:31], v[170:173], v[222:225], v[28:31]
	v_mfma_f32_16x16x32_bf16 v[16:19], v[162:165], v[230:233], v[16:19]
	v_mfma_f32_16x16x32_bf16 v[12:15], v[170:173], v[230:233], v[12:15]
	v_mfma_f32_16x16x32_bf16 v[56:59], v[186:189], v[202:205], v[56:59]
	v_mfma_f32_16x16x32_bf16 v[52:55], v[194:197], v[202:205], v[52:55]
	v_mfma_f32_16x16x32_bf16 v[40:43], v[186:189], v[210:213], v[40:43]
	v_mfma_f32_16x16x32_bf16 v[36:39], v[194:197], v[210:213], v[36:39]
	v_mfma_f32_16x16x32_bf16 v[24:27], v[186:189], v[218:221], v[24:27]
	v_mfma_f32_16x16x32_bf16 v[20:23], v[194:197], v[218:221], v[20:23]
	v_mfma_f32_16x16x32_bf16 v[8:11], v[186:189], v[226:229], v[8:11]
	v_mfma_f32_16x16x32_bf16 v[4:7], v[194:197], v[226:229], v[4:7]
	v_mfma_f32_16x16x32_bf16 v[56:59], v[190:193], v[206:209], v[56:59]
	v_mfma_f32_16x16x32_bf16 v[52:55], v[198:201], v[206:209], v[52:55]
	v_mfma_f32_16x16x32_bf16 v[40:43], v[190:193], v[214:217], v[40:43]
	v_mfma_f32_16x16x32_bf16 v[36:39], v[198:201], v[214:217], v[36:39]
	v_mfma_f32_16x16x32_bf16 v[24:27], v[190:193], v[222:225], v[24:27]
	v_mfma_f32_16x16x32_bf16 v[20:23], v[198:201], v[222:225], v[20:23]
	v_mfma_f32_16x16x32_bf16 v[8:11], v[190:193], v[230:233], v[8:11]
	v_mfma_f32_16x16x32_bf16 v[4:7], v[198:201], v[230:233], v[4:7]
	s_barrier
	s_mov_b32 s82, s81
	s_add_i32 s81, s81, 2
	s_and_b32 s54, s81, 6
	s_cmp_eq_u32 s54, 0
	s_cselect_b64 s[56:57], -1, 0
	s_cmp_gt_u32 s82, 29
	s_cselect_b64 s[54:55], -1, 0
	s_cmp_lt_u32 s82, 30
	s_cselect_b64 s[82:83], -1, 0
	s_and_b64 s[56:57], s[56:57], s[82:83]
	s_andn2_b64 vcc, exec, s[56:57]
	s_cbranch_vccnz .LBB0_503
; #define PG8_SCHED __builtin_amdgcn_sched_barrier(0)
;     __device__ __forceinline__ void kscale(f32x4 (&acc)[2][2][4][2], const Pre& pf, int b, int wr, int fr) const {
; #pragma unroll
;         for (int ai = 0; ai < 2; ++ai)
; #pragma unroll
;             for (int m = 0; m < 4; ++m) { const float f = pf.tab[(ai * HALF + wr * 64 + m * 16 + fr) * 4 + b];
; #pragma unroll
;                 for (int bj = 0; bj < 2; ++bj)
; #pragma unroll
;                     for (int n = 0; n < 2; ++n) acc[ai][bj][m][n] = acc[ai][bj][m][n] * f; }
;     }
; template <class Epi, class Sched, bool ALIGN_EPI = false>
; __device__ __forceinline__ void gemm_phase(PG8_LAS unsigned char* lds, const Gemm g, const Sched& S, const Epi& E) {
;     ...
;             if constexpr (Epi::KSCALE) { if (((t + 2) & 7) == 0 && t + 2 < nt) { E.kscale(acc, pf, ((t + 2) >> 3) - 1, wr, fr); PG8_SCHED; } }
	s_lshr_b32 s56, s81, 1
	v_add_u32_e32 v3, s56, v137
	v_add_u32_e32 v136, -4, v3
	ds_read_b32 v136, v136
	ds_read_b32 v138, v3 offset:2812
	ds_read2_b32 v[140:141], v3 offset0:63 offset1:127
	v_add_u32_e32 v3, 0xfc, v3
	s_waitcnt lgkmcnt(0)
	v_pk_mul_f32 v[130:131], v[130:131], v[136:137] op_sel_hi:[1,0]
	v_pk_mul_f32 v[128:129], v[128:129], v[136:137] op_sel_hi:[1,0]
	v_pk_mul_f32 v[126:127], v[126:127], v[136:137] op_sel_hi:[1,0]
	v_pk_mul_f32 v[124:125], v[124:125], v[136:137] op_sel_hi:[1,0]
	v_pk_mul_f32 v[118:119], v[118:119], v[136:137] op_sel_hi:[1,0]
	v_pk_mul_f32 v[116:117], v[116:117], v[136:137] op_sel_hi:[1,0]
	v_pk_mul_f32 v[110:111], v[110:111], v[136:137] op_sel_hi:[1,0]
	v_pk_mul_f32 v[108:109], v[108:109], v[136:137] op_sel_hi:[1,0]
	v_pk_mul_f32 v[122:123], v[122:123], v[140:141] op_sel_hi:[1,0]
	v_pk_mul_f32 v[120:121], v[120:121], v[140:141] op_sel_hi:[1,0]
	v_pk_mul_f32 v[114:115], v[114:115], v[140:141] op_sel_hi:[1,0]
	v_pk_mul_f32 v[112:113], v[112:113], v[140:141] op_sel_hi:[1,0]
	v_pk_mul_f32 v[106:107], v[106:107], v[140:141] op_sel_hi:[1,0]
	v_pk_mul_f32 v[104:105], v[104:105], v[140:141] op_sel_hi:[1,0]
	v_pk_mul_f32 v[102:103], v[102:103], v[140:141] op_sel_hi:[1,0]
	v_pk_mul_f32 v[100:101], v[100:101], v[140:141] op_sel_hi:[1,0]
	v_mov_b32_e32 v136, v141
	ds_read2st64_b32 v[140:141], v3 offset0:2 offset1:7
	v_pk_mul_f32 v[98:99], v[98:99], v[136:137] op_sel_hi:[1,0]
	v_pk_mul_f32 v[96:97], v[96:97], v[136:137] op_sel_hi:[1,0]
	v_pk_mul_f32 v[94:95], v[94:95], v[136:137] op_sel_hi:[1,0]
	v_pk_mul_f32 v[92:93], v[92:93], v[136:137] op_sel_hi:[1,0]
	v_pk_mul_f32 v[90:91], v[90:91], v[136:137] op_sel_hi:[1,0]
	v_pk_mul_f32 v[88:89], v[88:89], v[136:137] op_sel_hi:[1,0]
	v_pk_mul_f32 v[86:87], v[86:87], v[136:137] op_sel_hi:[1,0]
	v_pk_mul_f32 v[84:85], v[84:85], v[136:137] op_sel_hi:[1,0]
	s_waitcnt lgkmcnt(0)
	v_pk_mul_f32 v[82:83], v[82:83], v[140:141] op_sel_hi:[1,0]
	v_pk_mul_f32 v[80:81], v[80:81], v[140:141] op_sel_hi:[1,0]
	v_pk_mul_f32 v[78:79], v[78:79], v[140:141] op_sel_hi:[1,0]
	v_pk_mul_f32 v[76:77], v[76:77], v[140:141] op_sel_hi:[1,0]
	v_pk_mul_f32 v[74:75], v[74:75], v[140:141] op_sel_hi:[1,0]
	v_pk_mul_f32 v[72:73], v[72:73], v[140:141] op_sel_hi:[1,0]
	v_pk_mul_f32 v[70:71], v[70:71], v[140:141] op_sel_hi:[1,0]
	v_pk_mul_f32 v[68:69], v[68:69], v[140:141] op_sel_hi:[1,0]
	v_mov_b32_e32 v136, v141
	ds_read2st64_b32 v[140:141], v3 offset0:8 offset1:9
	v_pk_mul_f32 v[66:67], v[66:67], v[136:137] op_sel_hi:[1,0]
	v_pk_mul_f32 v[64:65], v[64:65], v[136:137] op_sel_hi:[1,0]
	v_pk_mul_f32 v[62:63], v[62:63], v[136:137] op_sel_hi:[1,0]
	v_pk_mul_f32 v[60:61], v[60:61], v[136:137] op_sel_hi:[1,0]
	v_pk_mul_f32 v[58:59], v[58:59], v[136:137] op_sel_hi:[1,0]
	v_pk_mul_f32 v[56:57], v[56:57], v[136:137] op_sel_hi:[1,0]
	v_pk_mul_f32 v[54:55], v[54:55], v[136:137] op_sel_hi:[1,0]
	v_pk_mul_f32 v[52:53], v[52:53], v[136:137] op_sel_hi:[1,0]
	s_waitcnt lgkmcnt(0)
	v_mov_b32_e32 v136, v141
	v_pk_mul_f32 v[50:51], v[50:51], v[140:141] op_sel_hi:[1,0]
	v_pk_mul_f32 v[48:49], v[48:49], v[140:141] op_sel_hi:[1,0]
	v_pk_mul_f32 v[46:47], v[46:47], v[140:141] op_sel_hi:[1,0]
	v_pk_mul_f32 v[44:45], v[44:45], v[140:141] op_sel_hi:[1,0]
	v_pk_mul_f32 v[42:43], v[42:43], v[140:141] op_sel_hi:[1,0]
	v_pk_mul_f32 v[40:41], v[40:41], v[140:141] op_sel_hi:[1,0]
	v_pk_mul_f32 v[38:39], v[38:39], v[140:141] op_sel_hi:[1,0]
	v_pk_mul_f32 v[36:37], v[36:37], v[140:141] op_sel_hi:[1,0]
	v_pk_mul_f32 v[34:35], v[34:35], v[136:137] op_sel_hi:[1,0]
	v_pk_mul_f32 v[32:33], v[32:33], v[136:137] op_sel_hi:[1,0]
	v_pk_mul_f32 v[30:31], v[30:31], v[136:137] op_sel_hi:[1,0]
	v_pk_mul_f32 v[28:29], v[28:29], v[136:137] op_sel_hi:[1,0]
	v_pk_mul_f32 v[26:27], v[26:27], v[136:137] op_sel_hi:[1,0]
	v_pk_mul_f32 v[24:25], v[24:25], v[136:137] op_sel_hi:[1,0]
	v_pk_mul_f32 v[22:23], v[22:23], v[136:137] op_sel_hi:[1,0]
	v_pk_mul_f32 v[20:21], v[20:21], v[136:137] op_sel_hi:[1,0]
	v_pk_mul_f32 v[18:19], v[18:19], v[138:139] op_sel_hi:[1,0]
	v_pk_mul_f32 v[16:17], v[16:17], v[138:139] op_sel_hi:[1,0]
	v_pk_mul_f32 v[14:15], v[14:15], v[138:139] op_sel_hi:[1,0]
	v_pk_mul_f32 v[12:13], v[12:13], v[138:139] op_sel_hi:[1,0]
	v_pk_mul_f32 v[10:11], v[10:11], v[138:139] op_sel_hi:[1,0]
	v_pk_mul_f32 v[8:9], v[8:9], v[138:139] op_sel_hi:[1,0]
	v_pk_mul_f32 v[6:7], v[6:7], v[138:139] op_sel_hi:[1,0]
	v_pk_mul_f32 v[4:5], v[4:5], v[138:139] op_sel_hi:[1,0]
	s_branch .LBB0_503

; #define PG8_STAGE(bufoff, gbase, voff) do { _Pragma("unroll") for (int _i = 0; _i < 2; ++_i) \
;         __builtin_amdgcn_global_load_lds((const unsigned*)((const char*)(gbase) + (voff)[_i]), (PG8_LAS unsigned*)(lds + (bufoff) + ldsw + _i * 8192), 16, 0, 0); } while (0)
; #define PG8_LDA(dst, b, h) do { _Pragma("unroll") for (int m = 0; m < 4; ++m) _Pragma("unroll") for (int k = 0; k < 2; ++k) dst[m][k] = *(const PG8_LAS bf16x8*)(lds + PG8_SA(b, h) + aoff + m * 2048 + k * 1024); } while (0)
; #define PG8_LDB(dst, b, h) do { _Pragma("unroll") for (int n = 0; n < 2; ++n) _Pragma("unroll") for (int k = 0; k < 2; ++k) dst[n][k] = *(const PG8_LAS bf16x8*)(lds + PG8_SB(b, h) + boff + n * 2048 + k * 1024); } while (0)
; #define PG8_MMA(ai, bj, At, Bt) do { __builtin_amdgcn_s_setprio(1); _Pragma("unroll") for (int m = 0; m < 4; ++m) _Pragma("unroll") for (int n = 0; n < 2; ++n) _Pragma("unroll") for (int k = 0; k < 2; ++k) \
;         acc[ai][bj][m][n] = __builtin_amdgcn_mfma_f32_16x16x32_bf16(Bt[n][k], At[m][k], acc[ai][bj][m][n], 0, 0, 0); __builtin_amdgcn_s_setprio(0); } while (0)
; #define PG8_BAR __builtin_amdgcn_s_barrier()
; template <class Epi, class Sched, bool ALIGN_EPI = false>
; __device__ __forceinline__ void gemm_phase(PG8_LAS unsigned char* lds, const Gemm g, const Sched& S, const Epi& E) {
;     ...
;             const bool last = (t == nt - 2);
;             const char* a1 = cA + (size_t)(t + 1) * kstep;
;             const char* a2 = last ? nA : cA + (size_t)(t + 2) * kstep; const char* b2 = last ? nB : cB + (size_t)(t + 2) * kstep;
;             const char* a3 = a2 + kstep; const char* b3 = b2 + kstep;
;             unsigned w0[2], w1[2];
; #pragma unroll
;             for (int i = 0; i < 2; ++i) { w0[i] = (Sched::GATHER && last) ? vn0[i] : vc0[i]; w1[i] = (Sched::GATHER && last) ? vn1[i] : vc1[i]; }
;             if (last && has_next) S.a_ready(nxt);
;             PG8_LDB(B0, 0, 0); PG8_LDB(B1, 0, 1); PG8_SCHED; PG8_LDA(At, 0, 0); PG8_STAGE(PG8_SA(1, 1), a1 + hstepA, vc1);
;             PG8_WAIT_V(8); PG8_WAIT_L(0); PG8_BAR; PG8_MMA(0, 0, At, B0); PG8_MMA(0, 1, At, B1); PG8_BAR; PG8_SCHED;
;             PG8_LDA(At, 0, 1); PG8_STAGE(PG8_SB(0, 0), b2, voffB); PG8_STAGE(PG8_SB(0, 1), b2 + hstep, voffB); PG8_STAGE(PG8_SA(0, 0), a2, w0);
;             PG8_WAIT_V(8); PG8_WAIT_L(0); PG8_BAR; PG8_MMA(1, 0, At, B0); PG8_MMA(1, 1, At, B1); PG8_BAR; PG8_SCHED;
.LBB0_721:
	s_add_u32 s58, s36, s56
	v_add_u32_e32 v155, s82, v143
	s_addc_u32 s59, s37, s57
	ds_read_b128 v[164:167], v155
	ds_read_b128 v[168:171], v155 offset:1024
	ds_read_b128 v[172:175], v155 offset:2048
	ds_read_b128 v[176:179], v155 offset:3072
	v_add_u32_e32 v155, s83, v143
	s_add_u32 s60, s58, 0x3c800100
	ds_read_b128 v[180:183], v155
	ds_read_b128 v[184:187], v155 offset:1024
	ds_read_b128 v[188:191], v155 offset:2048
	ds_read_b128 v[192:195], v155 offset:3072
	s_addc_u32 s61, s59, 0
	s_add_u32 s91, s49, s56
	s_addc_u32 s92, s89, s57
	s_cmpk_eq_i32 s56, 0xf00
	s_cselect_b64 vcc, -1, 0
	s_and_b64 s[58:59], vcc, exec
	v_cndmask_b32_e32 v134, v151, v149, vcc
	s_cselect_b32 s61, s21, s61
	s_cselect_b32 s60, s20, s60
	v_cndmask_b32_e32 v153, v152, v157, vcc
	v_cndmask_b32_e32 v228, v150, v162, vcc
	v_cndmask_b32_e32 v155, v154, v163, vcc
	s_cselect_b32 s59, s53, s92
	s_cselect_b32 s58, s52, s91
	v_lshl_add_u64 v[230:231], v[160:161], 0, s[56:57]
	s_add_i32 m0, s55, 0xc000
	ds_read_b128 v[196:199], v147
	ds_read_b128 v[200:203], v147 offset:1024
	ds_read_b128 v[204:207], v147 offset:2048
	ds_read_b128 v[208:211], v147 offset:3072
	ds_read_b128 v[212:215], v147 offset:4096
	ds_read_b128 v[216:219], v147 offset:5120
	ds_read_b128 v[220:223], v147 offset:6144
	ds_read_b128 v[224:227], v147 offset:7168
	global_load_lds_dwordx4 v[230:231], off
	v_lshl_add_u64 v[230:231], v[158:159], 0, s[56:57]
	s_add_i32 m0, s55, 0xe000
	s_nop 0
	global_load_lds_dwordx4 v[230:231], off
	s_waitcnt vmcnt(8)
	s_waitcnt lgkmcnt(0)
	v_mfma_f32_16x16x32_bf16 v[126:129], v[164:167], v[196:199], v[126:129]
	s_barrier
	v_mfma_f32_16x16x32_bf16 v[122:125], v[172:175], v[196:199], v[122:125]
	v_mfma_f32_16x16x32_bf16 v[110:113], v[164:167], v[204:207], v[110:113]
	v_mfma_f32_16x16x32_bf16 v[106:109], v[172:175], v[204:207], v[106:109]
	v_mfma_f32_16x16x32_bf16 v[94:97], v[164:167], v[212:215], v[94:97]
	v_mfma_f32_16x16x32_bf16 v[90:93], v[172:175], v[212:215], v[90:93]
	v_mfma_f32_16x16x32_bf16 v[78:81], v[164:167], v[220:223], v[78:81]
	v_mfma_f32_16x16x32_bf16 v[74:77], v[172:175], v[220:223], v[74:77]
	v_mfma_f32_16x16x32_bf16 v[126:129], v[168:171], v[200:203], v[126:129]
	v_mfma_f32_16x16x32_bf16 v[122:125], v[176:179], v[200:203], v[122:125]
	v_mfma_f32_16x16x32_bf16 v[110:113], v[168:171], v[208:211], v[110:113]
	v_mfma_f32_16x16x32_bf16 v[106:109], v[176:179], v[208:211], v[106:109]
	v_mfma_f32_16x16x32_bf16 v[94:97], v[168:171], v[216:219], v[94:97]
	v_mfma_f32_16x16x32_bf16 v[90:93], v[176:179], v[216:219], v[90:93]
	v_mfma_f32_16x16x32_bf16 v[78:81], v[168:171], v[224:227], v[78:81]
	v_mfma_f32_16x16x32_bf16 v[74:77], v[176:179], v[224:227], v[74:77]
	v_mfma_f32_16x16x32_bf16 v[118:121], v[180:183], v[196:199], v[118:121]
	v_mfma_f32_16x16x32_bf16 v[114:117], v[188:191], v[196:199], v[114:117]
	v_mfma_f32_16x16x32_bf16 v[102:105], v[180:183], v[204:207], v[102:105]
	v_mfma_f32_16x16x32_bf16 v[98:101], v[188:191], v[204:207], v[98:101]
	v_mfma_f32_16x16x32_bf16 v[86:89], v[180:183], v[212:215], v[86:89]
	v_mfma_f32_16x16x32_bf16 v[82:85], v[188:191], v[212:215], v[82:85]
	v_mfma_f32_16x16x32_bf16 v[70:73], v[180:183], v[220:223], v[70:73]
	v_mfma_f32_16x16x32_bf16 v[66:69], v[188:191], v[220:223], v[66:69]
	v_mfma_f32_16x16x32_bf16 v[118:121], v[184:187], v[200:203], v[118:121]
	v_mfma_f32_16x16x32_bf16 v[114:117], v[192:195], v[200:203], v[114:117]
	v_mfma_f32_16x16x32_bf16 v[102:105], v[184:187], v[208:211], v[102:105]
	v_mfma_f32_16x16x32_bf16 v[98:101], v[192:195], v[208:211], v[98:101]
	v_mfma_f32_16x16x32_bf16 v[86:89], v[184:187], v[216:219], v[86:89]
	v_mfma_f32_16x16x32_bf16 v[82:85], v[192:195], v[216:219], v[82:85]
	v_mfma_f32_16x16x32_bf16 v[70:73], v[184:187], v[224:227], v[70:73]
	v_mfma_f32_16x16x32_bf16 v[66:69], v[192:195], v[224:227], v[66:69]
	s_barrier
	s_add_i32 s91, s82, s74
	v_lshl_add_u64 v[230:231], s[58:59], 0, v[130:131]
	s_mov_b32 m0, s91
	ds_read_b128 v[196:199], v147 offset:16384
	ds_read_b128 v[200:203], v147 offset:17408
	ds_read_b128 v[204:207], v147 offset:18432
	ds_read_b128 v[208:211], v147 offset:19456
	ds_read_b128 v[212:215], v147 offset:20480
	ds_read_b128 v[216:219], v147 offset:21504
	ds_read_b128 v[220:223], v147 offset:22528
	ds_read_b128 v[224:227], v147 offset:23552
	global_load_lds_dwordx4 v[230:231], off
	s_add_i32 m0, s91, 0x2000
	s_add_u32 s92, s58, 0x80000
	v_lshl_add_u64 v[232:233], s[58:59], 0, v[132:133]
	s_addc_u32 s93, s59, 0
	s_add_i32 s91, s83, s74
	global_load_lds_dwordx4 v[232:233], off
	v_lshl_add_u64 v[234:235], s[92:93], 0, v[130:131]
	s_mov_b32 m0, s91
	v_mov_b32_e32 v229, v135
	global_load_lds_dwordx4 v[234:235], off
	v_lshl_add_u64 v[234:235], s[92:93], 0, v[132:133]
	s_add_i32 m0, s91, 0x2000
	s_nop 0
	global_load_lds_dwordx4 v[234:235], off
	s_mov_b32 m0, s55
	v_lshl_add_u64 v[234:235], s[60:61], 0, v[134:135]
	global_load_lds_dwordx4 v134, s[60:61]
	s_mov_b32 m0, s75
	s_nop 0
	global_load_lds_dwordx4 v228, s[60:61]
	s_waitcnt vmcnt(8)
	s_waitcnt lgkmcnt(0)
	v_lshl_add_u64 v[228:229], s[60:61], 0, v[228:229]
	v_mfma_f32_16x16x32_bf16 v[62:65], v[164:167], v[196:199], v[62:65]
	s_barrier
; #define PG8_STAGE(bufoff, gbase, voff) do { _Pragma("unroll") for (int _i = 0; _i < 2; ++_i) \
;         __builtin_amdgcn_global_load_lds((const unsigned*)((const char*)(gbase) + (voff)[_i]), (PG8_LAS unsigned*)(lds + (bufoff) + ldsw + _i * 8192), 16, 0, 0); } while (0)
; #define PG8_LDA(dst, b, h) do { _Pragma("unroll") for (int m = 0; m < 4; ++m) _Pragma("unroll") for (int k = 0; k < 2; ++k) dst[m][k] = *(const PG8_LAS bf16x8*)(lds + PG8_SA(b, h) + aoff + m * 2048 + k * 1024); } while (0)
; #define PG8_LDB(dst, b, h) do { _Pragma("unroll") for (int n = 0; n < 2; ++n) _Pragma("unroll") for (int k = 0; k < 2; ++k) dst[n][k] = *(const PG8_LAS bf16x8*)(lds + PG8_SB(b, h) + boff + n * 2048 + k * 1024); } while (0)
; #define PG8_MMA(ai, bj, At, Bt) do { __builtin_amdgcn_s_setprio(1); _Pragma("unroll") for (int m = 0; m < 4; ++m) _Pragma("unroll") for (int n = 0; n < 2; ++n) _Pragma("unroll") for (int k = 0; k < 2; ++k) \
;         acc[ai][bj][m][n] = __builtin_amdgcn_mfma_f32_16x16x32_bf16(Bt[n][k], At[m][k], acc[ai][bj][m][n], 0, 0, 0); __builtin_amdgcn_s_setprio(0); } while (0)
; #define PG8_WAIT_V(n) asm volatile("s_waitcnt vmcnt(" #n ")" ::: "memory")
; #define PG8_WAIT_L(n) asm volatile("s_waitcnt lgkmcnt(" #n ")" ::: "memory")
; #define PG8_BAR __builtin_amdgcn_s_barrier()
; #define PG8_SCHED __builtin_amdgcn_sched_barrier(0)
; template <class Epi, class Sched, bool ALIGN_EPI = false>
; __device__ __forceinline__ void gemm_phase(PG8_LAS unsigned char* lds, const Gemm g, const Sched& S, const Epi& E) {
;     ...
;             PG8_WAIT_V(8); PG8_WAIT_L(0); PG8_BAR; PG8_MMA(1, 0, At, B0); PG8_MMA(1, 1, At, B1); PG8_BAR; PG8_SCHED;
;             PG8_LDB(B0, 1, 0); PG8_LDB(B1, 1, 1); PG8_SCHED; PG8_LDA(At, 1, 0); PG8_STAGE(PG8_SA(0, 1), a2 + hstepA, w1);
;             PG8_WAIT_V(8); PG8_WAIT_L(0); PG8_BAR; PG8_MMA(0, 0, At, B0); PG8_MMA(0, 1, At, B1); PG8_BAR; PG8_SCHED;
	v_mfma_f32_16x16x32_bf16 v[58:61], v[172:175], v[196:199], v[58:61]
	v_mfma_f32_16x16x32_bf16 v[50:53], v[164:167], v[204:207], v[50:53]
	v_mfma_f32_16x16x32_bf16 v[42:45], v[172:175], v[204:207], v[42:45]
	v_mfma_f32_16x16x32_bf16 v[34:37], v[164:167], v[212:215], v[34:37]
	v_mfma_f32_16x16x32_bf16 v[30:33], v[172:175], v[212:215], v[30:33]
	v_mfma_f32_16x16x32_bf16 v[14:17], v[164:167], v[220:223], v[14:17]
	v_mfma_f32_16x16x32_bf16 v[2:5], v[172:175], v[220:223], v[2:5]
	v_mfma_f32_16x16x32_bf16 v[62:65], v[168:171], v[200:203], v[62:65]
	v_mfma_f32_16x16x32_bf16 v[58:61], v[176:179], v[200:203], v[58:61]
	v_mfma_f32_16x16x32_bf16 v[50:53], v[168:171], v[208:211], v[50:53]
	v_mfma_f32_16x16x32_bf16 v[42:45], v[176:179], v[208:211], v[42:45]
	v_mfma_f32_16x16x32_bf16 v[34:37], v[168:171], v[216:219], v[34:37]
	v_mfma_f32_16x16x32_bf16 v[30:33], v[176:179], v[216:219], v[30:33]
	v_mfma_f32_16x16x32_bf16 v[14:17], v[168:171], v[224:227], v[14:17]
	v_mfma_f32_16x16x32_bf16 v[2:5], v[176:179], v[224:227], v[2:5]
	v_mfma_f32_16x16x32_bf16 v[54:57], v[180:183], v[196:199], v[54:57]
	v_mfma_f32_16x16x32_bf16 v[46:49], v[188:191], v[196:199], v[46:49]
	v_mfma_f32_16x16x32_bf16 v[38:41], v[180:183], v[204:207], v[38:41]
	v_mfma_f32_16x16x32_bf16 v[26:29], v[188:191], v[204:207], v[26:29]
	v_mfma_f32_16x16x32_bf16 v[22:25], v[180:183], v[212:215], v[22:25]
	v_mfma_f32_16x16x32_bf16 v[18:21], v[188:191], v[212:215], v[18:21]
	v_mfma_f32_16x16x32_bf16 v[10:13], v[180:183], v[220:223], v[10:13]
	v_mfma_f32_16x16x32_bf16 v[6:9], v[188:191], v[220:223], v[6:9]
	v_mfma_f32_16x16x32_bf16 v[54:57], v[184:187], v[200:203], v[54:57]
	v_mfma_f32_16x16x32_bf16 v[46:49], v[192:195], v[200:203], v[46:49]
	v_mfma_f32_16x16x32_bf16 v[38:41], v[184:187], v[208:211], v[38:41]
	v_mfma_f32_16x16x32_bf16 v[26:29], v[192:195], v[208:211], v[26:29]
	v_mfma_f32_16x16x32_bf16 v[22:25], v[184:187], v[216:219], v[22:25]
	v_mfma_f32_16x16x32_bf16 v[18:21], v[192:195], v[216:219], v[18:21]
	v_mfma_f32_16x16x32_bf16 v[10:13], v[184:187], v[224:227], v[10:13]
	v_mfma_f32_16x16x32_bf16 v[6:9], v[192:195], v[224:227], v[6:9]
	s_barrier
	s_add_i32 s91, 0, 0x18000
	v_add_u32_e32 v134, s91, v143
	s_add_i32 s92, 0, 0x1c000
	ds_read_b128 v[164:167], v134
	ds_read_b128 v[168:171], v134 offset:1024
	ds_read_b128 v[172:175], v134 offset:2048
	ds_read_b128 v[176:179], v134 offset:3072
	v_add_u32_e32 v134, s92, v143
	ds_read_b128 v[180:183], v134
	ds_read_b128 v[184:187], v134 offset:1024
	ds_read_b128 v[188:191], v134 offset:2048
	ds_read_b128 v[192:195], v134 offset:3072
	s_mov_b32 m0, s76
	ds_read_b128 v[196:199], v147 offset:32768
	ds_read_b128 v[200:203], v147 offset:33792
	ds_read_b128 v[204:207], v147 offset:34816
	ds_read_b128 v[208:211], v147 offset:35840
	ds_read_b128 v[212:215], v147 offset:36864
	ds_read_b128 v[216:219], v147 offset:37888
	ds_read_b128 v[220:223], v147 offset:38912
	ds_read_b128 v[224:227], v147 offset:39936
	global_load_lds_dwordx4 v153, s[60:61]
	s_mov_b32 m0, s77
	s_nop 0
	global_load_lds_dwordx4 v155, s[60:61]
	s_waitcnt vmcnt(8)
	s_waitcnt lgkmcnt(0)
	v_mfma_f32_16x16x32_bf16 v[126:129], v[164:167], v[196:199], v[126:129]
	s_barrier
	v_mfma_f32_16x16x32_bf16 v[122:125], v[172:175], v[196:199], v[122:125]
	v_mfma_f32_16x16x32_bf16 v[110:113], v[164:167], v[204:207], v[110:113]
	v_mfma_f32_16x16x32_bf16 v[106:109], v[172:175], v[204:207], v[106:109]
	v_mfma_f32_16x16x32_bf16 v[94:97], v[164:167], v[212:215], v[94:97]
	v_mfma_f32_16x16x32_bf16 v[90:93], v[172:175], v[212:215], v[90:93]
	v_mfma_f32_16x16x32_bf16 v[78:81], v[164:167], v[220:223], v[78:81]
	v_mfma_f32_16x16x32_bf16 v[74:77], v[172:175], v[220:223], v[74:77]
	v_mfma_f32_16x16x32_bf16 v[126:129], v[168:171], v[200:203], v[126:129]
	v_mfma_f32_16x16x32_bf16 v[122:125], v[176:179], v[200:203], v[122:125]
	v_mfma_f32_16x16x32_bf16 v[110:113], v[168:171], v[208:211], v[110:113]
	v_mfma_f32_16x16x32_bf16 v[106:109], v[176:179], v[208:211], v[106:109]
	v_mfma_f32_16x16x32_bf16 v[94:97], v[168:171], v[216:219], v[94:97]
	v_mfma_f32_16x16x32_bf16 v[90:93], v[176:179], v[216:219], v[90:93]
	v_mfma_f32_16x16x32_bf16 v[78:81], v[168:171], v[224:227], v[78:81]
	v_mfma_f32_16x16x32_bf16 v[74:77], v[176:179], v[224:227], v[74:77]
	v_mfma_f32_16x16x32_bf16 v[118:121], v[180:183], v[196:199], v[118:121]
	v_mfma_f32_16x16x32_bf16 v[114:117], v[188:191], v[196:199], v[114:117]
	v_mfma_f32_16x16x32_bf16 v[102:105], v[180:183], v[204:207], v[102:105]
	v_mfma_f32_16x16x32_bf16 v[98:101], v[188:191], v[204:207], v[98:101]
	v_mfma_f32_16x16x32_bf16 v[86:89], v[180:183], v[212:215], v[86:89]
	v_mfma_f32_16x16x32_bf16 v[82:85], v[188:191], v[212:215], v[82:85]
	v_mfma_f32_16x16x32_bf16 v[70:73], v[180:183], v[220:223], v[70:73]
	v_mfma_f32_16x16x32_bf16 v[66:69], v[188:191], v[220:223], v[66:69]
	v_mfma_f32_16x16x32_bf16 v[118:121], v[184:187], v[200:203], v[118:121]
	v_mfma_f32_16x16x32_bf16 v[114:117], v[192:195], v[200:203], v[114:117]
	v_mfma_f32_16x16x32_bf16 v[102:105], v[184:187], v[208:211], v[102:105]
	v_mfma_f32_16x16x32_bf16 v[98:101], v[192:195], v[208:211], v[98:101]
	v_mfma_f32_16x16x32_bf16 v[86:89], v[184:187], v[216:219], v[86:89]
	v_mfma_f32_16x16x32_bf16 v[82:85], v[192:195], v[216:219], v[82:85]
	v_mfma_f32_16x16x32_bf16 v[70:73], v[184:187], v[224:227], v[70:73]
	v_mfma_f32_16x16x32_bf16 v[66:69], v[192:195], v[224:227], v[66:69]
	s_barrier
; #define PG8_STAGE(bufoff, gbase, voff) do { _Pragma("unroll") for (int _i = 0; _i < 2; ++_i) \
;         __builtin_amdgcn_global_load_lds((const unsigned*)((const char*)(gbase) + (voff)[_i]), (PG8_LAS unsigned*)(lds + (bufoff) + ldsw + _i * 8192), 16, 0, 0); } while (0)
; #define PG8_LDA(dst, b, h) do { _Pragma("unroll") for (int m = 0; m < 4; ++m) _Pragma("unroll") for (int k = 0; k < 2; ++k) dst[m][k] = *(const PG8_LAS bf16x8*)(lds + PG8_SA(b, h) + aoff + m * 2048 + k * 1024); } while (0)
; #define PG8_MMA(ai, bj, At, Bt) do { __builtin_amdgcn_s_setprio(1); _Pragma("unroll") for (int m = 0; m < 4; ++m) _Pragma("unroll") for (int n = 0; n < 2; ++n) _Pragma("unroll") for (int k = 0; k < 2; ++k) \
;         acc[ai][bj][m][n] = __builtin_amdgcn_mfma_f32_16x16x32_bf16(Bt[n][k], At[m][k], acc[ai][bj][m][n], 0, 0, 0); __builtin_amdgcn_s_setprio(0); } while (0)
; #define PG8_WAIT_V(n) asm volatile("s_waitcnt vmcnt(" #n ")" ::: "memory")
; #define PG8_WAIT_L(n) asm volatile("s_waitcnt lgkmcnt(" #n ")" ::: "memory")
; #define PG8_BAR __builtin_amdgcn_s_barrier()
; #define PG8_SCHED __builtin_amdgcn_sched_barrier(0)
; template <class Epi, class Sched, bool ALIGN_EPI = false>
; __device__ __forceinline__ void gemm_phase(PG8_LAS unsigned char* lds, const Gemm g, const Sched& S, const Epi& E) {
;     ...
;             PG8_LDA(At, 1, 1); PG8_STAGE(PG8_SB(1, 0), b3, voffB); PG8_STAGE(PG8_SB(1, 1), b3 + hstep, voffB); PG8_STAGE(PG8_SA(1, 0), a3, w0);
;             PG8_WAIT_V(8); PG8_WAIT_L(0); PG8_BAR; PG8_MMA(1, 0, At, B0); PG8_MMA(1, 1, At, B1); PG8_BAR; PG8_SCHED;
;             if constexpr (Epi::KSCALE) { if (((t + 2) & 7) == 0 && t + 2 < nt) { E.kscale(acc, pf, ((t + 2) >> 3) - 1, wr, fr); PG8_SCHED; } }
;         }
	s_add_i32 s60, s91, s74
	v_lshl_add_u64 v[230:231], v[230:231], 0, s[44:45]
	s_mov_b32 m0, s60
	ds_read_b128 v[196:199], v147 offset:49152
	ds_read_b128 v[200:203], v147 offset:50176
	ds_read_b128 v[204:207], v147 offset:51200
	ds_read_b128 v[208:211], v147 offset:52224
	ds_read_b128 v[212:215], v147 offset:53248
	ds_read_b128 v[216:219], v147 offset:54272
	ds_read_b128 v[220:223], v147 offset:55296
	ds_read_b128 v[224:227], v147 offset:56320
	global_load_lds_dwordx4 v[230:231], off
	s_add_i32 m0, s60, 0x2000
	s_add_u32 s58, s58, 0x80080
	v_lshl_add_u64 v[230:231], v[232:233], 0, s[44:45]
	s_addc_u32 s59, s59, 0
	s_add_i32 s60, s92, s74
	global_load_lds_dwordx4 v[230:231], off
	v_lshl_add_u64 v[230:231], s[58:59], 0, v[130:131]
	s_mov_b32 m0, s60
	v_lshl_add_u64 v[228:229], v[228:229], 0, s[44:45]
	global_load_lds_dwordx4 v[230:231], off
	v_lshl_add_u64 v[230:231], s[58:59], 0, v[132:133]
	s_add_i32 m0, s60, 0x2000
	s_nop 0
	global_load_lds_dwordx4 v[230:231], off
	v_lshl_add_u64 v[230:231], v[234:235], 0, s[44:45]
	s_mov_b32 m0, s80
	s_nop 0
	global_load_lds_dwordx4 v[230:231], off
	s_mov_b32 m0, s81
	s_nop 0
	global_load_lds_dwordx4 v[228:229], off
	s_waitcnt vmcnt(8)
	s_waitcnt lgkmcnt(0)
	v_mfma_f32_16x16x32_bf16 v[62:65], v[164:167], v[196:199], v[62:65]
	s_barrier
	v_mfma_f32_16x16x32_bf16 v[58:61], v[172:175], v[196:199], v[58:61]
	v_mfma_f32_16x16x32_bf16 v[50:53], v[164:167], v[204:207], v[50:53]
	v_mfma_f32_16x16x32_bf16 v[42:45], v[172:175], v[204:207], v[42:45]
	v_mfma_f32_16x16x32_bf16 v[34:37], v[164:167], v[212:215], v[34:37]
	v_mfma_f32_16x16x32_bf16 v[30:33], v[172:175], v[212:215], v[30:33]
	v_mfma_f32_16x16x32_bf16 v[14:17], v[164:167], v[220:223], v[14:17]
	v_mfma_f32_16x16x32_bf16 v[2:5], v[172:175], v[220:223], v[2:5]
	v_mfma_f32_16x16x32_bf16 v[62:65], v[168:171], v[200:203], v[62:65]
	v_mfma_f32_16x16x32_bf16 v[58:61], v[176:179], v[200:203], v[58:61]
	v_mfma_f32_16x16x32_bf16 v[50:53], v[168:171], v[208:211], v[50:53]
	v_mfma_f32_16x16x32_bf16 v[42:45], v[176:179], v[208:211], v[42:45]
	v_mfma_f32_16x16x32_bf16 v[34:37], v[168:171], v[216:219], v[34:37]
	v_mfma_f32_16x16x32_bf16 v[30:33], v[176:179], v[216:219], v[30:33]
	v_mfma_f32_16x16x32_bf16 v[14:17], v[168:171], v[224:227], v[14:17]
	v_mfma_f32_16x16x32_bf16 v[2:5], v[176:179], v[224:227], v[2:5]
	v_mfma_f32_16x16x32_bf16 v[54:57], v[180:183], v[196:199], v[54:57]
	v_mfma_f32_16x16x32_bf16 v[46:49], v[188:191], v[196:199], v[46:49]
	v_mfma_f32_16x16x32_bf16 v[38:41], v[180:183], v[204:207], v[38:41]
	v_mfma_f32_16x16x32_bf16 v[26:29], v[188:191], v[204:207], v[26:29]
	v_mfma_f32_16x16x32_bf16 v[22:25], v[180:183], v[212:215], v[22:25]
	v_mfma_f32_16x16x32_bf16 v[18:21], v[188:191], v[212:215], v[18:21]
	v_mfma_f32_16x16x32_bf16 v[10:13], v[180:183], v[220:223], v[10:13]
	v_mfma_f32_16x16x32_bf16 v[6:9], v[188:191], v[220:223], v[6:9]
	v_mfma_f32_16x16x32_bf16 v[54:57], v[184:187], v[200:203], v[54:57]
	v_mfma_f32_16x16x32_bf16 v[46:49], v[192:195], v[200:203], v[46:49]
	v_mfma_f32_16x16x32_bf16 v[38:41], v[184:187], v[208:211], v[38:41]
	v_mfma_f32_16x16x32_bf16 v[26:29], v[192:195], v[208:211], v[26:29]
	v_mfma_f32_16x16x32_bf16 v[22:25], v[184:187], v[216:219], v[22:25]
	v_mfma_f32_16x16x32_bf16 v[18:21], v[192:195], v[216:219], v[18:21]
	v_mfma_f32_16x16x32_bf16 v[10:13], v[184:187], v[224:227], v[10:13]
	v_mfma_f32_16x16x32_bf16 v[6:9], v[192:195], v[224:227], v[6:9]
	s_barrier
	s_add_i32 s90, s90, 2
	s_add_u32 s56, s56, 0x100
	s_addc_u32 s57, s57, 0
	s_cmp_gt_u32 s90, 29
	s_cbranch_scc0 .LBB0_721
	s_and_b64 vcc, exec, s[46:47]
	s_cbranch_vccz .LBB0_724
	s_barrier

; #define PG8_STAGE(bufoff, gbase, voff) do { _Pragma("unroll") for (int _i = 0; _i < 2; ++_i) \
;         __builtin_amdgcn_global_load_lds((const unsigned*)((const char*)(gbase) + (voff)[_i]), (PG8_LAS unsigned*)(lds + (bufoff) + ldsw + _i * 8192), 16, 0, 0); } while (0)
; #define PG8_LDA(dst, b, h) do { _Pragma("unroll") for (int m = 0; m < 4; ++m) _Pragma("unroll") for (int k = 0; k < 2; ++k) dst[m][k] = *(const PG8_LAS bf16x8*)(lds + PG8_SA(b, h) + aoff + m * 2048 + k * 1024); } while (0)
; #define PG8_LDB(dst, b, h) do { _Pragma("unroll") for (int n = 0; n < 2; ++n) _Pragma("unroll") for (int k = 0; k < 2; ++k) dst[n][k] = *(const PG8_LAS bf16x8*)(lds + PG8_SB(b, h) + boff + n * 2048 + k * 1024); } while (0)
; #define PG8_MMA(ai, bj, At, Bt) do { __builtin_amdgcn_s_setprio(1); _Pragma("unroll") for (int m = 0; m < 4; ++m) _Pragma("unroll") for (int n = 0; n < 2; ++n) _Pragma("unroll") for (int k = 0; k < 2; ++k) \
;         acc[ai][bj][m][n] = __builtin_amdgcn_mfma_f32_16x16x32_bf16(Bt[n][k], At[m][k], acc[ai][bj][m][n], 0, 0, 0); __builtin_amdgcn_s_setprio(0); } while (0)
; #define PG8_BAR __builtin_amdgcn_s_barrier()
; template <class Epi, class Sched, bool ALIGN_EPI = false>
; __device__ __forceinline__ void gemm_phase(PG8_LAS unsigned char* lds, const Gemm g, const Sched& S, const Epi& E) {
;     ...
;             const bool last = (t == nt - 2);
;             const char* a1 = cA + (size_t)(t + 1) * kstep;
;             const char* a2 = last ? nA : cA + (size_t)(t + 2) * kstep; const char* b2 = last ? nB : cB + (size_t)(t + 2) * kstep;
;             const char* a3 = a2 + kstep; const char* b3 = b2 + kstep;
;             unsigned w0[2], w1[2];
; #pragma unroll
;             for (int i = 0; i < 2; ++i) { w0[i] = (Sched::GATHER && last) ? vn0[i] : vc0[i]; w1[i] = (Sched::GATHER && last) ? vn1[i] : vc1[i]; }
;             if (last && has_next) S.a_ready(nxt);
;             PG8_LDB(B0, 0, 0); PG8_LDB(B1, 0, 1); PG8_SCHED; PG8_LDA(At, 0, 0); PG8_STAGE(PG8_SA(1, 1), a1 + hstepA, vc1);
;             PG8_WAIT_V(8); PG8_WAIT_L(0); PG8_BAR; PG8_MMA(0, 0, At, B0); PG8_MMA(0, 1, At, B1); PG8_BAR; PG8_SCHED;
;             PG8_LDA(At, 0, 1); PG8_STAGE(PG8_SB(0, 0), b2, voffB); PG8_STAGE(PG8_SB(0, 1), b2 + hstep, voffB); PG8_STAGE(PG8_SA(0, 0), a2, w0);
;             PG8_WAIT_V(8); PG8_WAIT_L(0); PG8_BAR; PG8_MMA(1, 0, At, B0); PG8_MMA(1, 1, At, B1); PG8_BAR; PG8_SCHED;
.LBB0_787:
	ds_read_b128 v[172:175], v167
	ds_read_b128 v[176:179], v167 offset:1024
	ds_read_b128 v[180:183], v167 offset:2048
	ds_read_b128 v[184:187], v167 offset:3072
	ds_read_b128 v[188:191], v168
	ds_read_b128 v[192:195], v168 offset:1024
	ds_read_b128 v[196:199], v168 offset:2048
	ds_read_b128 v[200:203], v168 offset:3072
	s_add_u32 s18, s16, 0x3c800100
	s_addc_u32 s19, s17, 0
	s_add_u32 s58, s16, s45
	s_addc_u32 s59, s17, s46
	s_cmp_eq_u32 s47, 28
	s_cselect_b32 s23, s21, s19
	s_cselect_b32 s22, s20, s18
	s_cselect_b32 s19, s13, s59
	s_cselect_b32 s18, s12, s58
	s_mov_b32 m0, s48
	v_lshl_add_u64 v[236:237], s[16:17], 0, v[160:161]
	ds_read_b128 v[204:207], v169
	ds_read_b128 v[208:211], v169 offset:1024
	ds_read_b128 v[212:215], v169 offset:2048
	ds_read_b128 v[216:219], v169 offset:3072
	ds_read_b128 v[220:223], v169 offset:4096
	ds_read_b128 v[224:227], v169 offset:5120
	ds_read_b128 v[228:231], v169 offset:6144
	ds_read_b128 v[232:235], v169 offset:7168
	global_load_lds_dwordx4 v[236:237], off
	v_lshl_add_u64 v[236:237], s[16:17], 0, v[158:159]
	s_mov_b32 m0, s49
	s_nop 0
	global_load_lds_dwordx4 v[236:237], off
	s_waitcnt vmcnt(8)
	s_waitcnt lgkmcnt(0)
	v_mfma_f32_16x16x32_bf16 v[126:129], v[172:175], v[204:207], v[126:129]
	s_barrier
	v_mfma_f32_16x16x32_bf16 v[122:125], v[180:183], v[204:207], v[122:125]
	v_mfma_f32_16x16x32_bf16 v[110:113], v[172:175], v[212:215], v[110:113]
	v_mfma_f32_16x16x32_bf16 v[106:109], v[180:183], v[212:215], v[106:109]
	v_mfma_f32_16x16x32_bf16 v[94:97], v[172:175], v[220:223], v[94:97]
	v_mfma_f32_16x16x32_bf16 v[90:93], v[180:183], v[220:223], v[90:93]
	v_mfma_f32_16x16x32_bf16 v[78:81], v[172:175], v[228:231], v[78:81]
	v_mfma_f32_16x16x32_bf16 v[74:77], v[180:183], v[228:231], v[74:77]
	v_mfma_f32_16x16x32_bf16 v[126:129], v[176:179], v[208:211], v[126:129]
	v_mfma_f32_16x16x32_bf16 v[122:125], v[184:187], v[208:211], v[122:125]
	v_mfma_f32_16x16x32_bf16 v[110:113], v[176:179], v[216:219], v[110:113]
	v_mfma_f32_16x16x32_bf16 v[106:109], v[184:187], v[216:219], v[106:109]
	v_mfma_f32_16x16x32_bf16 v[94:97], v[176:179], v[224:227], v[94:97]
	v_mfma_f32_16x16x32_bf16 v[90:93], v[184:187], v[224:227], v[90:93]
	v_mfma_f32_16x16x32_bf16 v[78:81], v[176:179], v[232:235], v[78:81]
	v_mfma_f32_16x16x32_bf16 v[74:77], v[184:187], v[232:235], v[74:77]
	v_mfma_f32_16x16x32_bf16 v[118:121], v[188:191], v[204:207], v[118:121]
	v_mfma_f32_16x16x32_bf16 v[114:117], v[196:199], v[204:207], v[114:117]
	v_mfma_f32_16x16x32_bf16 v[102:105], v[188:191], v[212:215], v[102:105]
	v_mfma_f32_16x16x32_bf16 v[98:101], v[196:199], v[212:215], v[98:101]
	v_mfma_f32_16x16x32_bf16 v[86:89], v[188:191], v[220:223], v[86:89]
	v_mfma_f32_16x16x32_bf16 v[82:85], v[196:199], v[220:223], v[82:85]
	v_mfma_f32_16x16x32_bf16 v[70:73], v[188:191], v[228:231], v[70:73]
	v_mfma_f32_16x16x32_bf16 v[66:69], v[196:199], v[228:231], v[66:69]
	v_mfma_f32_16x16x32_bf16 v[118:121], v[192:195], v[208:211], v[118:121]
	v_mfma_f32_16x16x32_bf16 v[114:117], v[200:203], v[208:211], v[114:117]
	v_mfma_f32_16x16x32_bf16 v[102:105], v[192:195], v[216:219], v[102:105]
	v_mfma_f32_16x16x32_bf16 v[98:101], v[200:203], v[216:219], v[98:101]
	v_mfma_f32_16x16x32_bf16 v[86:89], v[192:195], v[224:227], v[86:89]
	v_mfma_f32_16x16x32_bf16 v[82:85], v[200:203], v[224:227], v[82:85]
	v_mfma_f32_16x16x32_bf16 v[70:73], v[192:195], v[232:235], v[70:73]
	v_mfma_f32_16x16x32_bf16 v[66:69], v[200:203], v[232:235], v[66:69]
	s_barrier
	s_mov_b32 m0, s50
	v_lshl_add_u64 v[236:237], s[18:19], 0, v[146:147]
	s_add_u32 s58, s18, 0x80000
	ds_read_b128 v[204:207], v169 offset:16384
	ds_read_b128 v[208:211], v169 offset:17408
	ds_read_b128 v[212:215], v169 offset:18432
	ds_read_b128 v[216:219], v169 offset:19456
	ds_read_b128 v[220:223], v169 offset:20480
	ds_read_b128 v[224:227], v169 offset:21504
	ds_read_b128 v[228:231], v169 offset:22528
	ds_read_b128 v[232:235], v169 offset:23552
	global_load_lds_dwordx4 v[236:237], off
	v_lshl_add_u64 v[238:239], s[18:19], 0, v[144:145]
	s_mov_b32 m0, s51
	s_addc_u32 s59, s19, 0
	global_load_lds_dwordx4 v[238:239], off
	v_lshl_add_u64 v[240:241], s[58:59], 0, v[146:147]
	s_mov_b32 m0, s52
	v_lshl_add_u64 v[242:243], s[22:23], 0, v[150:151]
	global_load_lds_dwordx4 v[240:241], off
	v_lshl_add_u64 v[240:241], s[58:59], 0, v[144:145]
	s_mov_b32 m0, s53
	s_nop 0
	global_load_lds_dwordx4 v[240:241], off
	v_lshl_add_u64 v[240:241], s[22:23], 0, v[148:149]
	s_mov_b32 m0, s27
	s_nop 0
	global_load_lds_dwordx4 v[240:241], off
	s_mov_b32 m0, s35
	s_nop 0
	global_load_lds_dwordx4 v[242:243], off
	s_waitcnt vmcnt(8)
	s_waitcnt lgkmcnt(0)
	v_mfma_f32_16x16x32_bf16 v[62:65], v[172:175], v[204:207], v[62:65]
	s_barrier
; #define PG8_STAGE(bufoff, gbase, voff) do { _Pragma("unroll") for (int _i = 0; _i < 2; ++_i) \
;         __builtin_amdgcn_global_load_lds((const unsigned*)((const char*)(gbase) + (voff)[_i]), (PG8_LAS unsigned*)(lds + (bufoff) + ldsw + _i * 8192), 16, 0, 0); } while (0)
; #define PG8_LDA(dst, b, h) do { _Pragma("unroll") for (int m = 0; m < 4; ++m) _Pragma("unroll") for (int k = 0; k < 2; ++k) dst[m][k] = *(const PG8_LAS bf16x8*)(lds + PG8_SA(b, h) + aoff + m * 2048 + k * 1024); } while (0)
; #define PG8_LDB(dst, b, h) do { _Pragma("unroll") for (int n = 0; n < 2; ++n) _Pragma("unroll") for (int k = 0; k < 2; ++k) dst[n][k] = *(const PG8_LAS bf16x8*)(lds + PG8_SB(b, h) + boff + n * 2048 + k * 1024); } while (0)
; #define PG8_MMA(ai, bj, At, Bt) do { __builtin_amdgcn_s_setprio(1); _Pragma("unroll") for (int m = 0; m < 4; ++m) _Pragma("unroll") for (int n = 0; n < 2; ++n) _Pragma("unroll") for (int k = 0; k < 2; ++k) \
;         acc[ai][bj][m][n] = __builtin_amdgcn_mfma_f32_16x16x32_bf16(Bt[n][k], At[m][k], acc[ai][bj][m][n], 0, 0, 0); __builtin_amdgcn_s_setprio(0); } while (0)
; #define PG8_WAIT_V(n) asm volatile("s_waitcnt vmcnt(" #n ")" ::: "memory")
; #define PG8_WAIT_L(n) asm volatile("s_waitcnt lgkmcnt(" #n ")" ::: "memory")
; #define PG8_BAR __builtin_amdgcn_s_barrier()
; #define PG8_SCHED __builtin_amdgcn_sched_barrier(0)
; template <class Epi, class Sched, bool ALIGN_EPI = false>
; __device__ __forceinline__ void gemm_phase(PG8_LAS unsigned char* lds, const Gemm g, const Sched& S, const Epi& E) {
;     ...
;             PG8_WAIT_V(8); PG8_WAIT_L(0); PG8_BAR; PG8_MMA(1, 0, At, B0); PG8_MMA(1, 1, At, B1); PG8_BAR; PG8_SCHED;
;             PG8_LDB(B0, 1, 0); PG8_LDB(B1, 1, 1); PG8_SCHED; PG8_LDA(At, 1, 0); PG8_STAGE(PG8_SA(0, 1), a2 + hstepA, w1);
;             PG8_WAIT_V(8); PG8_WAIT_L(0); PG8_BAR; PG8_MMA(0, 0, At, B0); PG8_MMA(0, 1, At, B1); PG8_BAR; PG8_SCHED;
	v_mfma_f32_16x16x32_bf16 v[58:61], v[180:183], v[204:207], v[58:61]
	v_mfma_f32_16x16x32_bf16 v[50:53], v[172:175], v[212:215], v[50:53]
	v_mfma_f32_16x16x32_bf16 v[42:45], v[180:183], v[212:215], v[42:45]
	v_mfma_f32_16x16x32_bf16 v[34:37], v[172:175], v[220:223], v[34:37]
	v_mfma_f32_16x16x32_bf16 v[26:29], v[180:183], v[220:223], v[26:29]
	v_mfma_f32_16x16x32_bf16 v[14:17], v[172:175], v[228:231], v[14:17]
	v_mfma_f32_16x16x32_bf16 v[2:5], v[180:183], v[228:231], v[2:5]
	v_mfma_f32_16x16x32_bf16 v[62:65], v[176:179], v[208:211], v[62:65]
	v_mfma_f32_16x16x32_bf16 v[58:61], v[184:187], v[208:211], v[58:61]
	v_mfma_f32_16x16x32_bf16 v[50:53], v[176:179], v[216:219], v[50:53]
	v_mfma_f32_16x16x32_bf16 v[42:45], v[184:187], v[216:219], v[42:45]
	v_mfma_f32_16x16x32_bf16 v[34:37], v[176:179], v[224:227], v[34:37]
	v_mfma_f32_16x16x32_bf16 v[26:29], v[184:187], v[224:227], v[26:29]
	v_mfma_f32_16x16x32_bf16 v[14:17], v[176:179], v[232:235], v[14:17]
	v_mfma_f32_16x16x32_bf16 v[2:5], v[184:187], v[232:235], v[2:5]
	v_mfma_f32_16x16x32_bf16 v[54:57], v[188:191], v[204:207], v[54:57]
	v_mfma_f32_16x16x32_bf16 v[46:49], v[196:199], v[204:207], v[46:49]
	v_mfma_f32_16x16x32_bf16 v[38:41], v[188:191], v[212:215], v[38:41]
	v_mfma_f32_16x16x32_bf16 v[30:33], v[196:199], v[212:215], v[30:33]
	v_mfma_f32_16x16x32_bf16 v[22:25], v[188:191], v[220:223], v[22:25]
	v_mfma_f32_16x16x32_bf16 v[18:21], v[196:199], v[220:223], v[18:21]
	v_mfma_f32_16x16x32_bf16 v[10:13], v[188:191], v[228:231], v[10:13]
	v_mfma_f32_16x16x32_bf16 v[6:9], v[196:199], v[228:231], v[6:9]
	v_mfma_f32_16x16x32_bf16 v[54:57], v[192:195], v[208:211], v[54:57]
	v_mfma_f32_16x16x32_bf16 v[46:49], v[200:203], v[208:211], v[46:49]
	v_mfma_f32_16x16x32_bf16 v[38:41], v[192:195], v[216:219], v[38:41]
	v_mfma_f32_16x16x32_bf16 v[30:33], v[200:203], v[216:219], v[30:33]
	v_mfma_f32_16x16x32_bf16 v[22:25], v[192:195], v[224:227], v[22:25]
	v_mfma_f32_16x16x32_bf16 v[18:21], v[200:203], v[224:227], v[18:21]
	v_mfma_f32_16x16x32_bf16 v[10:13], v[192:195], v[232:235], v[10:13]
	v_mfma_f32_16x16x32_bf16 v[6:9], v[200:203], v[232:235], v[6:9]
	s_barrier
	ds_read_b128 v[172:175], v170
	ds_read_b128 v[176:179], v170 offset:1024
	ds_read_b128 v[180:183], v170 offset:2048
	ds_read_b128 v[184:187], v170 offset:3072
	ds_read_b128 v[188:191], v171
	ds_read_b128 v[192:195], v171 offset:1024
	ds_read_b128 v[196:199], v171 offset:2048
	ds_read_b128 v[200:203], v171 offset:3072
	s_mov_b32 m0, s40
	v_lshl_add_u64 v[244:245], s[22:23], 0, v[152:153]
	ds_read_b128 v[204:207], v169 offset:32768
	ds_read_b128 v[208:211], v169 offset:33792
	ds_read_b128 v[212:215], v169 offset:34816
	ds_read_b128 v[216:219], v169 offset:35840
	ds_read_b128 v[220:223], v169 offset:36864
	ds_read_b128 v[224:227], v169 offset:37888
	ds_read_b128 v[228:231], v169 offset:38912
	ds_read_b128 v[232:235], v169 offset:39936
	global_load_lds_dwordx4 v[244:245], off
	v_lshl_add_u64 v[244:245], s[22:23], 0, v[154:155]
	s_mov_b32 m0, s41
	s_nop 0
	global_load_lds_dwordx4 v[244:245], off
	s_waitcnt vmcnt(8)
	s_waitcnt lgkmcnt(0)
	v_mfma_f32_16x16x32_bf16 v[126:129], v[172:175], v[204:207], v[126:129]
	s_barrier
	v_mfma_f32_16x16x32_bf16 v[122:125], v[180:183], v[204:207], v[122:125]
	v_mfma_f32_16x16x32_bf16 v[110:113], v[172:175], v[212:215], v[110:113]
	v_mfma_f32_16x16x32_bf16 v[106:109], v[180:183], v[212:215], v[106:109]
	v_mfma_f32_16x16x32_bf16 v[94:97], v[172:175], v[220:223], v[94:97]
	v_mfma_f32_16x16x32_bf16 v[90:93], v[180:183], v[220:223], v[90:93]
	v_mfma_f32_16x16x32_bf16 v[78:81], v[172:175], v[228:231], v[78:81]
	v_mfma_f32_16x16x32_bf16 v[74:77], v[180:183], v[228:231], v[74:77]
	v_mfma_f32_16x16x32_bf16 v[126:129], v[176:179], v[208:211], v[126:129]
	v_mfma_f32_16x16x32_bf16 v[122:125], v[184:187], v[208:211], v[122:125]
	v_mfma_f32_16x16x32_bf16 v[110:113], v[176:179], v[216:219], v[110:113]
	v_mfma_f32_16x16x32_bf16 v[106:109], v[184:187], v[216:219], v[106:109]
	v_mfma_f32_16x16x32_bf16 v[94:97], v[176:179], v[224:227], v[94:97]
	v_mfma_f32_16x16x32_bf16 v[90:93], v[184:187], v[224:227], v[90:93]
	v_mfma_f32_16x16x32_bf16 v[78:81], v[176:179], v[232:235], v[78:81]
	v_mfma_f32_16x16x32_bf16 v[74:77], v[184:187], v[232:235], v[74:77]
	v_mfma_f32_16x16x32_bf16 v[118:121], v[188:191], v[204:207], v[118:121]
	v_mfma_f32_16x16x32_bf16 v[114:117], v[196:199], v[204:207], v[114:117]
	v_mfma_f32_16x16x32_bf16 v[102:105], v[188:191], v[212:215], v[102:105]
	v_mfma_f32_16x16x32_bf16 v[98:101], v[196:199], v[212:215], v[98:101]
	v_mfma_f32_16x16x32_bf16 v[86:89], v[188:191], v[220:223], v[86:89]
	v_mfma_f32_16x16x32_bf16 v[82:85], v[196:199], v[220:223], v[82:85]
	v_mfma_f32_16x16x32_bf16 v[70:73], v[188:191], v[228:231], v[70:73]
	v_mfma_f32_16x16x32_bf16 v[66:69], v[196:199], v[228:231], v[66:69]
	v_mfma_f32_16x16x32_bf16 v[118:121], v[192:195], v[208:211], v[118:121]
	v_mfma_f32_16x16x32_bf16 v[114:117], v[200:203], v[208:211], v[114:117]
	v_mfma_f32_16x16x32_bf16 v[102:105], v[192:195], v[216:219], v[102:105]
	v_mfma_f32_16x16x32_bf16 v[98:101], v[200:203], v[216:219], v[98:101]
	v_mfma_f32_16x16x32_bf16 v[86:89], v[192:195], v[224:227], v[86:89]
	v_mfma_f32_16x16x32_bf16 v[82:85], v[200:203], v[224:227], v[82:85]
	v_mfma_f32_16x16x32_bf16 v[70:73], v[192:195], v[232:235], v[70:73]
	v_mfma_f32_16x16x32_bf16 v[66:69], v[200:203], v[232:235], v[66:69]
	s_barrier
; #define PG8_STAGE(bufoff, gbase, voff) do { _Pragma("unroll") for (int _i = 0; _i < 2; ++_i) \
;         __builtin_amdgcn_global_load_lds((const unsigned*)((const char*)(gbase) + (voff)[_i]), (PG8_LAS unsigned*)(lds + (bufoff) + ldsw + _i * 8192), 16, 0, 0); } while (0)
; #define PG8_LDA(dst, b, h) do { _Pragma("unroll") for (int m = 0; m < 4; ++m) _Pragma("unroll") for (int k = 0; k < 2; ++k) dst[m][k] = *(const PG8_LAS bf16x8*)(lds + PG8_SA(b, h) + aoff + m * 2048 + k * 1024); } while (0)
; #define PG8_MMA(ai, bj, At, Bt) do { __builtin_amdgcn_s_setprio(1); _Pragma("unroll") for (int m = 0; m < 4; ++m) _Pragma("unroll") for (int n = 0; n < 2; ++n) _Pragma("unroll") for (int k = 0; k < 2; ++k) \
;         acc[ai][bj][m][n] = __builtin_amdgcn_mfma_f32_16x16x32_bf16(Bt[n][k], At[m][k], acc[ai][bj][m][n], 0, 0, 0); __builtin_amdgcn_s_setprio(0); } while (0)
; #define PG8_WAIT_V(n) asm volatile("s_waitcnt vmcnt(" #n ")" ::: "memory")
; #define PG8_WAIT_L(n) asm volatile("s_waitcnt lgkmcnt(" #n ")" ::: "memory")
; #define PG8_BAR __builtin_amdgcn_s_barrier()
; #define PG8_SCHED __builtin_amdgcn_sched_barrier(0)
; template <class Epi, class Sched, bool ALIGN_EPI = false>
; __device__ __forceinline__ void gemm_phase(PG8_LAS unsigned char* lds, const Gemm g, const Sched& S, const Epi& E) {
;     ...
;             PG8_LDA(At, 1, 1); PG8_STAGE(PG8_SB(1, 0), b3, voffB); PG8_STAGE(PG8_SB(1, 1), b3 + hstep, voffB); PG8_STAGE(PG8_SA(1, 0), a3, w0);
;             PG8_WAIT_V(8); PG8_WAIT_L(0); PG8_BAR; PG8_MMA(1, 0, At, B0); PG8_MMA(1, 1, At, B1); PG8_BAR; PG8_SCHED;
;             if constexpr (Epi::KSCALE) { if (((t + 2) & 7) == 0 && t + 2 < nt) { E.kscale(acc, pf, ((t + 2) >> 3) - 1, wr, fr); PG8_SCHED; } }
;         }
	s_mov_b32 m0, s54
	v_lshl_add_u64 v[236:237], v[236:237], 0, s[14:15]
	s_add_u32 s18, s18, 0x80080
	ds_read_b128 v[204:207], v169 offset:49152
	ds_read_b128 v[208:211], v169 offset:50176
	ds_read_b128 v[212:215], v169 offset:51200
	ds_read_b128 v[216:219], v169 offset:52224
	ds_read_b128 v[220:223], v169 offset:53248
	ds_read_b128 v[224:227], v169 offset:54272
	ds_read_b128 v[228:231], v169 offset:55296
	ds_read_b128 v[232:235], v169 offset:56320
	global_load_lds_dwordx4 v[236:237], off
	v_lshl_add_u64 v[236:237], v[238:239], 0, s[14:15]
	s_mov_b32 m0, s55
	s_addc_u32 s19, s19, 0
	global_load_lds_dwordx4 v[236:237], off
	v_lshl_add_u64 v[236:237], s[18:19], 0, v[146:147]
	s_mov_b32 m0, s56
	s_nop 0
	global_load_lds_dwordx4 v[236:237], off
	v_lshl_add_u64 v[236:237], s[18:19], 0, v[144:145]
	s_mov_b32 m0, s57
	s_nop 0
	global_load_lds_dwordx4 v[236:237], off
	v_lshl_add_u64 v[236:237], v[240:241], 0, s[14:15]
	s_mov_b32 m0, s43
	s_nop 0
	global_load_lds_dwordx4 v[236:237], off
	v_lshl_add_u64 v[236:237], v[242:243], 0, s[14:15]
	s_mov_b32 m0, s44
	s_nop 0
	global_load_lds_dwordx4 v[236:237], off
	s_waitcnt vmcnt(8)
	s_waitcnt lgkmcnt(0)
	v_mfma_f32_16x16x32_bf16 v[62:65], v[172:175], v[204:207], v[62:65]
	s_barrier
	v_mfma_f32_16x16x32_bf16 v[58:61], v[180:183], v[204:207], v[58:61]
	v_mfma_f32_16x16x32_bf16 v[50:53], v[172:175], v[212:215], v[50:53]
	v_mfma_f32_16x16x32_bf16 v[42:45], v[180:183], v[212:215], v[42:45]
	v_mfma_f32_16x16x32_bf16 v[34:37], v[172:175], v[220:223], v[34:37]
	v_mfma_f32_16x16x32_bf16 v[26:29], v[180:183], v[220:223], v[26:29]
	v_mfma_f32_16x16x32_bf16 v[14:17], v[172:175], v[228:231], v[14:17]
	v_mfma_f32_16x16x32_bf16 v[2:5], v[180:183], v[228:231], v[2:5]
	v_mfma_f32_16x16x32_bf16 v[62:65], v[176:179], v[208:211], v[62:65]
	v_mfma_f32_16x16x32_bf16 v[58:61], v[184:187], v[208:211], v[58:61]
	v_mfma_f32_16x16x32_bf16 v[50:53], v[176:179], v[216:219], v[50:53]
	v_mfma_f32_16x16x32_bf16 v[42:45], v[184:187], v[216:219], v[42:45]
	v_mfma_f32_16x16x32_bf16 v[34:37], v[176:179], v[224:227], v[34:37]
	v_mfma_f32_16x16x32_bf16 v[26:29], v[184:187], v[224:227], v[26:29]
	v_mfma_f32_16x16x32_bf16 v[14:17], v[176:179], v[232:235], v[14:17]
	v_mfma_f32_16x16x32_bf16 v[2:5], v[184:187], v[232:235], v[2:5]
	v_mfma_f32_16x16x32_bf16 v[54:57], v[188:191], v[204:207], v[54:57]
	v_mfma_f32_16x16x32_bf16 v[46:49], v[196:199], v[204:207], v[46:49]
	v_mfma_f32_16x16x32_bf16 v[38:41], v[188:191], v[212:215], v[38:41]
	v_mfma_f32_16x16x32_bf16 v[30:33], v[196:199], v[212:215], v[30:33]
	v_mfma_f32_16x16x32_bf16 v[22:25], v[188:191], v[220:223], v[22:25]
	v_mfma_f32_16x16x32_bf16 v[18:21], v[196:199], v[220:223], v[18:21]
	v_mfma_f32_16x16x32_bf16 v[10:13], v[188:191], v[228:231], v[10:13]
	v_mfma_f32_16x16x32_bf16 v[6:9], v[196:199], v[228:231], v[6:9]
	v_mfma_f32_16x16x32_bf16 v[54:57], v[192:195], v[208:211], v[54:57]
	v_mfma_f32_16x16x32_bf16 v[46:49], v[200:203], v[208:211], v[46:49]
	v_mfma_f32_16x16x32_bf16 v[38:41], v[192:195], v[216:219], v[38:41]
	v_mfma_f32_16x16x32_bf16 v[30:33], v[200:203], v[216:219], v[30:33]
	v_mfma_f32_16x16x32_bf16 v[22:25], v[192:195], v[224:227], v[22:25]
	v_mfma_f32_16x16x32_bf16 v[18:21], v[200:203], v[224:227], v[18:21]
	v_mfma_f32_16x16x32_bf16 v[10:13], v[192:195], v[232:235], v[10:13]
	v_mfma_f32_16x16x32_bf16 v[6:9], v[200:203], v[232:235], v[6:9]
	s_barrier
	s_add_i32 s47, s47, 2
	s_add_u32 s16, s16, 0x100
	s_addc_u32 s17, s17, 0
	s_cmp_gt_u32 s47, 29
	s_cbranch_scc0 .LBB0_787
	s_cmpk_lt_u32 s24, 0x100
	s_cbranch_scc0 .LBB0_790
	s_barrier

; #define PG8_STAGE(bufoff, gbase, voff) do { _Pragma("unroll") for (int _i = 0; _i < 2; ++_i) \
;         __builtin_amdgcn_global_load_lds((const unsigned*)((const char*)(gbase) + (voff)[_i]), (PG8_LAS unsigned*)(lds + (bufoff) + ldsw + _i * 8192), 16, 0, 0); } while (0)
; #define PG8_LDA(dst, b, h) do { _Pragma("unroll") for (int m = 0; m < 4; ++m) _Pragma("unroll") for (int k = 0; k < 2; ++k) dst[m][k] = *(const PG8_LAS bf16x8*)(lds + PG8_SA(b, h) + aoff + m * 2048 + k * 1024); } while (0)
; #define PG8_LDB(dst, b, h) do { _Pragma("unroll") for (int n = 0; n < 2; ++n) _Pragma("unroll") for (int k = 0; k < 2; ++k) dst[n][k] = *(const PG8_LAS bf16x8*)(lds + PG8_SB(b, h) + boff + n * 2048 + k * 1024); } while (0)
; #define PG8_MMA(ai, bj, At, Bt) do { __builtin_amdgcn_s_setprio(1); _Pragma("unroll") for (int m = 0; m < 4; ++m) _Pragma("unroll") for (int n = 0; n < 2; ++n) _Pragma("unroll") for (int k = 0; k < 2; ++k) \
;         acc[ai][bj][m][n] = __builtin_amdgcn_mfma_f32_16x16x32_bf16(Bt[n][k], At[m][k], acc[ai][bj][m][n], 0, 0, 0); __builtin_amdgcn_s_setprio(0); } while (0)
; #define PG8_BAR __builtin_amdgcn_s_barrier()
; template <class Epi, class Sched, bool ALIGN_EPI = false>
; __device__ __forceinline__ void gemm_phase(PG8_LAS unsigned char* lds, const Gemm g, const Sched& S, const Epi& E) {
;     ...
;             const bool last = (t == nt - 2);
;             const char* a1 = cA + (size_t)(t + 1) * kstep;
;             const char* a2 = last ? nA : cA + (size_t)(t + 2) * kstep; const char* b2 = last ? nB : cB + (size_t)(t + 2) * kstep;
;             const char* a3 = a2 + kstep; const char* b3 = b2 + kstep;
;             unsigned w0[2], w1[2];
; #pragma unroll
;             for (int i = 0; i < 2; ++i) { w0[i] = (Sched::GATHER && last) ? vn0[i] : vc0[i]; w1[i] = (Sched::GATHER && last) ? vn1[i] : vc1[i]; }
;             if (last && has_next) S.a_ready(nxt);
;             PG8_LDB(B0, 0, 0); PG8_LDB(B1, 0, 1); PG8_SCHED; PG8_LDA(At, 0, 0); PG8_STAGE(PG8_SA(1, 1), a1 + hstepA, vc1);
;             PG8_WAIT_V(8); PG8_WAIT_L(0); PG8_BAR; PG8_MMA(0, 0, At, B0); PG8_MMA(0, 1, At, B1); PG8_BAR; PG8_SCHED;
;             PG8_LDA(At, 0, 1); PG8_STAGE(PG8_SB(0, 0), b2, voffB); PG8_STAGE(PG8_SB(0, 1), b2 + hstep, voffB); PG8_STAGE(PG8_SA(0, 0), a2, w0);
;             PG8_WAIT_V(8); PG8_WAIT_L(0); PG8_BAR; PG8_MMA(1, 0, At, B0); PG8_MMA(1, 1, At, B1); PG8_BAR; PG8_SCHED;
.LBB0_805:
	ds_read_b128 v[142:145], v1
	ds_read_b128 v[158:161], v1 offset:1024
	ds_read_b128 v[162:165], v1 offset:2048
	ds_read_b128 v[166:169], v1 offset:3072
	ds_read_b128 v[170:173], v156
	ds_read_b128 v[174:177], v156 offset:1024
	ds_read_b128 v[178:181], v156 offset:2048
	ds_read_b128 v[182:185], v156 offset:3072
	s_add_u32 s62, s60, 0xfffe0080
	s_addc_u32 s63, s61, -1
	s_cmp_eq_u32 s92, 4
	s_cselect_b32 s65, s45, s63
	s_cselect_b32 s64, s57, s62
	s_cselect_b32 s63, s47, s91
	s_cselect_b32 s62, s89, s90
	v_lshl_add_u64 v[218:219], s[60:61], 0, v[140:141]
	s_add_i32 m0, s59, 0xc000
	ds_read_b128 v[186:189], v157
	ds_read_b128 v[190:193], v157 offset:1024
	ds_read_b128 v[194:197], v157 offset:2048
	ds_read_b128 v[198:201], v157 offset:3072
	ds_read_b128 v[202:205], v157 offset:4096
	ds_read_b128 v[206:209], v157 offset:5120
	ds_read_b128 v[210:213], v157 offset:6144
	ds_read_b128 v[214:217], v157 offset:7168
	global_load_lds_dwordx4 v[218:219], off
	v_lshl_add_u64 v[218:219], s[60:61], 0, v[138:139]
	s_add_i32 m0, s59, 0xe000
	s_nop 0
	global_load_lds_dwordx4 v[218:219], off
	s_waitcnt vmcnt(8)
	s_waitcnt lgkmcnt(0)
	v_mfma_f32_16x16x32_bf16 v[126:129], v[142:145], v[186:189], v[126:129]
	s_barrier
	v_mfma_f32_16x16x32_bf16 v[122:125], v[162:165], v[186:189], v[122:125]
	v_mfma_f32_16x16x32_bf16 v[114:117], v[142:145], v[194:197], v[114:117]
	v_mfma_f32_16x16x32_bf16 v[106:109], v[162:165], v[194:197], v[106:109]
	v_mfma_f32_16x16x32_bf16 v[98:101], v[142:145], v[202:205], v[98:101]
	v_mfma_f32_16x16x32_bf16 v[90:93], v[162:165], v[202:205], v[90:93]
	v_mfma_f32_16x16x32_bf16 v[82:85], v[142:145], v[210:213], v[82:85]
	v_mfma_f32_16x16x32_bf16 v[74:77], v[162:165], v[210:213], v[74:77]
	v_mfma_f32_16x16x32_bf16 v[126:129], v[158:161], v[190:193], v[126:129]
	v_mfma_f32_16x16x32_bf16 v[122:125], v[166:169], v[190:193], v[122:125]
	v_mfma_f32_16x16x32_bf16 v[114:117], v[158:161], v[198:201], v[114:117]
	v_mfma_f32_16x16x32_bf16 v[106:109], v[166:169], v[198:201], v[106:109]
	v_mfma_f32_16x16x32_bf16 v[98:101], v[158:161], v[206:209], v[98:101]
	v_mfma_f32_16x16x32_bf16 v[90:93], v[166:169], v[206:209], v[90:93]
	v_mfma_f32_16x16x32_bf16 v[82:85], v[158:161], v[214:217], v[82:85]
	v_mfma_f32_16x16x32_bf16 v[74:77], v[166:169], v[214:217], v[74:77]
	v_mfma_f32_16x16x32_bf16 v[118:121], v[170:173], v[186:189], v[118:121]
	v_mfma_f32_16x16x32_bf16 v[110:113], v[178:181], v[186:189], v[110:113]
	v_mfma_f32_16x16x32_bf16 v[102:105], v[170:173], v[194:197], v[102:105]
	v_mfma_f32_16x16x32_bf16 v[94:97], v[178:181], v[194:197], v[94:97]
	v_mfma_f32_16x16x32_bf16 v[86:89], v[170:173], v[202:205], v[86:89]
	v_mfma_f32_16x16x32_bf16 v[78:81], v[178:181], v[202:205], v[78:81]
	v_mfma_f32_16x16x32_bf16 v[62:65], v[170:173], v[210:213], v[62:65]
	v_mfma_f32_16x16x32_bf16 v[58:61], v[178:181], v[210:213], v[58:61]
	v_mfma_f32_16x16x32_bf16 v[118:121], v[174:177], v[190:193], v[118:121]
	v_mfma_f32_16x16x32_bf16 v[110:113], v[182:185], v[190:193], v[110:113]
	v_mfma_f32_16x16x32_bf16 v[102:105], v[174:177], v[198:201], v[102:105]
	v_mfma_f32_16x16x32_bf16 v[94:97], v[182:185], v[198:201], v[94:97]
	v_mfma_f32_16x16x32_bf16 v[86:89], v[174:177], v[206:209], v[86:89]
	v_mfma_f32_16x16x32_bf16 v[78:81], v[182:185], v[206:209], v[78:81]
	v_mfma_f32_16x16x32_bf16 v[62:65], v[174:177], v[214:217], v[62:65]
	v_mfma_f32_16x16x32_bf16 v[58:61], v[182:185], v[214:217], v[58:61]
	s_barrier
	s_add_i32 s93, s79, s66
	v_lshl_add_u64 v[218:219], s[62:63], 0, v[132:133]
	s_mov_b32 m0, s93
	ds_read_b128 v[186:189], v157 offset:16384
	ds_read_b128 v[190:193], v157 offset:17408
	ds_read_b128 v[194:197], v157 offset:18432
	ds_read_b128 v[198:201], v157 offset:19456
	ds_read_b128 v[202:205], v157 offset:20480
	ds_read_b128 v[206:209], v157 offset:21504
	ds_read_b128 v[210:213], v157 offset:22528
	ds_read_b128 v[214:217], v157 offset:23552
	global_load_lds_dwordx4 v[218:219], off
	s_add_i32 m0, s93, 0x2000
	s_add_u32 s94, s62, 0x20000
	v_lshl_add_u64 v[220:221], s[62:63], 0, v[136:137]
	s_addc_u32 s95, s63, 0
	s_add_i32 s93, s80, s66
	global_load_lds_dwordx4 v[220:221], off
	v_lshl_add_u64 v[222:223], s[94:95], 0, v[132:133]
	s_mov_b32 m0, s93
	v_lshl_add_u64 v[224:225], s[64:65], 0, v[134:135]
	global_load_lds_dwordx4 v[222:223], off
	v_lshl_add_u64 v[222:223], s[94:95], 0, v[136:137]
	s_add_i32 m0, s93, 0x2000
	s_nop 0
	global_load_lds_dwordx4 v[222:223], off
	v_lshl_add_u64 v[222:223], s[64:65], 0, v[130:131]
	s_mov_b32 m0, s59
	s_nop 0
	global_load_lds_dwordx4 v[222:223], off
	s_mov_b32 m0, s67
	s_nop 0
	global_load_lds_dwordx4 v[224:225], off
	s_waitcnt vmcnt(8)
	s_waitcnt lgkmcnt(0)
	v_mfma_f32_16x16x32_bf16 v[54:57], v[142:145], v[186:189], v[54:57]
	s_barrier
; #define PG8_STAGE(bufoff, gbase, voff) do { _Pragma("unroll") for (int _i = 0; _i < 2; ++_i) \
;         __builtin_amdgcn_global_load_lds((const unsigned*)((const char*)(gbase) + (voff)[_i]), (PG8_LAS unsigned*)(lds + (bufoff) + ldsw + _i * 8192), 16, 0, 0); } while (0)
; #define PG8_LDA(dst, b, h) do { _Pragma("unroll") for (int m = 0; m < 4; ++m) _Pragma("unroll") for (int k = 0; k < 2; ++k) dst[m][k] = *(const PG8_LAS bf16x8*)(lds + PG8_SA(b, h) + aoff + m * 2048 + k * 1024); } while (0)
; #define PG8_LDB(dst, b, h) do { _Pragma("unroll") for (int n = 0; n < 2; ++n) _Pragma("unroll") for (int k = 0; k < 2; ++k) dst[n][k] = *(const PG8_LAS bf16x8*)(lds + PG8_SB(b, h) + boff + n * 2048 + k * 1024); } while (0)
; #define PG8_MMA(ai, bj, At, Bt) do { __builtin_amdgcn_s_setprio(1); _Pragma("unroll") for (int m = 0; m < 4; ++m) _Pragma("unroll") for (int n = 0; n < 2; ++n) _Pragma("unroll") for (int k = 0; k < 2; ++k) \
;         acc[ai][bj][m][n] = __builtin_amdgcn_mfma_f32_16x16x32_bf16(Bt[n][k], At[m][k], acc[ai][bj][m][n], 0, 0, 0); __builtin_amdgcn_s_setprio(0); } while (0)
; #define PG8_WAIT_V(n) asm volatile("s_waitcnt vmcnt(" #n ")" ::: "memory")
; #define PG8_WAIT_L(n) asm volatile("s_waitcnt lgkmcnt(" #n ")" ::: "memory")
; #define PG8_BAR __builtin_amdgcn_s_barrier()
; #define PG8_SCHED __builtin_amdgcn_sched_barrier(0)
; template <class Epi, class Sched, bool ALIGN_EPI = false>
; __device__ __forceinline__ void gemm_phase(PG8_LAS unsigned char* lds, const Gemm g, const Sched& S, const Epi& E) {
;     ...
;             PG8_WAIT_V(8); PG8_WAIT_L(0); PG8_BAR; PG8_MMA(1, 0, At, B0); PG8_MMA(1, 1, At, B1); PG8_BAR; PG8_SCHED;
;             PG8_LDB(B0, 1, 0); PG8_LDB(B1, 1, 1); PG8_SCHED; PG8_LDA(At, 1, 0); PG8_STAGE(PG8_SA(0, 1), a2 + hstepA, w1);
;             PG8_WAIT_V(8); PG8_WAIT_L(0); PG8_BAR; PG8_MMA(0, 0, At, B0); PG8_MMA(0, 1, At, B1); PG8_BAR; PG8_SCHED;
	v_mfma_f32_16x16x32_bf16 v[42:45], v[162:165], v[186:189], v[42:45]
	v_mfma_f32_16x16x32_bf16 v[30:33], v[142:145], v[194:197], v[30:33]
	v_mfma_f32_16x16x32_bf16 v[26:29], v[162:165], v[194:197], v[26:29]
	v_mfma_f32_16x16x32_bf16 v[14:17], v[142:145], v[202:205], v[14:17]
	v_mfma_f32_16x16x32_bf16 v[10:13], v[162:165], v[202:205], v[10:13]
	v_mfma_f32_16x16x32_bf16 v[6:9], v[142:145], v[210:213], v[6:9]
	v_mfma_f32_16x16x32_bf16 v[2:5], v[162:165], v[210:213], v[2:5]
	v_mfma_f32_16x16x32_bf16 v[54:57], v[158:161], v[190:193], v[54:57]
	v_mfma_f32_16x16x32_bf16 v[42:45], v[166:169], v[190:193], v[42:45]
	v_mfma_f32_16x16x32_bf16 v[30:33], v[158:161], v[198:201], v[30:33]
	v_mfma_f32_16x16x32_bf16 v[26:29], v[166:169], v[198:201], v[26:29]
	v_mfma_f32_16x16x32_bf16 v[14:17], v[158:161], v[206:209], v[14:17]
	v_mfma_f32_16x16x32_bf16 v[10:13], v[166:169], v[206:209], v[10:13]
	v_mfma_f32_16x16x32_bf16 v[6:9], v[158:161], v[214:217], v[6:9]
	v_mfma_f32_16x16x32_bf16 v[2:5], v[166:169], v[214:217], v[2:5]
	v_mfma_f32_16x16x32_bf16 v[70:73], v[170:173], v[186:189], v[70:73]
	v_mfma_f32_16x16x32_bf16 v[66:69], v[178:181], v[186:189], v[66:69]
	v_mfma_f32_16x16x32_bf16 v[50:53], v[170:173], v[194:197], v[50:53]
	v_mfma_f32_16x16x32_bf16 v[46:49], v[178:181], v[194:197], v[46:49]
	v_mfma_f32_16x16x32_bf16 v[38:41], v[170:173], v[202:205], v[38:41]
	v_mfma_f32_16x16x32_bf16 v[34:37], v[178:181], v[202:205], v[34:37]
	v_mfma_f32_16x16x32_bf16 v[22:25], v[170:173], v[210:213], v[22:25]
	v_mfma_f32_16x16x32_bf16 v[18:21], v[178:181], v[210:213], v[18:21]
	v_mfma_f32_16x16x32_bf16 v[70:73], v[174:177], v[190:193], v[70:73]
	v_mfma_f32_16x16x32_bf16 v[66:69], v[182:185], v[190:193], v[66:69]
	v_mfma_f32_16x16x32_bf16 v[50:53], v[174:177], v[198:201], v[50:53]
	v_mfma_f32_16x16x32_bf16 v[46:49], v[182:185], v[198:201], v[46:49]
	v_mfma_f32_16x16x32_bf16 v[38:41], v[174:177], v[206:209], v[38:41]
	v_mfma_f32_16x16x32_bf16 v[34:37], v[182:185], v[206:209], v[34:37]
	v_mfma_f32_16x16x32_bf16 v[22:25], v[174:177], v[214:217], v[22:25]
	v_mfma_f32_16x16x32_bf16 v[18:21], v[182:185], v[214:217], v[18:21]
	s_barrier
	s_add_i32 s93, 0, 0x18000
	s_add_i32 s94, 0, 0x1c000
	v_add_u32_e32 v166, s93, v147
	v_add_u32_e32 v182, s94, v147
	ds_read_b128 v[142:145], v166
	ds_read_b128 v[158:161], v166 offset:1024
	ds_read_b128 v[162:165], v166 offset:2048
	ds_read_b128 v[166:169], v166 offset:3072
	ds_read_b128 v[170:173], v182
	ds_read_b128 v[174:177], v182 offset:1024
	ds_read_b128 v[178:181], v182 offset:2048
	ds_read_b128 v[182:185], v182 offset:3072
	s_add_u32 s64, s64, 0x20000
	s_addc_u32 s65, s65, 0
	s_mov_b32 m0, s68
	v_lshl_add_u64 v[226:227], s[64:65], 0, v[130:131]
	ds_read_b128 v[186:189], v157 offset:32768
	ds_read_b128 v[190:193], v157 offset:33792
	ds_read_b128 v[194:197], v157 offset:34816
	ds_read_b128 v[198:201], v157 offset:35840
	ds_read_b128 v[202:205], v157 offset:36864
	ds_read_b128 v[206:209], v157 offset:37888
	ds_read_b128 v[210:213], v157 offset:38912
	ds_read_b128 v[214:217], v157 offset:39936
	global_load_lds_dwordx4 v[226:227], off
	v_lshl_add_u64 v[226:227], s[64:65], 0, v[134:135]
	s_mov_b32 m0, s69
	s_nop 0
	global_load_lds_dwordx4 v[226:227], off
	s_waitcnt vmcnt(8)
	s_waitcnt lgkmcnt(0)
	v_mfma_f32_16x16x32_bf16 v[126:129], v[142:145], v[186:189], v[126:129]
	s_barrier
	v_mfma_f32_16x16x32_bf16 v[122:125], v[162:165], v[186:189], v[122:125]
	v_mfma_f32_16x16x32_bf16 v[114:117], v[142:145], v[194:197], v[114:117]
	v_mfma_f32_16x16x32_bf16 v[106:109], v[162:165], v[194:197], v[106:109]
	v_mfma_f32_16x16x32_bf16 v[98:101], v[142:145], v[202:205], v[98:101]
	v_mfma_f32_16x16x32_bf16 v[90:93], v[162:165], v[202:205], v[90:93]
	v_mfma_f32_16x16x32_bf16 v[82:85], v[142:145], v[210:213], v[82:85]
	v_mfma_f32_16x16x32_bf16 v[74:77], v[162:165], v[210:213], v[74:77]
	v_mfma_f32_16x16x32_bf16 v[126:129], v[158:161], v[190:193], v[126:129]
	v_mfma_f32_16x16x32_bf16 v[122:125], v[166:169], v[190:193], v[122:125]
	v_mfma_f32_16x16x32_bf16 v[114:117], v[158:161], v[198:201], v[114:117]
	v_mfma_f32_16x16x32_bf16 v[106:109], v[166:169], v[198:201], v[106:109]
	v_mfma_f32_16x16x32_bf16 v[98:101], v[158:161], v[206:209], v[98:101]
	v_mfma_f32_16x16x32_bf16 v[90:93], v[166:169], v[206:209], v[90:93]
	v_mfma_f32_16x16x32_bf16 v[82:85], v[158:161], v[214:217], v[82:85]
	v_mfma_f32_16x16x32_bf16 v[74:77], v[166:169], v[214:217], v[74:77]
	v_mfma_f32_16x16x32_bf16 v[118:121], v[170:173], v[186:189], v[118:121]
	v_mfma_f32_16x16x32_bf16 v[110:113], v[178:181], v[186:189], v[110:113]
	v_mfma_f32_16x16x32_bf16 v[102:105], v[170:173], v[194:197], v[102:105]
	v_mfma_f32_16x16x32_bf16 v[94:97], v[178:181], v[194:197], v[94:97]
	v_mfma_f32_16x16x32_bf16 v[86:89], v[170:173], v[202:205], v[86:89]
	v_mfma_f32_16x16x32_bf16 v[78:81], v[178:181], v[202:205], v[78:81]
	v_mfma_f32_16x16x32_bf16 v[62:65], v[170:173], v[210:213], v[62:65]
	v_mfma_f32_16x16x32_bf16 v[58:61], v[178:181], v[210:213], v[58:61]
	v_mfma_f32_16x16x32_bf16 v[118:121], v[174:177], v[190:193], v[118:121]
	v_mfma_f32_16x16x32_bf16 v[110:113], v[182:185], v[190:193], v[110:113]
	v_mfma_f32_16x16x32_bf16 v[102:105], v[174:177], v[198:201], v[102:105]
	v_mfma_f32_16x16x32_bf16 v[94:97], v[182:185], v[198:201], v[94:97]
	v_mfma_f32_16x16x32_bf16 v[86:89], v[174:177], v[206:209], v[86:89]
	v_mfma_f32_16x16x32_bf16 v[78:81], v[182:185], v[206:209], v[78:81]
	v_mfma_f32_16x16x32_bf16 v[62:65], v[174:177], v[214:217], v[62:65]
	v_mfma_f32_16x16x32_bf16 v[58:61], v[182:185], v[214:217], v[58:61]
	s_barrier
; #define PG8_STAGE(bufoff, gbase, voff) do { _Pragma("unroll") for (int _i = 0; _i < 2; ++_i) \
;         __builtin_amdgcn_global_load_lds((const unsigned*)((const char*)(gbase) + (voff)[_i]), (PG8_LAS unsigned*)(lds + (bufoff) + ldsw + _i * 8192), 16, 0, 0); } while (0)
; #define PG8_LDA(dst, b, h) do { _Pragma("unroll") for (int m = 0; m < 4; ++m) _Pragma("unroll") for (int k = 0; k < 2; ++k) dst[m][k] = *(const PG8_LAS bf16x8*)(lds + PG8_SA(b, h) + aoff + m * 2048 + k * 1024); } while (0)
; #define PG8_MMA(ai, bj, At, Bt) do { __builtin_amdgcn_s_setprio(1); _Pragma("unroll") for (int m = 0; m < 4; ++m) _Pragma("unroll") for (int n = 0; n < 2; ++n) _Pragma("unroll") for (int k = 0; k < 2; ++k) \
;         acc[ai][bj][m][n] = __builtin_amdgcn_mfma_f32_16x16x32_bf16(Bt[n][k], At[m][k], acc[ai][bj][m][n], 0, 0, 0); __builtin_amdgcn_s_setprio(0); } while (0)
; #define PG8_WAIT_V(n) asm volatile("s_waitcnt vmcnt(" #n ")" ::: "memory")
; #define PG8_WAIT_L(n) asm volatile("s_waitcnt lgkmcnt(" #n ")" ::: "memory")
; #define PG8_BAR __builtin_amdgcn_s_barrier()
; #define PG8_SCHED __builtin_amdgcn_sched_barrier(0)
; template <class Epi, class Sched, bool ALIGN_EPI = false>
; __device__ __forceinline__ void gemm_phase(PG8_LAS unsigned char* lds, const Gemm g, const Sched& S, const Epi& E) {
;     ...
;             PG8_LDA(At, 1, 1); PG8_STAGE(PG8_SB(1, 0), b3, voffB); PG8_STAGE(PG8_SB(1, 1), b3 + hstep, voffB); PG8_STAGE(PG8_SA(1, 0), a3, w0);
;             PG8_WAIT_V(8); PG8_WAIT_L(0); PG8_BAR; PG8_MMA(1, 0, At, B0); PG8_MMA(1, 1, At, B1); PG8_BAR; PG8_SCHED;
;             if constexpr (Epi::KSCALE) { if (((t + 2) & 7) == 0 && t + 2 < nt) { E.kscale(acc, pf, ((t + 2) >> 3) - 1, wr, fr); PG8_SCHED; } }
;         }
;         if constexpr (ALIGN_EPI) { if (wr == 0) PG8_BAR; }
	s_add_i32 s64, s93, s66
	v_lshl_add_u64 v[218:219], v[218:219], 0, s[18:19]
	s_mov_b32 m0, s64
	ds_read_b128 v[186:189], v157 offset:49152
	ds_read_b128 v[190:193], v157 offset:50176
	ds_read_b128 v[194:197], v157 offset:51200
	ds_read_b128 v[198:201], v157 offset:52224
	ds_read_b128 v[202:205], v157 offset:53248
	ds_read_b128 v[206:209], v157 offset:54272
	ds_read_b128 v[210:213], v157 offset:55296
	ds_read_b128 v[214:217], v157 offset:56320
	global_load_lds_dwordx4 v[218:219], off
	s_add_i32 m0, s64, 0x2000
	s_add_u32 s62, s62, 0x20080
	v_lshl_add_u64 v[218:219], v[220:221], 0, s[18:19]
	s_addc_u32 s63, s63, 0
	s_add_i32 s64, s94, s66
	global_load_lds_dwordx4 v[218:219], off
	v_lshl_add_u64 v[218:219], s[62:63], 0, v[132:133]
	s_mov_b32 m0, s64
	s_nop 0
	global_load_lds_dwordx4 v[218:219], off
	v_lshl_add_u64 v[218:219], s[62:63], 0, v[136:137]
	s_add_i32 m0, s64, 0x2000
	s_nop 0
	global_load_lds_dwordx4 v[218:219], off
	v_lshl_add_u64 v[218:219], v[222:223], 0, s[18:19]
	s_mov_b32 m0, s73
	s_nop 0
	global_load_lds_dwordx4 v[218:219], off
	v_lshl_add_u64 v[218:219], v[224:225], 0, s[18:19]
	s_mov_b32 m0, s74
	s_nop 0
	global_load_lds_dwordx4 v[218:219], off
	s_waitcnt vmcnt(8)
	s_waitcnt lgkmcnt(0)
	v_mfma_f32_16x16x32_bf16 v[54:57], v[142:145], v[186:189], v[54:57]
	s_barrier
	v_mfma_f32_16x16x32_bf16 v[42:45], v[162:165], v[186:189], v[42:45]
	v_mfma_f32_16x16x32_bf16 v[30:33], v[142:145], v[194:197], v[30:33]
	v_mfma_f32_16x16x32_bf16 v[26:29], v[162:165], v[194:197], v[26:29]
	v_mfma_f32_16x16x32_bf16 v[14:17], v[142:145], v[202:205], v[14:17]
	v_mfma_f32_16x16x32_bf16 v[10:13], v[162:165], v[202:205], v[10:13]
	v_mfma_f32_16x16x32_bf16 v[6:9], v[142:145], v[210:213], v[6:9]
	v_mfma_f32_16x16x32_bf16 v[2:5], v[162:165], v[210:213], v[2:5]
	v_mfma_f32_16x16x32_bf16 v[54:57], v[158:161], v[190:193], v[54:57]
	v_mfma_f32_16x16x32_bf16 v[42:45], v[166:169], v[190:193], v[42:45]
	v_mfma_f32_16x16x32_bf16 v[30:33], v[158:161], v[198:201], v[30:33]
	v_mfma_f32_16x16x32_bf16 v[26:29], v[166:169], v[198:201], v[26:29]
	v_mfma_f32_16x16x32_bf16 v[14:17], v[158:161], v[206:209], v[14:17]
	v_mfma_f32_16x16x32_bf16 v[10:13], v[166:169], v[206:209], v[10:13]
	v_mfma_f32_16x16x32_bf16 v[6:9], v[158:161], v[214:217], v[6:9]
	v_mfma_f32_16x16x32_bf16 v[2:5], v[166:169], v[214:217], v[2:5]
	v_mfma_f32_16x16x32_bf16 v[70:73], v[170:173], v[186:189], v[70:73]
	v_mfma_f32_16x16x32_bf16 v[66:69], v[178:181], v[186:189], v[66:69]
	v_mfma_f32_16x16x32_bf16 v[50:53], v[170:173], v[194:197], v[50:53]
	v_mfma_f32_16x16x32_bf16 v[46:49], v[178:181], v[194:197], v[46:49]
	v_mfma_f32_16x16x32_bf16 v[38:41], v[170:173], v[202:205], v[38:41]
	v_mfma_f32_16x16x32_bf16 v[34:37], v[178:181], v[202:205], v[34:37]
	v_mfma_f32_16x16x32_bf16 v[22:25], v[170:173], v[210:213], v[22:25]
	v_mfma_f32_16x16x32_bf16 v[18:21], v[178:181], v[210:213], v[18:21]
	v_mfma_f32_16x16x32_bf16 v[70:73], v[174:177], v[190:193], v[70:73]
	v_mfma_f32_16x16x32_bf16 v[66:69], v[182:185], v[190:193], v[66:69]
	v_mfma_f32_16x16x32_bf16 v[50:53], v[174:177], v[198:201], v[50:53]
	v_mfma_f32_16x16x32_bf16 v[46:49], v[182:185], v[198:201], v[46:49]
	v_mfma_f32_16x16x32_bf16 v[38:41], v[174:177], v[206:209], v[38:41]
	v_mfma_f32_16x16x32_bf16 v[34:37], v[182:185], v[206:209], v[34:37]
	v_mfma_f32_16x16x32_bf16 v[22:25], v[174:177], v[214:217], v[22:25]
	v_mfma_f32_16x16x32_bf16 v[18:21], v[182:185], v[214:217], v[18:21]
	s_barrier
	s_add_i32 s92, s92, 2
	s_add_u32 s90, s90, 0x100
	s_addc_u32 s91, s91, 0
	s_add_u32 s60, s60, 0x100
	s_addc_u32 s61, s61, 0
	s_cmp_gt_u32 s92, 5
	s_cbranch_scc0 .LBB0_805
	s_and_b64 vcc, exec, s[22:23]
	s_cbranch_vccz .LBB0_808
	s_barrier

; #define PG8_STAGE(bufoff, gbase, voff) do { _Pragma("unroll") for (int _i = 0; _i < 2; ++_i) \
;         __builtin_amdgcn_global_load_lds((const unsigned*)((const char*)(gbase) + (voff)[_i]), (PG8_LAS unsigned*)(lds + (bufoff) + ldsw + _i * 8192), 16, 0, 0); } while (0)
; #define PG8_LDA(dst, b, h) do { _Pragma("unroll") for (int m = 0; m < 4; ++m) _Pragma("unroll") for (int k = 0; k < 2; ++k) dst[m][k] = *(const PG8_LAS bf16x8*)(lds + PG8_SA(b, h) + aoff + m * 2048 + k * 1024); } while (0)
; #define PG8_LDB(dst, b, h) do { _Pragma("unroll") for (int n = 0; n < 2; ++n) _Pragma("unroll") for (int k = 0; k < 2; ++k) dst[n][k] = *(const PG8_LAS bf16x8*)(lds + PG8_SB(b, h) + boff + n * 2048 + k * 1024); } while (0)
; #define PG8_MMA(ai, bj, At, Bt) do { __builtin_amdgcn_s_setprio(1); _Pragma("unroll") for (int m = 0; m < 4; ++m) _Pragma("unroll") for (int n = 0; n < 2; ++n) _Pragma("unroll") for (int k = 0; k < 2; ++k) \
;         acc[ai][bj][m][n] = __builtin_amdgcn_mfma_f32_16x16x32_bf16(Bt[n][k], At[m][k], acc[ai][bj][m][n], 0, 0, 0); __builtin_amdgcn_s_setprio(0); } while (0)
; template <class Epi, class Sched, bool ALIGN_EPI = false>
; __device__ __forceinline__ void gemm_phase(PG8_LAS unsigned char* lds, const Gemm g, const Sched& S, const Epi& E) {
;     ...
;         for (int t = 0; t < nt; t += 2) {
;             const bool last = (t == nt - 2);
;             const char* a1 = cA + (size_t)(t + 1) * kstep;
;             const char* a2 = last ? nA : cA + (size_t)(t + 2) * kstep; const char* b2 = last ? nB : cB + (size_t)(t + 2) * kstep;
;             const char* a3 = a2 + kstep; const char* b3 = b2 + kstep;
;             unsigned w0[2], w1[2];
; #pragma unroll
;             for (int i = 0; i < 2; ++i) { w0[i] = (Sched::GATHER && last) ? vn0[i] : vc0[i]; w1[i] = (Sched::GATHER && last) ? vn1[i] : vc1[i]; }
;             if (last && has_next) S.a_ready(nxt);
;             PG8_LDB(B0, 0, 0); PG8_LDB(B1, 0, 1); PG8_SCHED; PG8_LDA(At, 0, 0); PG8_STAGE(PG8_SA(1, 1), a1 + hstepA, vc1);
;             PG8_WAIT_V(8); PG8_WAIT_L(0); PG8_BAR; PG8_MMA(0, 0, At, B0); PG8_MMA(0, 1, At, B1); PG8_BAR; PG8_SCHED;
;             PG8_LDA(At, 0, 1); PG8_STAGE(PG8_SB(0, 0), b2, voffB); PG8_STAGE(PG8_SB(0, 1), b2 + hstep, voffB); PG8_STAGE(PG8_SA(0, 0), a2, w0);
;             PG8_WAIT_V(8); PG8_WAIT_L(0); PG8_BAR; PG8_MMA(1, 0, At, B0); PG8_MMA(1, 1, At, B1); PG8_BAR; PG8_SCHED;
.LBB0_908:
	ds_read_b128 v[144:147], v157
	ds_read_b128 v[160:163], v157 offset:1024
	ds_read_b128 v[164:167], v157 offset:2048
	ds_read_b128 v[168:171], v157 offset:3072
	ds_read_b128 v[172:175], v158
	ds_read_b128 v[176:179], v158 offset:1024
	ds_read_b128 v[180:183], v158 offset:2048
	ds_read_b128 v[184:187], v158 offset:3072
	s_add_u32 s58, s56, 0xfffe0080
	s_addc_u32 s59, s57, -1
	s_cmp_eq_u32 s92, 4
	s_cselect_b32 s61, s41, s59
	s_cselect_b32 s60, s47, s58
	s_cselect_b32 s59, s43, s91
	s_cselect_b32 s58, s89, s90
	v_lshl_add_u64 v[220:221], s[56:57], 0, v[142:143]
	s_add_i32 m0, s49, 0xc000
	ds_read_b128 v[188:191], v159
	ds_read_b128 v[192:195], v159 offset:1024
	ds_read_b128 v[196:199], v159 offset:2048
	ds_read_b128 v[200:203], v159 offset:3072
	ds_read_b128 v[204:207], v159 offset:4096
	ds_read_b128 v[208:211], v159 offset:5120
	ds_read_b128 v[212:215], v159 offset:6144
	ds_read_b128 v[216:219], v159 offset:7168
	global_load_lds_dwordx4 v[220:221], off
	v_lshl_add_u64 v[220:221], s[56:57], 0, v[140:141]
	s_add_i32 m0, s49, 0xe000
	s_nop 0
	global_load_lds_dwordx4 v[220:221], off
	s_waitcnt vmcnt(8)
	s_waitcnt lgkmcnt(0)
	v_mfma_f32_16x16x32_bf16 v[126:129], v[144:147], v[188:191], v[126:129]
	s_barrier
	v_mfma_f32_16x16x32_bf16 v[122:125], v[164:167], v[188:191], v[122:125]
	v_mfma_f32_16x16x32_bf16 v[114:117], v[144:147], v[196:199], v[114:117]
	v_mfma_f32_16x16x32_bf16 v[106:109], v[164:167], v[196:199], v[106:109]
	v_mfma_f32_16x16x32_bf16 v[98:101], v[144:147], v[204:207], v[98:101]
	v_mfma_f32_16x16x32_bf16 v[90:93], v[164:167], v[204:207], v[90:93]
	v_mfma_f32_16x16x32_bf16 v[82:85], v[144:147], v[212:215], v[82:85]
	v_mfma_f32_16x16x32_bf16 v[74:77], v[164:167], v[212:215], v[74:77]
	v_mfma_f32_16x16x32_bf16 v[126:129], v[160:163], v[192:195], v[126:129]
	v_mfma_f32_16x16x32_bf16 v[122:125], v[168:171], v[192:195], v[122:125]
	v_mfma_f32_16x16x32_bf16 v[114:117], v[160:163], v[200:203], v[114:117]
	v_mfma_f32_16x16x32_bf16 v[106:109], v[168:171], v[200:203], v[106:109]
	v_mfma_f32_16x16x32_bf16 v[98:101], v[160:163], v[208:211], v[98:101]
	v_mfma_f32_16x16x32_bf16 v[90:93], v[168:171], v[208:211], v[90:93]
	v_mfma_f32_16x16x32_bf16 v[82:85], v[160:163], v[216:219], v[82:85]
	v_mfma_f32_16x16x32_bf16 v[74:77], v[168:171], v[216:219], v[74:77]
	v_mfma_f32_16x16x32_bf16 v[118:121], v[172:175], v[188:191], v[118:121]
	v_mfma_f32_16x16x32_bf16 v[110:113], v[180:183], v[188:191], v[110:113]
	v_mfma_f32_16x16x32_bf16 v[102:105], v[172:175], v[196:199], v[102:105]
	v_mfma_f32_16x16x32_bf16 v[94:97], v[180:183], v[196:199], v[94:97]
	v_mfma_f32_16x16x32_bf16 v[86:89], v[172:175], v[204:207], v[86:89]
	v_mfma_f32_16x16x32_bf16 v[78:81], v[180:183], v[204:207], v[78:81]
	v_mfma_f32_16x16x32_bf16 v[62:65], v[172:175], v[212:215], v[62:65]
	v_mfma_f32_16x16x32_bf16 v[58:61], v[180:183], v[212:215], v[58:61]
	v_mfma_f32_16x16x32_bf16 v[118:121], v[176:179], v[192:195], v[118:121]
	v_mfma_f32_16x16x32_bf16 v[110:113], v[184:187], v[192:195], v[110:113]
	v_mfma_f32_16x16x32_bf16 v[102:105], v[176:179], v[200:203], v[102:105]
	v_mfma_f32_16x16x32_bf16 v[94:97], v[184:187], v[200:203], v[94:97]
	v_mfma_f32_16x16x32_bf16 v[86:89], v[176:179], v[208:211], v[86:89]
	v_mfma_f32_16x16x32_bf16 v[78:81], v[184:187], v[208:211], v[78:81]
	v_mfma_f32_16x16x32_bf16 v[62:65], v[176:179], v[216:219], v[62:65]
	v_mfma_f32_16x16x32_bf16 v[58:61], v[184:187], v[216:219], v[58:61]
	s_barrier
	s_add_i32 s93, s79, s66
	v_lshl_add_u64 v[220:221], s[58:59], 0, v[134:135]
	s_mov_b32 m0, s93
	ds_read_b128 v[188:191], v159 offset:16384
	ds_read_b128 v[192:195], v159 offset:17408
	ds_read_b128 v[196:199], v159 offset:18432
	ds_read_b128 v[200:203], v159 offset:19456
	ds_read_b128 v[204:207], v159 offset:20480
	ds_read_b128 v[208:211], v159 offset:21504
	ds_read_b128 v[212:215], v159 offset:22528
	ds_read_b128 v[216:219], v159 offset:23552
	global_load_lds_dwordx4 v[220:221], off
	s_add_i32 m0, s93, 0x2000
	s_add_u32 s94, s58, 0x20000
	v_lshl_add_u64 v[222:223], s[58:59], 0, v[138:139]
	s_addc_u32 s95, s59, 0
	s_add_i32 s93, s80, s66
	global_load_lds_dwordx4 v[222:223], off
	v_lshl_add_u64 v[224:225], s[94:95], 0, v[134:135]
	s_mov_b32 m0, s93
	v_lshl_add_u64 v[226:227], s[60:61], 0, v[136:137]
	global_load_lds_dwordx4 v[224:225], off
	v_lshl_add_u64 v[224:225], s[94:95], 0, v[138:139]
	s_add_i32 m0, s93, 0x2000
	s_nop 0
	global_load_lds_dwordx4 v[224:225], off
	v_lshl_add_u64 v[224:225], s[60:61], 0, v[132:133]
	s_mov_b32 m0, s49
	s_nop 0
	global_load_lds_dwordx4 v[224:225], off
	s_mov_b32 m0, s67
	s_nop 0
	global_load_lds_dwordx4 v[226:227], off
	s_waitcnt vmcnt(8)
	s_waitcnt lgkmcnt(0)
	v_mfma_f32_16x16x32_bf16 v[54:57], v[144:147], v[188:191], v[54:57]
	s_barrier
; #define PG8_STAGE(bufoff, gbase, voff) do { _Pragma("unroll") for (int _i = 0; _i < 2; ++_i) \
;         __builtin_amdgcn_global_load_lds((const unsigned*)((const char*)(gbase) + (voff)[_i]), (PG8_LAS unsigned*)(lds + (bufoff) + ldsw + _i * 8192), 16, 0, 0); } while (0)
; #define PG8_LDA(dst, b, h) do { _Pragma("unroll") for (int m = 0; m < 4; ++m) _Pragma("unroll") for (int k = 0; k < 2; ++k) dst[m][k] = *(const PG8_LAS bf16x8*)(lds + PG8_SA(b, h) + aoff + m * 2048 + k * 1024); } while (0)
; #define PG8_LDB(dst, b, h) do { _Pragma("unroll") for (int n = 0; n < 2; ++n) _Pragma("unroll") for (int k = 0; k < 2; ++k) dst[n][k] = *(const PG8_LAS bf16x8*)(lds + PG8_SB(b, h) + boff + n * 2048 + k * 1024); } while (0)
; #define PG8_MMA(ai, bj, At, Bt) do { __builtin_amdgcn_s_setprio(1); _Pragma("unroll") for (int m = 0; m < 4; ++m) _Pragma("unroll") for (int n = 0; n < 2; ++n) _Pragma("unroll") for (int k = 0; k < 2; ++k) \
;         acc[ai][bj][m][n] = __builtin_amdgcn_mfma_f32_16x16x32_bf16(Bt[n][k], At[m][k], acc[ai][bj][m][n], 0, 0, 0); __builtin_amdgcn_s_setprio(0); } while (0)
; #define PG8_WAIT_V(n) asm volatile("s_waitcnt vmcnt(" #n ")" ::: "memory")
; #define PG8_WAIT_L(n) asm volatile("s_waitcnt lgkmcnt(" #n ")" ::: "memory")
; #define PG8_BAR __builtin_amdgcn_s_barrier()
; #define PG8_SCHED __builtin_amdgcn_sched_barrier(0)
; template <class Epi, class Sched, bool ALIGN_EPI = false>
; __device__ __forceinline__ void gemm_phase(PG8_LAS unsigned char* lds, const Gemm g, const Sched& S, const Epi& E) {
;     ...
;             PG8_WAIT_V(8); PG8_WAIT_L(0); PG8_BAR; PG8_MMA(1, 0, At, B0); PG8_MMA(1, 1, At, B1); PG8_BAR; PG8_SCHED;
;             PG8_LDB(B0, 1, 0); PG8_LDB(B1, 1, 1); PG8_SCHED; PG8_LDA(At, 1, 0); PG8_STAGE(PG8_SA(0, 1), a2 + hstepA, w1);
;             PG8_WAIT_V(8); PG8_WAIT_L(0); PG8_BAR; PG8_MMA(0, 0, At, B0); PG8_MMA(0, 1, At, B1); PG8_BAR; PG8_SCHED;
	v_mfma_f32_16x16x32_bf16 v[42:45], v[164:167], v[188:191], v[42:45]
	v_mfma_f32_16x16x32_bf16 v[30:33], v[144:147], v[196:199], v[30:33]
	v_mfma_f32_16x16x32_bf16 v[26:29], v[164:167], v[196:199], v[26:29]
	v_mfma_f32_16x16x32_bf16 v[14:17], v[144:147], v[204:207], v[14:17]
	v_mfma_f32_16x16x32_bf16 v[10:13], v[164:167], v[204:207], v[10:13]
	v_mfma_f32_16x16x32_bf16 v[6:9], v[144:147], v[212:215], v[6:9]
	v_mfma_f32_16x16x32_bf16 v[2:5], v[164:167], v[212:215], v[2:5]
	v_mfma_f32_16x16x32_bf16 v[54:57], v[160:163], v[192:195], v[54:57]
	v_mfma_f32_16x16x32_bf16 v[42:45], v[168:171], v[192:195], v[42:45]
	v_mfma_f32_16x16x32_bf16 v[30:33], v[160:163], v[200:203], v[30:33]
	v_mfma_f32_16x16x32_bf16 v[26:29], v[168:171], v[200:203], v[26:29]
	v_mfma_f32_16x16x32_bf16 v[14:17], v[160:163], v[208:211], v[14:17]
	v_mfma_f32_16x16x32_bf16 v[10:13], v[168:171], v[208:211], v[10:13]
	v_mfma_f32_16x16x32_bf16 v[6:9], v[160:163], v[216:219], v[6:9]
	v_mfma_f32_16x16x32_bf16 v[2:5], v[168:171], v[216:219], v[2:5]
	v_mfma_f32_16x16x32_bf16 v[70:73], v[172:175], v[188:191], v[70:73]
	v_mfma_f32_16x16x32_bf16 v[66:69], v[180:183], v[188:191], v[66:69]
	v_mfma_f32_16x16x32_bf16 v[50:53], v[172:175], v[196:199], v[50:53]
	v_mfma_f32_16x16x32_bf16 v[46:49], v[180:183], v[196:199], v[46:49]
	v_mfma_f32_16x16x32_bf16 v[38:41], v[172:175], v[204:207], v[38:41]
	v_mfma_f32_16x16x32_bf16 v[34:37], v[180:183], v[204:207], v[34:37]
	v_mfma_f32_16x16x32_bf16 v[22:25], v[172:175], v[212:215], v[22:25]
	v_mfma_f32_16x16x32_bf16 v[18:21], v[180:183], v[212:215], v[18:21]
	v_mfma_f32_16x16x32_bf16 v[70:73], v[176:179], v[192:195], v[70:73]
	v_mfma_f32_16x16x32_bf16 v[66:69], v[184:187], v[192:195], v[66:69]
	v_mfma_f32_16x16x32_bf16 v[50:53], v[176:179], v[200:203], v[50:53]
	v_mfma_f32_16x16x32_bf16 v[46:49], v[184:187], v[200:203], v[46:49]
	v_mfma_f32_16x16x32_bf16 v[38:41], v[176:179], v[208:211], v[38:41]
	v_mfma_f32_16x16x32_bf16 v[34:37], v[184:187], v[208:211], v[34:37]
	v_mfma_f32_16x16x32_bf16 v[22:25], v[176:179], v[216:219], v[22:25]
	v_mfma_f32_16x16x32_bf16 v[18:21], v[184:187], v[216:219], v[18:21]
	s_barrier
	s_add_i32 s93, 0, 0x18000
	s_add_i32 s94, 0, 0x1c000
	v_add_u32_e32 v168, s93, v148
	v_add_u32_e32 v184, s94, v148
	ds_read_b128 v[144:147], v168
	ds_read_b128 v[160:163], v168 offset:1024
	ds_read_b128 v[164:167], v168 offset:2048
	ds_read_b128 v[168:171], v168 offset:3072
	ds_read_b128 v[172:175], v184
	ds_read_b128 v[176:179], v184 offset:1024
	ds_read_b128 v[180:183], v184 offset:2048
	ds_read_b128 v[184:187], v184 offset:3072
	s_add_u32 s60, s60, 0x20000
	s_addc_u32 s61, s61, 0
	s_mov_b32 m0, s68
	v_lshl_add_u64 v[228:229], s[60:61], 0, v[132:133]
	ds_read_b128 v[188:191], v159 offset:32768
	ds_read_b128 v[192:195], v159 offset:33792
	ds_read_b128 v[196:199], v159 offset:34816
	ds_read_b128 v[200:203], v159 offset:35840
	ds_read_b128 v[204:207], v159 offset:36864
	ds_read_b128 v[208:211], v159 offset:37888
	ds_read_b128 v[212:215], v159 offset:38912
	ds_read_b128 v[216:219], v159 offset:39936
	global_load_lds_dwordx4 v[228:229], off
	v_lshl_add_u64 v[228:229], s[60:61], 0, v[136:137]
	s_mov_b32 m0, s69
	s_nop 0
	global_load_lds_dwordx4 v[228:229], off
	s_waitcnt vmcnt(8)
	s_waitcnt lgkmcnt(0)
	v_mfma_f32_16x16x32_bf16 v[126:129], v[144:147], v[188:191], v[126:129]
	s_barrier
	v_mfma_f32_16x16x32_bf16 v[122:125], v[164:167], v[188:191], v[122:125]
	v_mfma_f32_16x16x32_bf16 v[114:117], v[144:147], v[196:199], v[114:117]
	v_mfma_f32_16x16x32_bf16 v[106:109], v[164:167], v[196:199], v[106:109]
	v_mfma_f32_16x16x32_bf16 v[98:101], v[144:147], v[204:207], v[98:101]
	v_mfma_f32_16x16x32_bf16 v[90:93], v[164:167], v[204:207], v[90:93]
	v_mfma_f32_16x16x32_bf16 v[82:85], v[144:147], v[212:215], v[82:85]
	v_mfma_f32_16x16x32_bf16 v[74:77], v[164:167], v[212:215], v[74:77]
	v_mfma_f32_16x16x32_bf16 v[126:129], v[160:163], v[192:195], v[126:129]
	v_mfma_f32_16x16x32_bf16 v[122:125], v[168:171], v[192:195], v[122:125]
	v_mfma_f32_16x16x32_bf16 v[114:117], v[160:163], v[200:203], v[114:117]
	v_mfma_f32_16x16x32_bf16 v[106:109], v[168:171], v[200:203], v[106:109]
	v_mfma_f32_16x16x32_bf16 v[98:101], v[160:163], v[208:211], v[98:101]
	v_mfma_f32_16x16x32_bf16 v[90:93], v[168:171], v[208:211], v[90:93]
	v_mfma_f32_16x16x32_bf16 v[82:85], v[160:163], v[216:219], v[82:85]
	v_mfma_f32_16x16x32_bf16 v[74:77], v[168:171], v[216:219], v[74:77]
	v_mfma_f32_16x16x32_bf16 v[118:121], v[172:175], v[188:191], v[118:121]
	v_mfma_f32_16x16x32_bf16 v[110:113], v[180:183], v[188:191], v[110:113]
	v_mfma_f32_16x16x32_bf16 v[102:105], v[172:175], v[196:199], v[102:105]
	v_mfma_f32_16x16x32_bf16 v[94:97], v[180:183], v[196:199], v[94:97]
	v_mfma_f32_16x16x32_bf16 v[86:89], v[172:175], v[204:207], v[86:89]
	v_mfma_f32_16x16x32_bf16 v[78:81], v[180:183], v[204:207], v[78:81]
	v_mfma_f32_16x16x32_bf16 v[62:65], v[172:175], v[212:215], v[62:65]
	v_mfma_f32_16x16x32_bf16 v[58:61], v[180:183], v[212:215], v[58:61]
	v_mfma_f32_16x16x32_bf16 v[118:121], v[176:179], v[192:195], v[118:121]
	v_mfma_f32_16x16x32_bf16 v[110:113], v[184:187], v[192:195], v[110:113]
	v_mfma_f32_16x16x32_bf16 v[102:105], v[176:179], v[200:203], v[102:105]
	v_mfma_f32_16x16x32_bf16 v[94:97], v[184:187], v[200:203], v[94:97]
	v_mfma_f32_16x16x32_bf16 v[86:89], v[176:179], v[208:211], v[86:89]
	v_mfma_f32_16x16x32_bf16 v[78:81], v[184:187], v[208:211], v[78:81]
	v_mfma_f32_16x16x32_bf16 v[62:65], v[176:179], v[216:219], v[62:65]
	v_mfma_f32_16x16x32_bf16 v[58:61], v[184:187], v[216:219], v[58:61]
	s_barrier
; #define PG8_STAGE(bufoff, gbase, voff) do { _Pragma("unroll") for (int _i = 0; _i < 2; ++_i) \
;         __builtin_amdgcn_global_load_lds((const unsigned*)((const char*)(gbase) + (voff)[_i]), (PG8_LAS unsigned*)(lds + (bufoff) + ldsw + _i * 8192), 16, 0, 0); } while (0)
; #define PG8_LDA(dst, b, h) do { _Pragma("unroll") for (int m = 0; m < 4; ++m) _Pragma("unroll") for (int k = 0; k < 2; ++k) dst[m][k] = *(const PG8_LAS bf16x8*)(lds + PG8_SA(b, h) + aoff + m * 2048 + k * 1024); } while (0)
; #define PG8_MMA(ai, bj, At, Bt) do { __builtin_amdgcn_s_setprio(1); _Pragma("unroll") for (int m = 0; m < 4; ++m) _Pragma("unroll") for (int n = 0; n < 2; ++n) _Pragma("unroll") for (int k = 0; k < 2; ++k) \
;         acc[ai][bj][m][n] = __builtin_amdgcn_mfma_f32_16x16x32_bf16(Bt[n][k], At[m][k], acc[ai][bj][m][n], 0, 0, 0); __builtin_amdgcn_s_setprio(0); } while (0)
; #define PG8_WAIT_V(n) asm volatile("s_waitcnt vmcnt(" #n ")" ::: "memory")
; #define PG8_WAIT_L(n) asm volatile("s_waitcnt lgkmcnt(" #n ")" ::: "memory")
; #define PG8_BAR __builtin_amdgcn_s_barrier()
; #define PG8_SCHED __builtin_amdgcn_sched_barrier(0)
; template <class Epi, class Sched, bool ALIGN_EPI = false>
; __device__ __forceinline__ void gemm_phase(PG8_LAS unsigned char* lds, const Gemm g, const Sched& S, const Epi& E) {
;     ...
;             PG8_LDA(At, 1, 1); PG8_STAGE(PG8_SB(1, 0), b3, voffB); PG8_STAGE(PG8_SB(1, 1), b3 + hstep, voffB); PG8_STAGE(PG8_SA(1, 0), a3, w0);
;             PG8_WAIT_V(8); PG8_WAIT_L(0); PG8_BAR; PG8_MMA(1, 0, At, B0); PG8_MMA(1, 1, At, B1); PG8_BAR; PG8_SCHED;
;             if constexpr (Epi::KSCALE) { if (((t + 2) & 7) == 0 && t + 2 < nt) { E.kscale(acc, pf, ((t + 2) >> 3) - 1, wr, fr); PG8_SCHED; } }
;         }
;         if constexpr (ALIGN_EPI) { if (wr == 0) PG8_BAR; }
	s_add_i32 s60, s93, s66
	v_lshl_add_u64 v[220:221], v[220:221], 0, s[14:15]
	s_mov_b32 m0, s60
	ds_read_b128 v[188:191], v159 offset:49152
	ds_read_b128 v[192:195], v159 offset:50176
	ds_read_b128 v[196:199], v159 offset:51200
	ds_read_b128 v[200:203], v159 offset:52224
	ds_read_b128 v[204:207], v159 offset:53248
	ds_read_b128 v[208:211], v159 offset:54272
	ds_read_b128 v[212:215], v159 offset:55296
	ds_read_b128 v[216:219], v159 offset:56320
	global_load_lds_dwordx4 v[220:221], off
	s_add_i32 m0, s60, 0x2000
	s_add_u32 s58, s58, 0x20080
	v_lshl_add_u64 v[220:221], v[222:223], 0, s[14:15]
	s_addc_u32 s59, s59, 0
	s_add_i32 s60, s94, s66
	global_load_lds_dwordx4 v[220:221], off
	v_lshl_add_u64 v[220:221], s[58:59], 0, v[134:135]
	s_mov_b32 m0, s60
	s_nop 0
	global_load_lds_dwordx4 v[220:221], off
	v_lshl_add_u64 v[220:221], s[58:59], 0, v[138:139]
	s_add_i32 m0, s60, 0x2000
	s_nop 0
	global_load_lds_dwordx4 v[220:221], off
	v_lshl_add_u64 v[220:221], v[224:225], 0, s[14:15]
	s_mov_b32 m0, s74
	s_nop 0
	global_load_lds_dwordx4 v[220:221], off
	v_lshl_add_u64 v[220:221], v[226:227], 0, s[14:15]
	s_mov_b32 m0, s75
	s_nop 0
	global_load_lds_dwordx4 v[220:221], off
	s_waitcnt vmcnt(8)
	s_waitcnt lgkmcnt(0)
	v_mfma_f32_16x16x32_bf16 v[54:57], v[144:147], v[188:191], v[54:57]
	s_barrier
	v_mfma_f32_16x16x32_bf16 v[42:45], v[164:167], v[188:191], v[42:45]
	v_mfma_f32_16x16x32_bf16 v[30:33], v[144:147], v[196:199], v[30:33]
	v_mfma_f32_16x16x32_bf16 v[26:29], v[164:167], v[196:199], v[26:29]
	v_mfma_f32_16x16x32_bf16 v[14:17], v[144:147], v[204:207], v[14:17]
	v_mfma_f32_16x16x32_bf16 v[10:13], v[164:167], v[204:207], v[10:13]
	v_mfma_f32_16x16x32_bf16 v[6:9], v[144:147], v[212:215], v[6:9]
	v_mfma_f32_16x16x32_bf16 v[2:5], v[164:167], v[212:215], v[2:5]
	v_mfma_f32_16x16x32_bf16 v[54:57], v[160:163], v[192:195], v[54:57]
	v_mfma_f32_16x16x32_bf16 v[42:45], v[168:171], v[192:195], v[42:45]
	v_mfma_f32_16x16x32_bf16 v[30:33], v[160:163], v[200:203], v[30:33]
	v_mfma_f32_16x16x32_bf16 v[26:29], v[168:171], v[200:203], v[26:29]
	v_mfma_f32_16x16x32_bf16 v[14:17], v[160:163], v[208:211], v[14:17]
	v_mfma_f32_16x16x32_bf16 v[10:13], v[168:171], v[208:211], v[10:13]
	v_mfma_f32_16x16x32_bf16 v[6:9], v[160:163], v[216:219], v[6:9]
	v_mfma_f32_16x16x32_bf16 v[2:5], v[168:171], v[216:219], v[2:5]
	v_mfma_f32_16x16x32_bf16 v[70:73], v[172:175], v[188:191], v[70:73]
	v_mfma_f32_16x16x32_bf16 v[66:69], v[180:183], v[188:191], v[66:69]
	v_mfma_f32_16x16x32_bf16 v[50:53], v[172:175], v[196:199], v[50:53]
	v_mfma_f32_16x16x32_bf16 v[46:49], v[180:183], v[196:199], v[46:49]
	v_mfma_f32_16x16x32_bf16 v[38:41], v[172:175], v[204:207], v[38:41]
	v_mfma_f32_16x16x32_bf16 v[34:37], v[180:183], v[204:207], v[34:37]
	v_mfma_f32_16x16x32_bf16 v[22:25], v[172:175], v[212:215], v[22:25]
	v_mfma_f32_16x16x32_bf16 v[18:21], v[180:183], v[212:215], v[18:21]
	v_mfma_f32_16x16x32_bf16 v[70:73], v[176:179], v[192:195], v[70:73]
	v_mfma_f32_16x16x32_bf16 v[66:69], v[184:187], v[192:195], v[66:69]
	v_mfma_f32_16x16x32_bf16 v[50:53], v[176:179], v[200:203], v[50:53]
	v_mfma_f32_16x16x32_bf16 v[46:49], v[184:187], v[200:203], v[46:49]
	v_mfma_f32_16x16x32_bf16 v[38:41], v[176:179], v[208:211], v[38:41]
	v_mfma_f32_16x16x32_bf16 v[34:37], v[184:187], v[208:211], v[34:37]
	v_mfma_f32_16x16x32_bf16 v[22:25], v[176:179], v[216:219], v[22:25]
	v_mfma_f32_16x16x32_bf16 v[18:21], v[184:187], v[216:219], v[18:21]
	s_barrier
	s_add_i32 s92, s92, 2
	s_add_u32 s90, s90, 0x100
	s_addc_u32 s91, s91, 0
	s_add_u32 s56, s56, 0x100
	s_addc_u32 s57, s57, 0
	s_cmp_gt_u32 s92, 5
	s_cbranch_scc0 .LBB0_908
	s_and_b64 vcc, exec, s[16:17]
	s_cbranch_vccz .LBB0_911
	s_barrier

; #define PG8_STAGE(bufoff, gbase, voff) do { _Pragma("unroll") for (int _i = 0; _i < 2; ++_i) \
;         __builtin_amdgcn_global_load_lds((const unsigned*)((const char*)(gbase) + (voff)[_i]), (PG8_LAS unsigned*)(lds + (bufoff) + ldsw + _i * 8192), 16, 0, 0); } while (0)
; #define PG8_LDA(dst, b, h) do { _Pragma("unroll") for (int m = 0; m < 4; ++m) _Pragma("unroll") for (int k = 0; k < 2; ++k) dst[m][k] = *(const PG8_LAS bf16x8*)(lds + PG8_SA(b, h) + aoff + m * 2048 + k * 1024); } while (0)
; #define PG8_LDB(dst, b, h) do { _Pragma("unroll") for (int n = 0; n < 2; ++n) _Pragma("unroll") for (int k = 0; k < 2; ++k) dst[n][k] = *(const PG8_LAS bf16x8*)(lds + PG8_SB(b, h) + boff + n * 2048 + k * 1024); } while (0)
; #define PG8_MMA(ai, bj, At, Bt) do { __builtin_amdgcn_s_setprio(1); _Pragma("unroll") for (int m = 0; m < 4; ++m) _Pragma("unroll") for (int n = 0; n < 2; ++n) _Pragma("unroll") for (int k = 0; k < 2; ++k) \
;         acc[ai][bj][m][n] = __builtin_amdgcn_mfma_f32_16x16x32_bf16(Bt[n][k], At[m][k], acc[ai][bj][m][n], 0, 0, 0); __builtin_amdgcn_s_setprio(0); } while (0)
; template <class Epi, class Sched, bool ALIGN_EPI = false>
; __device__ __forceinline__ void gemm_phase(PG8_LAS unsigned char* lds, const Gemm g, const Sched& S, const Epi& E) {
;     ...
;         for (int t = 0; t < nt; t += 2) {
;             const bool last = (t == nt - 2);
;             const char* a1 = cA + (size_t)(t + 1) * kstep;
;             const char* a2 = last ? nA : cA + (size_t)(t + 2) * kstep; const char* b2 = last ? nB : cB + (size_t)(t + 2) * kstep;
;             const char* a3 = a2 + kstep; const char* b3 = b2 + kstep;
;             unsigned w0[2], w1[2];
; #pragma unroll
;             for (int i = 0; i < 2; ++i) { w0[i] = (Sched::GATHER && last) ? vn0[i] : vc0[i]; w1[i] = (Sched::GATHER && last) ? vn1[i] : vc1[i]; }
;             if (last && has_next) S.a_ready(nxt);
;             PG8_LDB(B0, 0, 0); PG8_LDB(B1, 0, 1); PG8_SCHED; PG8_LDA(At, 0, 0); PG8_STAGE(PG8_SA(1, 1), a1 + hstepA, vc1);
;             PG8_WAIT_V(8); PG8_WAIT_L(0); PG8_BAR; PG8_MMA(0, 0, At, B0); PG8_MMA(0, 1, At, B1); PG8_BAR; PG8_SCHED;
;             PG8_LDA(At, 0, 1); PG8_STAGE(PG8_SB(0, 0), b2, voffB); PG8_STAGE(PG8_SB(0, 1), b2 + hstep, voffB); PG8_STAGE(PG8_SA(0, 0), a2, w0);
;             PG8_WAIT_V(8); PG8_WAIT_L(0); PG8_BAR; PG8_MMA(1, 0, At, B0); PG8_MMA(1, 1, At, B1); PG8_BAR; PG8_SCHED;
.LBB0_1055:
	ds_read_b128 v[166:169], v155
	ds_read_b128 v[170:173], v155 offset:1024
	ds_read_b128 v[174:177], v155 offset:2048
	ds_read_b128 v[178:181], v155 offset:3072
	ds_read_b128 v[182:185], v157
	ds_read_b128 v[186:189], v157 offset:1024
	ds_read_b128 v[190:193], v157 offset:2048
	ds_read_b128 v[194:197], v157 offset:3072
	s_add_u32 s56, s54, 0xfff80080
	s_addc_u32 s57, s55, -1
	s_cmp_eq_u32 s83, 28
	s_cselect_b32 s59, s15, s57
	s_cselect_b32 s58, s79, s56
	s_cselect_b32 s57, s49, s82
	s_cselect_b32 s56, s80, s81
	v_lshl_add_u64 v[230:231], s[54:55], 0, v[140:141]
	s_add_i32 m0, s63, 0xc000
	ds_read_b128 v[198:201], v159
	ds_read_b128 v[202:205], v159 offset:1024
	ds_read_b128 v[206:209], v159 offset:2048
	ds_read_b128 v[210:213], v159 offset:3072
	ds_read_b128 v[214:217], v159 offset:4096
	ds_read_b128 v[218:221], v159 offset:5120
	ds_read_b128 v[222:225], v159 offset:6144
	ds_read_b128 v[226:229], v159 offset:7168
	global_load_lds_dwordx4 v[230:231], off
	v_lshl_add_u64 v[230:231], s[54:55], 0, v[142:143]
	s_add_i32 m0, s63, 0xe000
	s_nop 0
	global_load_lds_dwordx4 v[230:231], off
	s_waitcnt vmcnt(8)
	s_waitcnt lgkmcnt(0)
	v_mfma_f32_16x16x32_bf16 v[126:129], v[166:169], v[198:201], v[126:129]
	s_barrier
	v_mfma_f32_16x16x32_bf16 v[122:125], v[174:177], v[198:201], v[122:125]
	v_mfma_f32_16x16x32_bf16 v[114:117], v[166:169], v[206:209], v[114:117]
	v_mfma_f32_16x16x32_bf16 v[106:109], v[174:177], v[206:209], v[106:109]
	v_mfma_f32_16x16x32_bf16 v[98:101], v[166:169], v[214:217], v[98:101]
	v_mfma_f32_16x16x32_bf16 v[90:93], v[174:177], v[214:217], v[90:93]
	v_mfma_f32_16x16x32_bf16 v[82:85], v[166:169], v[222:225], v[82:85]
	v_mfma_f32_16x16x32_bf16 v[74:77], v[174:177], v[222:225], v[74:77]
	v_mfma_f32_16x16x32_bf16 v[126:129], v[170:173], v[202:205], v[126:129]
	v_mfma_f32_16x16x32_bf16 v[122:125], v[178:181], v[202:205], v[122:125]
	v_mfma_f32_16x16x32_bf16 v[114:117], v[170:173], v[210:213], v[114:117]
	v_mfma_f32_16x16x32_bf16 v[106:109], v[178:181], v[210:213], v[106:109]
	v_mfma_f32_16x16x32_bf16 v[98:101], v[170:173], v[218:221], v[98:101]
	v_mfma_f32_16x16x32_bf16 v[90:93], v[178:181], v[218:221], v[90:93]
	v_mfma_f32_16x16x32_bf16 v[82:85], v[170:173], v[226:229], v[82:85]
	v_mfma_f32_16x16x32_bf16 v[74:77], v[178:181], v[226:229], v[74:77]
	v_mfma_f32_16x16x32_bf16 v[118:121], v[182:185], v[198:201], v[118:121]
	v_mfma_f32_16x16x32_bf16 v[110:113], v[190:193], v[198:201], v[110:113]
	v_mfma_f32_16x16x32_bf16 v[102:105], v[182:185], v[206:209], v[102:105]
	v_mfma_f32_16x16x32_bf16 v[94:97], v[190:193], v[206:209], v[94:97]
	v_mfma_f32_16x16x32_bf16 v[86:89], v[182:185], v[214:217], v[86:89]
	v_mfma_f32_16x16x32_bf16 v[78:81], v[190:193], v[214:217], v[78:81]
	v_mfma_f32_16x16x32_bf16 v[62:65], v[182:185], v[222:225], v[62:65]
	v_mfma_f32_16x16x32_bf16 v[58:61], v[190:193], v[222:225], v[58:61]
	v_mfma_f32_16x16x32_bf16 v[118:121], v[186:189], v[202:205], v[118:121]
	v_mfma_f32_16x16x32_bf16 v[110:113], v[194:197], v[202:205], v[110:113]
	v_mfma_f32_16x16x32_bf16 v[102:105], v[186:189], v[210:213], v[102:105]
	v_mfma_f32_16x16x32_bf16 v[94:97], v[194:197], v[210:213], v[94:97]
	v_mfma_f32_16x16x32_bf16 v[86:89], v[186:189], v[218:221], v[86:89]
	v_mfma_f32_16x16x32_bf16 v[78:81], v[194:197], v[218:221], v[78:81]
	v_mfma_f32_16x16x32_bf16 v[62:65], v[186:189], v[226:229], v[62:65]
	v_mfma_f32_16x16x32_bf16 v[58:61], v[194:197], v[226:229], v[58:61]
	s_barrier
	s_add_i32 s84, s73, s61
	v_lshl_add_u64 v[230:231], s[56:57], 0, v[132:133]
	s_mov_b32 m0, s84
	ds_read_b128 v[198:201], v159 offset:16384
	ds_read_b128 v[202:205], v159 offset:17408
	ds_read_b128 v[206:209], v159 offset:18432
	ds_read_b128 v[210:213], v159 offset:19456
	ds_read_b128 v[214:217], v159 offset:20480
	ds_read_b128 v[218:221], v159 offset:21504
	ds_read_b128 v[222:225], v159 offset:22528
	ds_read_b128 v[226:229], v159 offset:23552
	global_load_lds_dwordx4 v[230:231], off
	s_add_i32 m0, s84, 0x2000
	s_add_u32 s84, s56, 0x80000
	v_lshl_add_u64 v[232:233], s[56:57], 0, v[136:137]
	s_addc_u32 s85, s57, 0
	s_add_i32 s86, s74, s61
	global_load_lds_dwordx4 v[232:233], off
	v_lshl_add_u64 v[234:235], s[84:85], 0, v[132:133]
	s_mov_b32 m0, s86
	v_lshl_add_u64 v[236:237], s[58:59], 0, v[134:135]
	global_load_lds_dwordx4 v[234:235], off
	v_lshl_add_u64 v[234:235], s[84:85], 0, v[136:137]
	s_add_i32 m0, s86, 0x2000
	s_nop 0
	global_load_lds_dwordx4 v[234:235], off
	v_lshl_add_u64 v[234:235], s[58:59], 0, v[130:131]
	s_mov_b32 m0, s63
	s_nop 0
	global_load_lds_dwordx4 v[234:235], off
	s_mov_b32 m0, s64
	s_nop 0
	global_load_lds_dwordx4 v[236:237], off
	s_waitcnt vmcnt(8)
	s_waitcnt lgkmcnt(0)
	v_mfma_f32_16x16x32_bf16 v[54:57], v[166:169], v[198:201], v[54:57]
	s_barrier
; #define PG8_STAGE(bufoff, gbase, voff) do { _Pragma("unroll") for (int _i = 0; _i < 2; ++_i) \
;         __builtin_amdgcn_global_load_lds((const unsigned*)((const char*)(gbase) + (voff)[_i]), (PG8_LAS unsigned*)(lds + (bufoff) + ldsw + _i * 8192), 16, 0, 0); } while (0)
; #define PG8_LDA(dst, b, h) do { _Pragma("unroll") for (int m = 0; m < 4; ++m) _Pragma("unroll") for (int k = 0; k < 2; ++k) dst[m][k] = *(const PG8_LAS bf16x8*)(lds + PG8_SA(b, h) + aoff + m * 2048 + k * 1024); } while (0)
; #define PG8_LDB(dst, b, h) do { _Pragma("unroll") for (int n = 0; n < 2; ++n) _Pragma("unroll") for (int k = 0; k < 2; ++k) dst[n][k] = *(const PG8_LAS bf16x8*)(lds + PG8_SB(b, h) + boff + n * 2048 + k * 1024); } while (0)
; #define PG8_MMA(ai, bj, At, Bt) do { __builtin_amdgcn_s_setprio(1); _Pragma("unroll") for (int m = 0; m < 4; ++m) _Pragma("unroll") for (int n = 0; n < 2; ++n) _Pragma("unroll") for (int k = 0; k < 2; ++k) \
;         acc[ai][bj][m][n] = __builtin_amdgcn_mfma_f32_16x16x32_bf16(Bt[n][k], At[m][k], acc[ai][bj][m][n], 0, 0, 0); __builtin_amdgcn_s_setprio(0); } while (0)
; #define PG8_WAIT_V(n) asm volatile("s_waitcnt vmcnt(" #n ")" ::: "memory")
; #define PG8_WAIT_L(n) asm volatile("s_waitcnt lgkmcnt(" #n ")" ::: "memory")
; #define PG8_BAR __builtin_amdgcn_s_barrier()
; #define PG8_SCHED __builtin_amdgcn_sched_barrier(0)
; template <class Epi, class Sched, bool ALIGN_EPI = false>
; __device__ __forceinline__ void gemm_phase(PG8_LAS unsigned char* lds, const Gemm g, const Sched& S, const Epi& E) {
;     ...
;             PG8_WAIT_V(8); PG8_WAIT_L(0); PG8_BAR; PG8_MMA(1, 0, At, B0); PG8_MMA(1, 1, At, B1); PG8_BAR; PG8_SCHED;
;             PG8_LDB(B0, 1, 0); PG8_LDB(B1, 1, 1); PG8_SCHED; PG8_LDA(At, 1, 0); PG8_STAGE(PG8_SA(0, 1), a2 + hstepA, w1);
;             PG8_WAIT_V(8); PG8_WAIT_L(0); PG8_BAR; PG8_MMA(0, 0, At, B0); PG8_MMA(0, 1, At, B1); PG8_BAR; PG8_SCHED;
	v_mfma_f32_16x16x32_bf16 v[42:45], v[174:177], v[198:201], v[42:45]
	v_mfma_f32_16x16x32_bf16 v[30:33], v[166:169], v[206:209], v[30:33]
	v_mfma_f32_16x16x32_bf16 v[26:29], v[174:177], v[206:209], v[26:29]
	v_mfma_f32_16x16x32_bf16 v[14:17], v[166:169], v[214:217], v[14:17]
	v_mfma_f32_16x16x32_bf16 v[10:13], v[174:177], v[214:217], v[10:13]
	v_mfma_f32_16x16x32_bf16 v[6:9], v[166:169], v[222:225], v[6:9]
	v_mfma_f32_16x16x32_bf16 v[2:5], v[174:177], v[222:225], v[2:5]
	v_mfma_f32_16x16x32_bf16 v[54:57], v[170:173], v[202:205], v[54:57]
	v_mfma_f32_16x16x32_bf16 v[42:45], v[178:181], v[202:205], v[42:45]
	v_mfma_f32_16x16x32_bf16 v[30:33], v[170:173], v[210:213], v[30:33]
	v_mfma_f32_16x16x32_bf16 v[26:29], v[178:181], v[210:213], v[26:29]
	v_mfma_f32_16x16x32_bf16 v[14:17], v[170:173], v[218:221], v[14:17]
	v_mfma_f32_16x16x32_bf16 v[10:13], v[178:181], v[218:221], v[10:13]
	v_mfma_f32_16x16x32_bf16 v[6:9], v[170:173], v[226:229], v[6:9]
	v_mfma_f32_16x16x32_bf16 v[2:5], v[178:181], v[226:229], v[2:5]
	v_mfma_f32_16x16x32_bf16 v[66:69], v[182:185], v[198:201], v[66:69]
	v_mfma_f32_16x16x32_bf16 v[70:73], v[190:193], v[198:201], v[70:73]
	v_mfma_f32_16x16x32_bf16 v[46:49], v[182:185], v[206:209], v[46:49]
	v_mfma_f32_16x16x32_bf16 v[50:53], v[190:193], v[206:209], v[50:53]
	v_mfma_f32_16x16x32_bf16 v[34:37], v[182:185], v[214:217], v[34:37]
	v_mfma_f32_16x16x32_bf16 v[38:41], v[190:193], v[214:217], v[38:41]
	v_mfma_f32_16x16x32_bf16 v[18:21], v[182:185], v[222:225], v[18:21]
	v_mfma_f32_16x16x32_bf16 v[22:25], v[190:193], v[222:225], v[22:25]
	v_mfma_f32_16x16x32_bf16 v[66:69], v[186:189], v[202:205], v[66:69]
	v_mfma_f32_16x16x32_bf16 v[70:73], v[194:197], v[202:205], v[70:73]
	v_mfma_f32_16x16x32_bf16 v[46:49], v[186:189], v[210:213], v[46:49]
	v_mfma_f32_16x16x32_bf16 v[50:53], v[194:197], v[210:213], v[50:53]
	v_mfma_f32_16x16x32_bf16 v[34:37], v[186:189], v[218:221], v[34:37]
	v_mfma_f32_16x16x32_bf16 v[38:41], v[194:197], v[218:221], v[38:41]
	v_mfma_f32_16x16x32_bf16 v[18:21], v[186:189], v[226:229], v[18:21]
	v_mfma_f32_16x16x32_bf16 v[22:25], v[194:197], v[226:229], v[22:25]
	s_barrier
	s_add_i32 s84, 0, 0x18000
	v_add_u32_e32 v138, s84, v149
	s_add_i32 s85, 0, 0x1c000
	ds_read_b128 v[166:169], v138
	ds_read_b128 v[170:173], v138 offset:1024
	ds_read_b128 v[174:177], v138 offset:2048
	ds_read_b128 v[178:181], v138 offset:3072
	v_add_u32_e32 v138, s85, v149
	ds_read_b128 v[182:185], v138
	ds_read_b128 v[186:189], v138 offset:1024
	ds_read_b128 v[190:193], v138 offset:2048
	ds_read_b128 v[194:197], v138 offset:3072
	s_add_u32 s58, s58, 0x80000
	s_addc_u32 s59, s59, 0
	s_mov_b32 m0, s65
	v_lshl_add_u64 v[238:239], s[58:59], 0, v[130:131]
	ds_read_b128 v[198:201], v159 offset:32768
	ds_read_b128 v[202:205], v159 offset:33792
	ds_read_b128 v[206:209], v159 offset:34816
	ds_read_b128 v[210:213], v159 offset:35840
	ds_read_b128 v[214:217], v159 offset:36864
	ds_read_b128 v[218:221], v159 offset:37888
	ds_read_b128 v[222:225], v159 offset:38912
	ds_read_b128 v[226:229], v159 offset:39936
	global_load_lds_dwordx4 v[238:239], off
	v_lshl_add_u64 v[238:239], s[58:59], 0, v[134:135]
	s_mov_b32 m0, s66
	s_nop 0
	global_load_lds_dwordx4 v[238:239], off
	s_waitcnt vmcnt(8)
	s_waitcnt lgkmcnt(0)
	v_mfma_f32_16x16x32_bf16 v[126:129], v[166:169], v[198:201], v[126:129]
	s_barrier
	v_mfma_f32_16x16x32_bf16 v[122:125], v[174:177], v[198:201], v[122:125]
	v_mfma_f32_16x16x32_bf16 v[114:117], v[166:169], v[206:209], v[114:117]
	v_mfma_f32_16x16x32_bf16 v[106:109], v[174:177], v[206:209], v[106:109]
	v_mfma_f32_16x16x32_bf16 v[98:101], v[166:169], v[214:217], v[98:101]
	v_mfma_f32_16x16x32_bf16 v[90:93], v[174:177], v[214:217], v[90:93]
	v_mfma_f32_16x16x32_bf16 v[82:85], v[166:169], v[222:225], v[82:85]
	v_mfma_f32_16x16x32_bf16 v[74:77], v[174:177], v[222:225], v[74:77]
	v_mfma_f32_16x16x32_bf16 v[126:129], v[170:173], v[202:205], v[126:129]
	v_mfma_f32_16x16x32_bf16 v[122:125], v[178:181], v[202:205], v[122:125]
	v_mfma_f32_16x16x32_bf16 v[114:117], v[170:173], v[210:213], v[114:117]
	v_mfma_f32_16x16x32_bf16 v[106:109], v[178:181], v[210:213], v[106:109]
	v_mfma_f32_16x16x32_bf16 v[98:101], v[170:173], v[218:221], v[98:101]
	v_mfma_f32_16x16x32_bf16 v[90:93], v[178:181], v[218:221], v[90:93]
	v_mfma_f32_16x16x32_bf16 v[82:85], v[170:173], v[226:229], v[82:85]
	v_mfma_f32_16x16x32_bf16 v[74:77], v[178:181], v[226:229], v[74:77]
	v_mfma_f32_16x16x32_bf16 v[118:121], v[182:185], v[198:201], v[118:121]
	v_mfma_f32_16x16x32_bf16 v[110:113], v[190:193], v[198:201], v[110:113]
	v_mfma_f32_16x16x32_bf16 v[102:105], v[182:185], v[206:209], v[102:105]
	v_mfma_f32_16x16x32_bf16 v[94:97], v[190:193], v[206:209], v[94:97]
	v_mfma_f32_16x16x32_bf16 v[86:89], v[182:185], v[214:217], v[86:89]
	v_mfma_f32_16x16x32_bf16 v[78:81], v[190:193], v[214:217], v[78:81]
	v_mfma_f32_16x16x32_bf16 v[62:65], v[182:185], v[222:225], v[62:65]
	v_mfma_f32_16x16x32_bf16 v[58:61], v[190:193], v[222:225], v[58:61]
	v_mfma_f32_16x16x32_bf16 v[118:121], v[186:189], v[202:205], v[118:121]
	v_mfma_f32_16x16x32_bf16 v[110:113], v[194:197], v[202:205], v[110:113]
	v_mfma_f32_16x16x32_bf16 v[102:105], v[186:189], v[210:213], v[102:105]
	v_mfma_f32_16x16x32_bf16 v[94:97], v[194:197], v[210:213], v[94:97]
	v_mfma_f32_16x16x32_bf16 v[86:89], v[186:189], v[218:221], v[86:89]
	v_mfma_f32_16x16x32_bf16 v[78:81], v[194:197], v[218:221], v[78:81]
	v_mfma_f32_16x16x32_bf16 v[62:65], v[186:189], v[226:229], v[62:65]
	v_mfma_f32_16x16x32_bf16 v[58:61], v[194:197], v[226:229], v[58:61]
	s_barrier
; #define PG8_STAGE(bufoff, gbase, voff) do { _Pragma("unroll") for (int _i = 0; _i < 2; ++_i) \
;         __builtin_amdgcn_global_load_lds((const unsigned*)((const char*)(gbase) + (voff)[_i]), (PG8_LAS unsigned*)(lds + (bufoff) + ldsw + _i * 8192), 16, 0, 0); } while (0)
; #define PG8_LDA(dst, b, h) do { _Pragma("unroll") for (int m = 0; m < 4; ++m) _Pragma("unroll") for (int k = 0; k < 2; ++k) dst[m][k] = *(const PG8_LAS bf16x8*)(lds + PG8_SA(b, h) + aoff + m * 2048 + k * 1024); } while (0)
; #define PG8_MMA(ai, bj, At, Bt) do { __builtin_amdgcn_s_setprio(1); _Pragma("unroll") for (int m = 0; m < 4; ++m) _Pragma("unroll") for (int n = 0; n < 2; ++n) _Pragma("unroll") for (int k = 0; k < 2; ++k) \
;         acc[ai][bj][m][n] = __builtin_amdgcn_mfma_f32_16x16x32_bf16(Bt[n][k], At[m][k], acc[ai][bj][m][n], 0, 0, 0); __builtin_amdgcn_s_setprio(0); } while (0)
; #define PG8_WAIT_V(n) asm volatile("s_waitcnt vmcnt(" #n ")" ::: "memory")
; #define PG8_WAIT_L(n) asm volatile("s_waitcnt lgkmcnt(" #n ")" ::: "memory")
; #define PG8_BAR __builtin_amdgcn_s_barrier()
; #define PG8_SCHED __builtin_amdgcn_sched_barrier(0)
; template <class Epi, class Sched, bool ALIGN_EPI = false>
; __device__ __forceinline__ void gemm_phase(PG8_LAS unsigned char* lds, const Gemm g, const Sched& S, const Epi& E) {
;     ...
;             PG8_LDA(At, 1, 1); PG8_STAGE(PG8_SB(1, 0), b3, voffB); PG8_STAGE(PG8_SB(1, 1), b3 + hstep, voffB); PG8_STAGE(PG8_SA(1, 0), a3, w0);
;             PG8_WAIT_V(8); PG8_WAIT_L(0); PG8_BAR; PG8_MMA(1, 0, At, B0); PG8_MMA(1, 1, At, B1); PG8_BAR; PG8_SCHED;
;             if constexpr (Epi::KSCALE) { if (((t + 2) & 7) == 0 && t + 2 < nt) { E.kscale(acc, pf, ((t + 2) >> 3) - 1, wr, fr); PG8_SCHED; } }
;         }
;         if constexpr (ALIGN_EPI) { if (wr == 0) PG8_BAR; }
	s_add_i32 s58, s84, s61
	v_lshl_add_u64 v[230:231], v[230:231], 0, s[26:27]
	s_mov_b32 m0, s58
	ds_read_b128 v[198:201], v159 offset:49152
	ds_read_b128 v[202:205], v159 offset:50176
	ds_read_b128 v[206:209], v159 offset:51200
	ds_read_b128 v[210:213], v159 offset:52224
	ds_read_b128 v[214:217], v159 offset:53248
	ds_read_b128 v[218:221], v159 offset:54272
	ds_read_b128 v[222:225], v159 offset:55296
	ds_read_b128 v[226:229], v159 offset:56320
	global_load_lds_dwordx4 v[230:231], off
	s_add_i32 m0, s58, 0x2000
	s_add_u32 s56, s56, 0x80080
	v_lshl_add_u64 v[230:231], v[232:233], 0, s[26:27]
	s_addc_u32 s57, s57, 0
	s_add_i32 s58, s85, s61
	global_load_lds_dwordx4 v[230:231], off
	v_lshl_add_u64 v[230:231], s[56:57], 0, v[132:133]
	s_mov_b32 m0, s58
	s_nop 0
	global_load_lds_dwordx4 v[230:231], off
	v_lshl_add_u64 v[230:231], s[56:57], 0, v[136:137]
	s_add_i32 m0, s58, 0x2000
	s_nop 0
	global_load_lds_dwordx4 v[230:231], off
	v_lshl_add_u64 v[230:231], v[234:235], 0, s[26:27]
	s_mov_b32 m0, s69
	s_nop 0
	global_load_lds_dwordx4 v[230:231], off
	v_lshl_add_u64 v[230:231], v[236:237], 0, s[26:27]
	s_mov_b32 m0, s72
	s_nop 0
	global_load_lds_dwordx4 v[230:231], off
	s_waitcnt vmcnt(8)
	s_waitcnt lgkmcnt(0)
	v_mfma_f32_16x16x32_bf16 v[54:57], v[166:169], v[198:201], v[54:57]
	s_barrier
	v_mfma_f32_16x16x32_bf16 v[42:45], v[174:177], v[198:201], v[42:45]
	v_mfma_f32_16x16x32_bf16 v[30:33], v[166:169], v[206:209], v[30:33]
	v_mfma_f32_16x16x32_bf16 v[26:29], v[174:177], v[206:209], v[26:29]
	v_mfma_f32_16x16x32_bf16 v[14:17], v[166:169], v[214:217], v[14:17]
	v_mfma_f32_16x16x32_bf16 v[10:13], v[174:177], v[214:217], v[10:13]
	v_mfma_f32_16x16x32_bf16 v[6:9], v[166:169], v[222:225], v[6:9]
	v_mfma_f32_16x16x32_bf16 v[2:5], v[174:177], v[222:225], v[2:5]
	v_mfma_f32_16x16x32_bf16 v[54:57], v[170:173], v[202:205], v[54:57]
	v_mfma_f32_16x16x32_bf16 v[42:45], v[178:181], v[202:205], v[42:45]
	v_mfma_f32_16x16x32_bf16 v[30:33], v[170:173], v[210:213], v[30:33]
	v_mfma_f32_16x16x32_bf16 v[26:29], v[178:181], v[210:213], v[26:29]
	v_mfma_f32_16x16x32_bf16 v[14:17], v[170:173], v[218:221], v[14:17]
	v_mfma_f32_16x16x32_bf16 v[10:13], v[178:181], v[218:221], v[10:13]
	v_mfma_f32_16x16x32_bf16 v[6:9], v[170:173], v[226:229], v[6:9]
	v_mfma_f32_16x16x32_bf16 v[2:5], v[178:181], v[226:229], v[2:5]
	v_mfma_f32_16x16x32_bf16 v[66:69], v[182:185], v[198:201], v[66:69]
	v_mfma_f32_16x16x32_bf16 v[70:73], v[190:193], v[198:201], v[70:73]
	v_mfma_f32_16x16x32_bf16 v[46:49], v[182:185], v[206:209], v[46:49]
	v_mfma_f32_16x16x32_bf16 v[50:53], v[190:193], v[206:209], v[50:53]
	v_mfma_f32_16x16x32_bf16 v[34:37], v[182:185], v[214:217], v[34:37]
	v_mfma_f32_16x16x32_bf16 v[38:41], v[190:193], v[214:217], v[38:41]
	v_mfma_f32_16x16x32_bf16 v[18:21], v[182:185], v[222:225], v[18:21]
	v_mfma_f32_16x16x32_bf16 v[22:25], v[190:193], v[222:225], v[22:25]
	v_mfma_f32_16x16x32_bf16 v[66:69], v[186:189], v[202:205], v[66:69]
	v_mfma_f32_16x16x32_bf16 v[70:73], v[194:197], v[202:205], v[70:73]
	v_mfma_f32_16x16x32_bf16 v[46:49], v[186:189], v[210:213], v[46:49]
	v_mfma_f32_16x16x32_bf16 v[50:53], v[194:197], v[210:213], v[50:53]
	v_mfma_f32_16x16x32_bf16 v[34:37], v[186:189], v[218:221], v[34:37]
	v_mfma_f32_16x16x32_bf16 v[38:41], v[194:197], v[218:221], v[38:41]
	v_mfma_f32_16x16x32_bf16 v[18:21], v[186:189], v[226:229], v[18:21]
	v_mfma_f32_16x16x32_bf16 v[22:25], v[194:197], v[226:229], v[22:25]
	s_barrier
	s_add_i32 s83, s83, 2
	s_add_u32 s54, s54, 0x100
	s_addc_u32 s55, s55, 0
	s_add_u32 s81, s81, 0x100
	s_addc_u32 s82, s82, 0
	s_cmp_gt_u32 s83, 29
	s_cbranch_scc0 .LBB0_1055
	s_and_b64 vcc, exec, s[40:41]
	s_cbranch_vccz .LBB0_1058
	s_barrier

; #define PG8_STAGE(bufoff, gbase, voff) do { _Pragma("unroll") for (int _i = 0; _i < 2; ++_i) \
;         __builtin_amdgcn_global_load_lds((const unsigned*)((const char*)(gbase) + (voff)[_i]), (PG8_LAS unsigned*)(lds + (bufoff) + ldsw + _i * 8192), 16, 0, 0); } while (0)
; #define PG8_LDA(dst, b, h) do { _Pragma("unroll") for (int m = 0; m < 4; ++m) _Pragma("unroll") for (int k = 0; k < 2; ++k) dst[m][k] = *(const PG8_LAS bf16x8*)(lds + PG8_SA(b, h) + aoff + m * 2048 + k * 1024); } while (0)
; #define PG8_LDB(dst, b, h) do { _Pragma("unroll") for (int n = 0; n < 2; ++n) _Pragma("unroll") for (int k = 0; k < 2; ++k) dst[n][k] = *(const PG8_LAS bf16x8*)(lds + PG8_SB(b, h) + boff + n * 2048 + k * 1024); } while (0)
; #define PG8_MMA(ai, bj, At, Bt) do { __builtin_amdgcn_s_setprio(1); _Pragma("unroll") for (int m = 0; m < 4; ++m) _Pragma("unroll") for (int n = 0; n < 2; ++n) _Pragma("unroll") for (int k = 0; k < 2; ++k) \
;         acc[ai][bj][m][n] = __builtin_amdgcn_mfma_f32_16x16x32_bf16(Bt[n][k], At[m][k], acc[ai][bj][m][n], 0, 0, 0); __builtin_amdgcn_s_setprio(0); } while (0)
; template <class Epi, class Sched, bool ALIGN_EPI = false>
; __device__ __forceinline__ void gemm_phase(PG8_LAS unsigned char* lds, const Gemm g, const Sched& S, const Epi& E) {
;     ...
;         for (int t = 0; t < nt; t += 2) {
;             const bool last = (t == nt - 2);
;             const char* a1 = cA + (size_t)(t + 1) * kstep;
;             const char* a2 = last ? nA : cA + (size_t)(t + 2) * kstep; const char* b2 = last ? nB : cB + (size_t)(t + 2) * kstep;
;             const char* a3 = a2 + kstep; const char* b3 = b2 + kstep;
;             unsigned w0[2], w1[2];
; #pragma unroll
;             for (int i = 0; i < 2; ++i) { w0[i] = (Sched::GATHER && last) ? vn0[i] : vc0[i]; w1[i] = (Sched::GATHER && last) ? vn1[i] : vc1[i]; }
;             if (last && has_next) S.a_ready(nxt);
;             PG8_LDB(B0, 0, 0); PG8_LDB(B1, 0, 1); PG8_SCHED; PG8_LDA(At, 0, 0); PG8_STAGE(PG8_SA(1, 1), a1 + hstepA, vc1);
;             PG8_WAIT_V(8); PG8_WAIT_L(0); PG8_BAR; PG8_MMA(0, 0, At, B0); PG8_MMA(0, 1, At, B1); PG8_BAR; PG8_SCHED;
;             PG8_LDA(At, 0, 1); PG8_STAGE(PG8_SB(0, 0), b2, voffB); PG8_STAGE(PG8_SB(0, 1), b2 + hstep, voffB); PG8_STAGE(PG8_SA(0, 0), a2, w0);
;             PG8_WAIT_V(8); PG8_WAIT_L(0); PG8_BAR; PG8_MMA(1, 0, At, B0); PG8_MMA(1, 1, At, B1); PG8_BAR; PG8_SCHED;
.LBB0_1198:
	ds_read_b128 v[130:133], v168
	ds_read_b128 v[134:137], v168 offset:1024
	ds_read_b128 v[154:157], v168 offset:2048
	ds_read_b128 v[158:161], v168 offset:3072
	ds_read_b128 v[162:165], v169
	ds_read_b128 v[172:175], v169 offset:1024
	ds_read_b128 v[176:179], v169 offset:2048
	ds_read_b128 v[180:183], v169 offset:3072
	s_add_u32 s54, s52, 0xfff80080
	s_addc_u32 s55, s53, -1
	s_cmp_eq_u32 s78, 28
	s_cselect_b32 s57, s45, s55
	s_cselect_b32 s56, s74, s54
	s_cselect_b32 s55, s43, s77
	s_cselect_b32 s54, s75, s76
	v_lshl_add_u64 v[216:217], s[52:53], 0, v[146:147]
	s_add_i32 m0, s51, 0xc000
	ds_read_b128 v[184:187], v170
	ds_read_b128 v[188:191], v170 offset:1024
	ds_read_b128 v[192:195], v170 offset:2048
	ds_read_b128 v[196:199], v170 offset:3072
	ds_read_b128 v[200:203], v170 offset:4096
	ds_read_b128 v[204:207], v170 offset:5120
	ds_read_b128 v[208:211], v170 offset:6144
	ds_read_b128 v[212:215], v170 offset:7168
	global_load_lds_dwordx4 v[216:217], off
	v_lshl_add_u64 v[216:217], s[52:53], 0, v[148:149]
	s_add_i32 m0, s51, 0xe000
	s_nop 0
	global_load_lds_dwordx4 v[216:217], off
	s_waitcnt vmcnt(8)
	s_waitcnt lgkmcnt(0)
	v_mfma_f32_16x16x32_bf16 v[126:129], v[130:133], v[184:187], v[126:129]
	s_barrier
	v_mfma_f32_16x16x32_bf16 v[122:125], v[154:157], v[184:187], v[122:125]
	v_mfma_f32_16x16x32_bf16 v[118:121], v[130:133], v[192:195], v[118:121]
	v_mfma_f32_16x16x32_bf16 v[114:117], v[154:157], v[192:195], v[114:117]
	v_mfma_f32_16x16x32_bf16 v[94:97], v[130:133], v[200:203], v[94:97]
	v_mfma_f32_16x16x32_bf16 v[90:93], v[154:157], v[200:203], v[90:93]
	v_mfma_f32_16x16x32_bf16 v[78:81], v[130:133], v[208:211], v[78:81]
	v_mfma_f32_16x16x32_bf16 v[74:77], v[154:157], v[208:211], v[74:77]
	v_mfma_f32_16x16x32_bf16 v[126:129], v[134:137], v[188:191], v[126:129]
	v_mfma_f32_16x16x32_bf16 v[122:125], v[158:161], v[188:191], v[122:125]
	v_mfma_f32_16x16x32_bf16 v[118:121], v[134:137], v[196:199], v[118:121]
	v_mfma_f32_16x16x32_bf16 v[114:117], v[158:161], v[196:199], v[114:117]
	v_mfma_f32_16x16x32_bf16 v[94:97], v[134:137], v[204:207], v[94:97]
	v_mfma_f32_16x16x32_bf16 v[90:93], v[158:161], v[204:207], v[90:93]
	v_mfma_f32_16x16x32_bf16 v[78:81], v[134:137], v[212:215], v[78:81]
	v_mfma_f32_16x16x32_bf16 v[74:77], v[158:161], v[212:215], v[74:77]
	v_mfma_f32_16x16x32_bf16 v[110:113], v[162:165], v[184:187], v[110:113]
	v_mfma_f32_16x16x32_bf16 v[106:109], v[176:179], v[184:187], v[106:109]
	v_mfma_f32_16x16x32_bf16 v[102:105], v[162:165], v[192:195], v[102:105]
	v_mfma_f32_16x16x32_bf16 v[98:101], v[176:179], v[192:195], v[98:101]
	v_mfma_f32_16x16x32_bf16 v[86:89], v[162:165], v[200:203], v[86:89]
	v_mfma_f32_16x16x32_bf16 v[82:85], v[176:179], v[200:203], v[82:85]
	v_mfma_f32_16x16x32_bf16 v[70:73], v[162:165], v[208:211], v[70:73]
	v_mfma_f32_16x16x32_bf16 v[66:69], v[176:179], v[208:211], v[66:69]
	v_mfma_f32_16x16x32_bf16 v[110:113], v[172:175], v[188:191], v[110:113]
	v_mfma_f32_16x16x32_bf16 v[106:109], v[180:183], v[188:191], v[106:109]
	v_mfma_f32_16x16x32_bf16 v[102:105], v[172:175], v[196:199], v[102:105]
	v_mfma_f32_16x16x32_bf16 v[98:101], v[180:183], v[196:199], v[98:101]
	v_mfma_f32_16x16x32_bf16 v[86:89], v[172:175], v[204:207], v[86:89]
	v_mfma_f32_16x16x32_bf16 v[82:85], v[180:183], v[204:207], v[82:85]
	v_mfma_f32_16x16x32_bf16 v[70:73], v[172:175], v[212:215], v[70:73]
	v_mfma_f32_16x16x32_bf16 v[66:69], v[180:183], v[212:215], v[66:69]
	s_barrier
	s_add_i32 s79, s69, s61
	v_lshl_add_u64 v[216:217], s[54:55], 0, v[140:141]
	s_mov_b32 m0, s79
	ds_read_b128 v[184:187], v170 offset:16384
	ds_read_b128 v[188:191], v170 offset:17408
	ds_read_b128 v[192:195], v170 offset:18432
	ds_read_b128 v[196:199], v170 offset:19456
	ds_read_b128 v[200:203], v170 offset:20480
	ds_read_b128 v[204:207], v170 offset:21504
	ds_read_b128 v[208:211], v170 offset:22528
	ds_read_b128 v[212:215], v170 offset:23552
	global_load_lds_dwordx4 v[216:217], off
	s_add_i32 m0, s79, 0x2000
	s_add_u32 s80, s54, 0x80000
	v_lshl_add_u64 v[218:219], s[54:55], 0, v[144:145]
	s_addc_u32 s81, s55, 0
	s_add_i32 s79, s72, s61
	global_load_lds_dwordx4 v[218:219], off
	v_lshl_add_u64 v[220:221], s[80:81], 0, v[140:141]
	s_mov_b32 m0, s79
	v_lshl_add_u64 v[222:223], s[56:57], 0, v[142:143]
	global_load_lds_dwordx4 v[220:221], off
	v_lshl_add_u64 v[220:221], s[80:81], 0, v[144:145]
	s_add_i32 m0, s79, 0x2000
	s_nop 0
	global_load_lds_dwordx4 v[220:221], off
	v_lshl_add_u64 v[220:221], s[56:57], 0, v[138:139]
	s_mov_b32 m0, s51
	s_nop 0
	global_load_lds_dwordx4 v[220:221], off
	s_mov_b32 m0, s62
	s_nop 0
	global_load_lds_dwordx4 v[222:223], off
	s_waitcnt vmcnt(8)
	s_waitcnt lgkmcnt(0)
	v_mfma_f32_16x16x32_bf16 v[54:57], v[130:133], v[184:187], v[54:57]
	s_barrier
; #define PG8_STAGE(bufoff, gbase, voff) do { _Pragma("unroll") for (int _i = 0; _i < 2; ++_i) \
;         __builtin_amdgcn_global_load_lds((const unsigned*)((const char*)(gbase) + (voff)[_i]), (PG8_LAS unsigned*)(lds + (bufoff) + ldsw + _i * 8192), 16, 0, 0); } while (0)
; #define PG8_LDA(dst, b, h) do { _Pragma("unroll") for (int m = 0; m < 4; ++m) _Pragma("unroll") for (int k = 0; k < 2; ++k) dst[m][k] = *(const PG8_LAS bf16x8*)(lds + PG8_SA(b, h) + aoff + m * 2048 + k * 1024); } while (0)
; #define PG8_LDB(dst, b, h) do { _Pragma("unroll") for (int n = 0; n < 2; ++n) _Pragma("unroll") for (int k = 0; k < 2; ++k) dst[n][k] = *(const PG8_LAS bf16x8*)(lds + PG8_SB(b, h) + boff + n * 2048 + k * 1024); } while (0)
; #define PG8_MMA(ai, bj, At, Bt) do { __builtin_amdgcn_s_setprio(1); _Pragma("unroll") for (int m = 0; m < 4; ++m) _Pragma("unroll") for (int n = 0; n < 2; ++n) _Pragma("unroll") for (int k = 0; k < 2; ++k) \
;         acc[ai][bj][m][n] = __builtin_amdgcn_mfma_f32_16x16x32_bf16(Bt[n][k], At[m][k], acc[ai][bj][m][n], 0, 0, 0); __builtin_amdgcn_s_setprio(0); } while (0)
; #define PG8_WAIT_V(n) asm volatile("s_waitcnt vmcnt(" #n ")" ::: "memory")
; #define PG8_WAIT_L(n) asm volatile("s_waitcnt lgkmcnt(" #n ")" ::: "memory")
; #define PG8_BAR __builtin_amdgcn_s_barrier()
; #define PG8_SCHED __builtin_amdgcn_sched_barrier(0)
; template <class Epi, class Sched, bool ALIGN_EPI = false>
; __device__ __forceinline__ void gemm_phase(PG8_LAS unsigned char* lds, const Gemm g, const Sched& S, const Epi& E) {
;     ...
;             PG8_WAIT_V(8); PG8_WAIT_L(0); PG8_BAR; PG8_MMA(1, 0, At, B0); PG8_MMA(1, 1, At, B1); PG8_BAR; PG8_SCHED;
;             PG8_LDB(B0, 1, 0); PG8_LDB(B1, 1, 1); PG8_SCHED; PG8_LDA(At, 1, 0); PG8_STAGE(PG8_SA(0, 1), a2 + hstepA, w1);
;             PG8_WAIT_V(8); PG8_WAIT_L(0); PG8_BAR; PG8_MMA(0, 0, At, B0); PG8_MMA(0, 1, At, B1); PG8_BAR; PG8_SCHED;
	v_mfma_f32_16x16x32_bf16 v[50:53], v[154:157], v[184:187], v[50:53]
	v_mfma_f32_16x16x32_bf16 v[38:41], v[130:133], v[192:195], v[38:41]
	v_mfma_f32_16x16x32_bf16 v[34:37], v[154:157], v[192:195], v[34:37]
	v_mfma_f32_16x16x32_bf16 v[22:25], v[130:133], v[200:203], v[22:25]
	v_mfma_f32_16x16x32_bf16 v[18:21], v[154:157], v[200:203], v[18:21]
	v_mfma_f32_16x16x32_bf16 v[6:9], v[130:133], v[208:211], v[6:9]
	v_mfma_f32_16x16x32_bf16 v[2:5], v[154:157], v[208:211], v[2:5]
	v_mfma_f32_16x16x32_bf16 v[54:57], v[134:137], v[188:191], v[54:57]
	v_mfma_f32_16x16x32_bf16 v[50:53], v[158:161], v[188:191], v[50:53]
	v_mfma_f32_16x16x32_bf16 v[38:41], v[134:137], v[196:199], v[38:41]
	v_mfma_f32_16x16x32_bf16 v[34:37], v[158:161], v[196:199], v[34:37]
	v_mfma_f32_16x16x32_bf16 v[22:25], v[134:137], v[204:207], v[22:25]
	v_mfma_f32_16x16x32_bf16 v[18:21], v[158:161], v[204:207], v[18:21]
	v_mfma_f32_16x16x32_bf16 v[6:9], v[134:137], v[212:215], v[6:9]
	v_mfma_f32_16x16x32_bf16 v[2:5], v[158:161], v[212:215], v[2:5]
	v_mfma_f32_16x16x32_bf16 v[62:65], v[162:165], v[184:187], v[62:65]
	v_mfma_f32_16x16x32_bf16 v[58:61], v[176:179], v[184:187], v[58:61]
	v_mfma_f32_16x16x32_bf16 v[46:49], v[162:165], v[192:195], v[46:49]
	v_mfma_f32_16x16x32_bf16 v[42:45], v[176:179], v[192:195], v[42:45]
	v_mfma_f32_16x16x32_bf16 v[30:33], v[162:165], v[200:203], v[30:33]
	v_mfma_f32_16x16x32_bf16 v[26:29], v[176:179], v[200:203], v[26:29]
	v_mfma_f32_16x16x32_bf16 v[14:17], v[162:165], v[208:211], v[14:17]
	v_mfma_f32_16x16x32_bf16 v[10:13], v[176:179], v[208:211], v[10:13]
	v_mfma_f32_16x16x32_bf16 v[62:65], v[172:175], v[188:191], v[62:65]
	v_mfma_f32_16x16x32_bf16 v[58:61], v[180:183], v[188:191], v[58:61]
	v_mfma_f32_16x16x32_bf16 v[46:49], v[172:175], v[196:199], v[46:49]
	v_mfma_f32_16x16x32_bf16 v[42:45], v[180:183], v[196:199], v[42:45]
	v_mfma_f32_16x16x32_bf16 v[30:33], v[172:175], v[204:207], v[30:33]
	v_mfma_f32_16x16x32_bf16 v[26:29], v[180:183], v[204:207], v[26:29]
	v_mfma_f32_16x16x32_bf16 v[14:17], v[172:175], v[212:215], v[14:17]
	v_mfma_f32_16x16x32_bf16 v[10:13], v[180:183], v[212:215], v[10:13]
	s_barrier
	s_add_i32 s79, 0, 0x18000
	s_add_i32 s80, 0, 0x1c000
	v_add_u32_e32 v158, s79, v166
	v_add_u32_e32 v171, s80, v166
	ds_read_b128 v[130:133], v158
	ds_read_b128 v[134:137], v158 offset:1024
	ds_read_b128 v[154:157], v158 offset:2048
	ds_read_b128 v[158:161], v158 offset:3072
	ds_read_b128 v[162:165], v171
	ds_read_b128 v[172:175], v171 offset:1024
	ds_read_b128 v[176:179], v171 offset:2048
	ds_read_b128 v[180:183], v171 offset:3072
	s_add_u32 s56, s56, 0x80000
	s_addc_u32 s57, s57, 0
	s_mov_b32 m0, s63
	v_lshl_add_u64 v[224:225], s[56:57], 0, v[138:139]
	ds_read_b128 v[184:187], v170 offset:32768
	ds_read_b128 v[188:191], v170 offset:33792
	ds_read_b128 v[192:195], v170 offset:34816
	ds_read_b128 v[196:199], v170 offset:35840
	ds_read_b128 v[200:203], v170 offset:36864
	ds_read_b128 v[204:207], v170 offset:37888
	ds_read_b128 v[208:211], v170 offset:38912
	ds_read_b128 v[212:215], v170 offset:39936
	global_load_lds_dwordx4 v[224:225], off
	v_lshl_add_u64 v[224:225], s[56:57], 0, v[142:143]
	s_mov_b32 m0, s64
	s_nop 0
	global_load_lds_dwordx4 v[224:225], off
	s_waitcnt vmcnt(8)
	s_waitcnt lgkmcnt(0)
	v_mfma_f32_16x16x32_bf16 v[126:129], v[130:133], v[184:187], v[126:129]
	s_barrier
	v_mfma_f32_16x16x32_bf16 v[122:125], v[154:157], v[184:187], v[122:125]
	v_mfma_f32_16x16x32_bf16 v[118:121], v[130:133], v[192:195], v[118:121]
	v_mfma_f32_16x16x32_bf16 v[114:117], v[154:157], v[192:195], v[114:117]
	v_mfma_f32_16x16x32_bf16 v[94:97], v[130:133], v[200:203], v[94:97]
	v_mfma_f32_16x16x32_bf16 v[90:93], v[154:157], v[200:203], v[90:93]
	v_mfma_f32_16x16x32_bf16 v[78:81], v[130:133], v[208:211], v[78:81]
	v_mfma_f32_16x16x32_bf16 v[74:77], v[154:157], v[208:211], v[74:77]
	v_mfma_f32_16x16x32_bf16 v[126:129], v[134:137], v[188:191], v[126:129]
	v_mfma_f32_16x16x32_bf16 v[122:125], v[158:161], v[188:191], v[122:125]
	v_mfma_f32_16x16x32_bf16 v[118:121], v[134:137], v[196:199], v[118:121]
	v_mfma_f32_16x16x32_bf16 v[114:117], v[158:161], v[196:199], v[114:117]
	v_mfma_f32_16x16x32_bf16 v[94:97], v[134:137], v[204:207], v[94:97]
	v_mfma_f32_16x16x32_bf16 v[90:93], v[158:161], v[204:207], v[90:93]
	v_mfma_f32_16x16x32_bf16 v[78:81], v[134:137], v[212:215], v[78:81]
	v_mfma_f32_16x16x32_bf16 v[74:77], v[158:161], v[212:215], v[74:77]
	v_mfma_f32_16x16x32_bf16 v[110:113], v[162:165], v[184:187], v[110:113]
	v_mfma_f32_16x16x32_bf16 v[106:109], v[176:179], v[184:187], v[106:109]
	v_mfma_f32_16x16x32_bf16 v[102:105], v[162:165], v[192:195], v[102:105]
	v_mfma_f32_16x16x32_bf16 v[98:101], v[176:179], v[192:195], v[98:101]
	v_mfma_f32_16x16x32_bf16 v[86:89], v[162:165], v[200:203], v[86:89]
	v_mfma_f32_16x16x32_bf16 v[82:85], v[176:179], v[200:203], v[82:85]
	v_mfma_f32_16x16x32_bf16 v[70:73], v[162:165], v[208:211], v[70:73]
	v_mfma_f32_16x16x32_bf16 v[66:69], v[176:179], v[208:211], v[66:69]
	v_mfma_f32_16x16x32_bf16 v[110:113], v[172:175], v[188:191], v[110:113]
	v_mfma_f32_16x16x32_bf16 v[106:109], v[180:183], v[188:191], v[106:109]
	v_mfma_f32_16x16x32_bf16 v[102:105], v[172:175], v[196:199], v[102:105]
	v_mfma_f32_16x16x32_bf16 v[98:101], v[180:183], v[196:199], v[98:101]
	v_mfma_f32_16x16x32_bf16 v[86:89], v[172:175], v[204:207], v[86:89]
	v_mfma_f32_16x16x32_bf16 v[82:85], v[180:183], v[204:207], v[82:85]
	v_mfma_f32_16x16x32_bf16 v[70:73], v[172:175], v[212:215], v[70:73]
	v_mfma_f32_16x16x32_bf16 v[66:69], v[180:183], v[212:215], v[66:69]
	s_barrier
; #define PG8_STAGE(bufoff, gbase, voff) do { _Pragma("unroll") for (int _i = 0; _i < 2; ++_i) \
;         __builtin_amdgcn_global_load_lds((const unsigned*)((const char*)(gbase) + (voff)[_i]), (PG8_LAS unsigned*)(lds + (bufoff) + ldsw + _i * 8192), 16, 0, 0); } while (0)
; #define PG8_LDA(dst, b, h) do { _Pragma("unroll") for (int m = 0; m < 4; ++m) _Pragma("unroll") for (int k = 0; k < 2; ++k) dst[m][k] = *(const PG8_LAS bf16x8*)(lds + PG8_SA(b, h) + aoff + m * 2048 + k * 1024); } while (0)
; #define PG8_MMA(ai, bj, At, Bt) do { __builtin_amdgcn_s_setprio(1); _Pragma("unroll") for (int m = 0; m < 4; ++m) _Pragma("unroll") for (int n = 0; n < 2; ++n) _Pragma("unroll") for (int k = 0; k < 2; ++k) \
;         acc[ai][bj][m][n] = __builtin_amdgcn_mfma_f32_16x16x32_bf16(Bt[n][k], At[m][k], acc[ai][bj][m][n], 0, 0, 0); __builtin_amdgcn_s_setprio(0); } while (0)
; #define PG8_WAIT_V(n) asm volatile("s_waitcnt vmcnt(" #n ")" ::: "memory")
; #define PG8_WAIT_L(n) asm volatile("s_waitcnt lgkmcnt(" #n ")" ::: "memory")
; #define PG8_BAR __builtin_amdgcn_s_barrier()
; #define PG8_SCHED __builtin_amdgcn_sched_barrier(0)
; template <class Epi, class Sched, bool ALIGN_EPI = false>
; __device__ __forceinline__ void gemm_phase(PG8_LAS unsigned char* lds, const Gemm g, const Sched& S, const Epi& E) {
;     ...
;             PG8_LDA(At, 1, 1); PG8_STAGE(PG8_SB(1, 0), b3, voffB); PG8_STAGE(PG8_SB(1, 1), b3 + hstep, voffB); PG8_STAGE(PG8_SA(1, 0), a3, w0);
;             PG8_WAIT_V(8); PG8_WAIT_L(0); PG8_BAR; PG8_MMA(1, 0, At, B0); PG8_MMA(1, 1, At, B1); PG8_BAR; PG8_SCHED;
;             if constexpr (Epi::KSCALE) { if (((t + 2) & 7) == 0 && t + 2 < nt) { E.kscale(acc, pf, ((t + 2) >> 3) - 1, wr, fr); PG8_SCHED; } }
;         }
;         if constexpr (ALIGN_EPI) { if (wr == 0) PG8_BAR; }
	s_add_i32 s56, s79, s61
	v_lshl_add_u64 v[216:217], v[216:217], 0, s[18:19]
	s_mov_b32 m0, s56
	ds_read_b128 v[184:187], v170 offset:49152
	ds_read_b128 v[188:191], v170 offset:50176
	ds_read_b128 v[192:195], v170 offset:51200
	ds_read_b128 v[196:199], v170 offset:52224
	ds_read_b128 v[200:203], v170 offset:53248
	ds_read_b128 v[204:207], v170 offset:54272
	ds_read_b128 v[208:211], v170 offset:55296
	ds_read_b128 v[212:215], v170 offset:56320
	global_load_lds_dwordx4 v[216:217], off
	s_add_i32 m0, s56, 0x2000
	s_add_u32 s54, s54, 0x80080
	v_lshl_add_u64 v[216:217], v[218:219], 0, s[18:19]
	s_addc_u32 s55, s55, 0
	s_add_i32 s56, s80, s61
	global_load_lds_dwordx4 v[216:217], off
	v_lshl_add_u64 v[216:217], s[54:55], 0, v[140:141]
	s_mov_b32 m0, s56
	s_nop 0
	global_load_lds_dwordx4 v[216:217], off
	v_lshl_add_u64 v[216:217], s[54:55], 0, v[144:145]
	s_add_i32 m0, s56, 0x2000
	s_nop 0
	global_load_lds_dwordx4 v[216:217], off
	v_lshl_add_u64 v[216:217], v[220:221], 0, s[18:19]
	s_mov_b32 m0, s67
	s_nop 0
	global_load_lds_dwordx4 v[216:217], off
	v_lshl_add_u64 v[216:217], v[222:223], 0, s[18:19]
	s_mov_b32 m0, s68
	s_nop 0
	global_load_lds_dwordx4 v[216:217], off
	s_waitcnt vmcnt(8)
	s_waitcnt lgkmcnt(0)
	v_mfma_f32_16x16x32_bf16 v[54:57], v[130:133], v[184:187], v[54:57]
	s_barrier
	v_mfma_f32_16x16x32_bf16 v[50:53], v[154:157], v[184:187], v[50:53]
	v_mfma_f32_16x16x32_bf16 v[38:41], v[130:133], v[192:195], v[38:41]
	v_mfma_f32_16x16x32_bf16 v[34:37], v[154:157], v[192:195], v[34:37]
	v_mfma_f32_16x16x32_bf16 v[22:25], v[130:133], v[200:203], v[22:25]
	v_mfma_f32_16x16x32_bf16 v[18:21], v[154:157], v[200:203], v[18:21]
	v_mfma_f32_16x16x32_bf16 v[6:9], v[130:133], v[208:211], v[6:9]
	v_mfma_f32_16x16x32_bf16 v[2:5], v[154:157], v[208:211], v[2:5]
	v_mfma_f32_16x16x32_bf16 v[54:57], v[134:137], v[188:191], v[54:57]
	v_mfma_f32_16x16x32_bf16 v[50:53], v[158:161], v[188:191], v[50:53]
	v_mfma_f32_16x16x32_bf16 v[38:41], v[134:137], v[196:199], v[38:41]
	v_mfma_f32_16x16x32_bf16 v[34:37], v[158:161], v[196:199], v[34:37]
	v_mfma_f32_16x16x32_bf16 v[22:25], v[134:137], v[204:207], v[22:25]
	v_mfma_f32_16x16x32_bf16 v[18:21], v[158:161], v[204:207], v[18:21]
	v_mfma_f32_16x16x32_bf16 v[6:9], v[134:137], v[212:215], v[6:9]
	v_mfma_f32_16x16x32_bf16 v[2:5], v[158:161], v[212:215], v[2:5]
	v_mfma_f32_16x16x32_bf16 v[62:65], v[162:165], v[184:187], v[62:65]
	v_mfma_f32_16x16x32_bf16 v[58:61], v[176:179], v[184:187], v[58:61]
	v_mfma_f32_16x16x32_bf16 v[46:49], v[162:165], v[192:195], v[46:49]
	v_mfma_f32_16x16x32_bf16 v[42:45], v[176:179], v[192:195], v[42:45]
	v_mfma_f32_16x16x32_bf16 v[30:33], v[162:165], v[200:203], v[30:33]
	v_mfma_f32_16x16x32_bf16 v[26:29], v[176:179], v[200:203], v[26:29]
	v_mfma_f32_16x16x32_bf16 v[14:17], v[162:165], v[208:211], v[14:17]
	v_mfma_f32_16x16x32_bf16 v[10:13], v[176:179], v[208:211], v[10:13]
	v_mfma_f32_16x16x32_bf16 v[62:65], v[172:175], v[188:191], v[62:65]
	v_mfma_f32_16x16x32_bf16 v[58:61], v[180:183], v[188:191], v[58:61]
	v_mfma_f32_16x16x32_bf16 v[46:49], v[172:175], v[196:199], v[46:49]
	v_mfma_f32_16x16x32_bf16 v[42:45], v[180:183], v[196:199], v[42:45]
	v_mfma_f32_16x16x32_bf16 v[30:33], v[172:175], v[204:207], v[30:33]
	v_mfma_f32_16x16x32_bf16 v[26:29], v[180:183], v[204:207], v[26:29]
	v_mfma_f32_16x16x32_bf16 v[14:17], v[172:175], v[212:215], v[14:17]
	v_mfma_f32_16x16x32_bf16 v[10:13], v[180:183], v[212:215], v[10:13]
	s_barrier
	s_add_i32 s78, s78, 2
	s_add_u32 s52, s52, 0x100
	s_addc_u32 s53, s53, 0
	s_add_u32 s76, s76, 0x100
	s_addc_u32 s77, s77, 0
	s_cmp_gt_u32 s78, 29
	s_cbranch_scc0 .LBB0_1198
	s_and_b64 vcc, exec, s[22:23]
	s_cbranch_vccz .LBB0_1201
	s_barrier

; #define PG8_STAGE(bufoff, gbase, voff) do { _Pragma("unroll") for (int _i = 0; _i < 2; ++_i) \
;         __builtin_amdgcn_global_load_lds((const unsigned*)((const char*)(gbase) + (voff)[_i]), (PG8_LAS unsigned*)(lds + (bufoff) + ldsw + _i * 8192), 16, 0, 0); } while (0)
; #define PG8_LDA(dst, b, h) do { _Pragma("unroll") for (int m = 0; m < 4; ++m) _Pragma("unroll") for (int k = 0; k < 2; ++k) dst[m][k] = *(const PG8_LAS bf16x8*)(lds + PG8_SA(b, h) + aoff + m * 2048 + k * 1024); } while (0)
; #define PG8_LDB(dst, b, h) do { _Pragma("unroll") for (int n = 0; n < 2; ++n) _Pragma("unroll") for (int k = 0; k < 2; ++k) dst[n][k] = *(const PG8_LAS bf16x8*)(lds + PG8_SB(b, h) + boff + n * 2048 + k * 1024); } while (0)
; #define PG8_MMA(ai, bj, At, Bt) do { __builtin_amdgcn_s_setprio(1); _Pragma("unroll") for (int m = 0; m < 4; ++m) _Pragma("unroll") for (int n = 0; n < 2; ++n) _Pragma("unroll") for (int k = 0; k < 2; ++k) \
;         acc[ai][bj][m][n] = __builtin_amdgcn_mfma_f32_16x16x32_bf16(Bt[n][k], At[m][k], acc[ai][bj][m][n], 0, 0, 0); __builtin_amdgcn_s_setprio(0); } while (0)
; template <class Epi, class Sched, bool ALIGN_EPI = false>
; __device__ __forceinline__ void gemm_phase(PG8_LAS unsigned char* lds, const Gemm g, const Sched& S, const Epi& E) {
;     ...
;         for (int t = 0; t < nt; t += 2) {
;             const bool last = (t == nt - 2);
;             const char* a1 = cA + (size_t)(t + 1) * kstep;
;             const char* a2 = last ? nA : cA + (size_t)(t + 2) * kstep; const char* b2 = last ? nB : cB + (size_t)(t + 2) * kstep;
;             const char* a3 = a2 + kstep; const char* b3 = b2 + kstep;
;             unsigned w0[2], w1[2];
; #pragma unroll
;             for (int i = 0; i < 2; ++i) { w0[i] = (Sched::GATHER && last) ? vn0[i] : vc0[i]; w1[i] = (Sched::GATHER && last) ? vn1[i] : vc1[i]; }
;             if (last && has_next) S.a_ready(nxt);
;             PG8_LDB(B0, 0, 0); PG8_LDB(B1, 0, 1); PG8_SCHED; PG8_LDA(At, 0, 0); PG8_STAGE(PG8_SA(1, 1), a1 + hstepA, vc1);
;             PG8_WAIT_V(8); PG8_WAIT_L(0); PG8_BAR; PG8_MMA(0, 0, At, B0); PG8_MMA(0, 1, At, B1); PG8_BAR; PG8_SCHED;
;             PG8_LDA(At, 0, 1); PG8_STAGE(PG8_SB(0, 0), b2, voffB); PG8_STAGE(PG8_SB(0, 1), b2 + hstep, voffB); PG8_STAGE(PG8_SA(0, 0), a2, w0);
;             PG8_WAIT_V(8); PG8_WAIT_L(0); PG8_BAR; PG8_MMA(1, 0, At, B0); PG8_MMA(1, 1, At, B1); PG8_BAR; PG8_SCHED;
.LBB0_1414:
	s_add_u32 s56, s36, s54
	v_add_u32_e32 v155, s79, v143
	s_addc_u32 s57, s37, s55
	ds_read_b128 v[164:167], v155
	ds_read_b128 v[168:171], v155 offset:1024
	ds_read_b128 v[172:175], v155 offset:2048
	ds_read_b128 v[176:179], v155 offset:3072
	v_add_u32_e32 v155, s80, v143
	s_add_u32 s58, s56, 0x3c800100
	ds_read_b128 v[180:183], v155
	ds_read_b128 v[184:187], v155 offset:1024
	ds_read_b128 v[188:191], v155 offset:2048
	ds_read_b128 v[192:195], v155 offset:3072
	s_addc_u32 s59, s57, 0
	s_add_u32 s88, s47, s54
	s_addc_u32 s89, s86, s55
	s_cmpk_eq_i32 s54, 0xf00
	s_cselect_b64 vcc, -1, 0
	s_and_b64 s[56:57], vcc, exec
	v_cndmask_b32_e32 v134, v151, v149, vcc
	s_cselect_b32 s59, s21, s59
	s_cselect_b32 s58, s20, s58
	v_cndmask_b32_e32 v153, v152, v157, vcc
	v_cndmask_b32_e32 v228, v150, v162, vcc
	v_cndmask_b32_e32 v155, v154, v163, vcc
	s_cselect_b32 s57, s51, s89
	s_cselect_b32 s56, s50, s88
	v_lshl_add_u64 v[230:231], v[160:161], 0, s[54:55]
	s_add_i32 m0, s53, 0xc000
	ds_read_b128 v[196:199], v147
	ds_read_b128 v[200:203], v147 offset:1024
	ds_read_b128 v[204:207], v147 offset:2048
	ds_read_b128 v[208:211], v147 offset:3072
	ds_read_b128 v[212:215], v147 offset:4096
	ds_read_b128 v[216:219], v147 offset:5120
	ds_read_b128 v[220:223], v147 offset:6144
	ds_read_b128 v[224:227], v147 offset:7168
	global_load_lds_dwordx4 v[230:231], off
	v_lshl_add_u64 v[230:231], v[158:159], 0, s[54:55]
	s_add_i32 m0, s53, 0xe000
	s_nop 0
	global_load_lds_dwordx4 v[230:231], off
	s_waitcnt vmcnt(8)
	s_waitcnt lgkmcnt(0)
	v_mfma_f32_16x16x32_bf16 v[126:129], v[164:167], v[196:199], v[126:129]
	s_barrier
	v_mfma_f32_16x16x32_bf16 v[122:125], v[172:175], v[196:199], v[122:125]
	v_mfma_f32_16x16x32_bf16 v[110:113], v[164:167], v[204:207], v[110:113]
	v_mfma_f32_16x16x32_bf16 v[106:109], v[172:175], v[204:207], v[106:109]
	v_mfma_f32_16x16x32_bf16 v[94:97], v[164:167], v[212:215], v[94:97]
	v_mfma_f32_16x16x32_bf16 v[90:93], v[172:175], v[212:215], v[90:93]
	v_mfma_f32_16x16x32_bf16 v[78:81], v[164:167], v[220:223], v[78:81]
	v_mfma_f32_16x16x32_bf16 v[74:77], v[172:175], v[220:223], v[74:77]
	v_mfma_f32_16x16x32_bf16 v[126:129], v[168:171], v[200:203], v[126:129]
	v_mfma_f32_16x16x32_bf16 v[122:125], v[176:179], v[200:203], v[122:125]
	v_mfma_f32_16x16x32_bf16 v[110:113], v[168:171], v[208:211], v[110:113]
	v_mfma_f32_16x16x32_bf16 v[106:109], v[176:179], v[208:211], v[106:109]
	v_mfma_f32_16x16x32_bf16 v[94:97], v[168:171], v[216:219], v[94:97]
	v_mfma_f32_16x16x32_bf16 v[90:93], v[176:179], v[216:219], v[90:93]
	v_mfma_f32_16x16x32_bf16 v[78:81], v[168:171], v[224:227], v[78:81]
	v_mfma_f32_16x16x32_bf16 v[74:77], v[176:179], v[224:227], v[74:77]
	v_mfma_f32_16x16x32_bf16 v[118:121], v[180:183], v[196:199], v[118:121]
	v_mfma_f32_16x16x32_bf16 v[114:117], v[188:191], v[196:199], v[114:117]
	v_mfma_f32_16x16x32_bf16 v[102:105], v[180:183], v[204:207], v[102:105]
	v_mfma_f32_16x16x32_bf16 v[98:101], v[188:191], v[204:207], v[98:101]
	v_mfma_f32_16x16x32_bf16 v[86:89], v[180:183], v[212:215], v[86:89]
	v_mfma_f32_16x16x32_bf16 v[82:85], v[188:191], v[212:215], v[82:85]
	v_mfma_f32_16x16x32_bf16 v[70:73], v[180:183], v[220:223], v[70:73]
	v_mfma_f32_16x16x32_bf16 v[66:69], v[188:191], v[220:223], v[66:69]
	v_mfma_f32_16x16x32_bf16 v[118:121], v[184:187], v[200:203], v[118:121]
	v_mfma_f32_16x16x32_bf16 v[114:117], v[192:195], v[200:203], v[114:117]
	v_mfma_f32_16x16x32_bf16 v[102:105], v[184:187], v[208:211], v[102:105]
	v_mfma_f32_16x16x32_bf16 v[98:101], v[192:195], v[208:211], v[98:101]
	v_mfma_f32_16x16x32_bf16 v[86:89], v[184:187], v[216:219], v[86:89]
	v_mfma_f32_16x16x32_bf16 v[82:85], v[192:195], v[216:219], v[82:85]
	v_mfma_f32_16x16x32_bf16 v[70:73], v[184:187], v[224:227], v[70:73]
	v_mfma_f32_16x16x32_bf16 v[66:69], v[192:195], v[224:227], v[66:69]
	s_barrier
	s_add_i32 s88, s79, s71
	v_lshl_add_u64 v[230:231], s[56:57], 0, v[130:131]
	s_mov_b32 m0, s88
	ds_read_b128 v[196:199], v147 offset:16384
	ds_read_b128 v[200:203], v147 offset:17408
	ds_read_b128 v[204:207], v147 offset:18432
	ds_read_b128 v[208:211], v147 offset:19456
	ds_read_b128 v[212:215], v147 offset:20480
	ds_read_b128 v[216:219], v147 offset:21504
	ds_read_b128 v[220:223], v147 offset:22528
	ds_read_b128 v[224:227], v147 offset:23552
	global_load_lds_dwordx4 v[230:231], off
	s_add_i32 m0, s88, 0x2000
	s_add_u32 s88, s56, 0x80000
	v_lshl_add_u64 v[232:233], s[56:57], 0, v[132:133]
	s_addc_u32 s89, s57, 0
	s_add_i32 s90, s80, s71
	global_load_lds_dwordx4 v[232:233], off
	v_lshl_add_u64 v[234:235], s[88:89], 0, v[130:131]
	s_mov_b32 m0, s90
	v_mov_b32_e32 v229, v135
	global_load_lds_dwordx4 v[234:235], off
	v_lshl_add_u64 v[234:235], s[88:89], 0, v[132:133]
	s_add_i32 m0, s90, 0x2000
	s_nop 0
	global_load_lds_dwordx4 v[234:235], off
	s_mov_b32 m0, s53
	v_lshl_add_u64 v[234:235], s[58:59], 0, v[134:135]
	global_load_lds_dwordx4 v134, s[58:59]
	s_mov_b32 m0, s72
	s_nop 0
	global_load_lds_dwordx4 v228, s[58:59]
	s_waitcnt vmcnt(8)
	s_waitcnt lgkmcnt(0)
	v_lshl_add_u64 v[228:229], s[58:59], 0, v[228:229]
	v_mfma_f32_16x16x32_bf16 v[62:65], v[164:167], v[196:199], v[62:65]
	s_barrier
; #define PG8_STAGE(bufoff, gbase, voff) do { _Pragma("unroll") for (int _i = 0; _i < 2; ++_i) \
;         __builtin_amdgcn_global_load_lds((const unsigned*)((const char*)(gbase) + (voff)[_i]), (PG8_LAS unsigned*)(lds + (bufoff) + ldsw + _i * 8192), 16, 0, 0); } while (0)
; #define PG8_LDA(dst, b, h) do { _Pragma("unroll") for (int m = 0; m < 4; ++m) _Pragma("unroll") for (int k = 0; k < 2; ++k) dst[m][k] = *(const PG8_LAS bf16x8*)(lds + PG8_SA(b, h) + aoff + m * 2048 + k * 1024); } while (0)
; #define PG8_LDB(dst, b, h) do { _Pragma("unroll") for (int n = 0; n < 2; ++n) _Pragma("unroll") for (int k = 0; k < 2; ++k) dst[n][k] = *(const PG8_LAS bf16x8*)(lds + PG8_SB(b, h) + boff + n * 2048 + k * 1024); } while (0)
; #define PG8_MMA(ai, bj, At, Bt) do { __builtin_amdgcn_s_setprio(1); _Pragma("unroll") for (int m = 0; m < 4; ++m) _Pragma("unroll") for (int n = 0; n < 2; ++n) _Pragma("unroll") for (int k = 0; k < 2; ++k) \
;         acc[ai][bj][m][n] = __builtin_amdgcn_mfma_f32_16x16x32_bf16(Bt[n][k], At[m][k], acc[ai][bj][m][n], 0, 0, 0); __builtin_amdgcn_s_setprio(0); } while (0)
; #define PG8_WAIT_V(n) asm volatile("s_waitcnt vmcnt(" #n ")" ::: "memory")
; #define PG8_WAIT_L(n) asm volatile("s_waitcnt lgkmcnt(" #n ")" ::: "memory")
; #define PG8_BAR __builtin_amdgcn_s_barrier()
; #define PG8_SCHED __builtin_amdgcn_sched_barrier(0)
; template <class Epi, class Sched, bool ALIGN_EPI = false>
; __device__ __forceinline__ void gemm_phase(PG8_LAS unsigned char* lds, const Gemm g, const Sched& S, const Epi& E) {
;     ...
;             PG8_WAIT_V(8); PG8_WAIT_L(0); PG8_BAR; PG8_MMA(1, 0, At, B0); PG8_MMA(1, 1, At, B1); PG8_BAR; PG8_SCHED;
;             PG8_LDB(B0, 1, 0); PG8_LDB(B1, 1, 1); PG8_SCHED; PG8_LDA(At, 1, 0); PG8_STAGE(PG8_SA(0, 1), a2 + hstepA, w1);
;             PG8_WAIT_V(8); PG8_WAIT_L(0); PG8_BAR; PG8_MMA(0, 0, At, B0); PG8_MMA(0, 1, At, B1); PG8_BAR; PG8_SCHED;
	v_mfma_f32_16x16x32_bf16 v[58:61], v[172:175], v[196:199], v[58:61]
	v_mfma_f32_16x16x32_bf16 v[50:53], v[164:167], v[204:207], v[50:53]
	v_mfma_f32_16x16x32_bf16 v[42:45], v[172:175], v[204:207], v[42:45]
	v_mfma_f32_16x16x32_bf16 v[34:37], v[164:167], v[212:215], v[34:37]
	v_mfma_f32_16x16x32_bf16 v[30:33], v[172:175], v[212:215], v[30:33]
	v_mfma_f32_16x16x32_bf16 v[14:17], v[164:167], v[220:223], v[14:17]
	v_mfma_f32_16x16x32_bf16 v[2:5], v[172:175], v[220:223], v[2:5]
	v_mfma_f32_16x16x32_bf16 v[62:65], v[168:171], v[200:203], v[62:65]
	v_mfma_f32_16x16x32_bf16 v[58:61], v[176:179], v[200:203], v[58:61]
	v_mfma_f32_16x16x32_bf16 v[50:53], v[168:171], v[208:211], v[50:53]
	v_mfma_f32_16x16x32_bf16 v[42:45], v[176:179], v[208:211], v[42:45]
	v_mfma_f32_16x16x32_bf16 v[34:37], v[168:171], v[216:219], v[34:37]
	v_mfma_f32_16x16x32_bf16 v[30:33], v[176:179], v[216:219], v[30:33]
	v_mfma_f32_16x16x32_bf16 v[14:17], v[168:171], v[224:227], v[14:17]
	v_mfma_f32_16x16x32_bf16 v[2:5], v[176:179], v[224:227], v[2:5]
	v_mfma_f32_16x16x32_bf16 v[54:57], v[180:183], v[196:199], v[54:57]
	v_mfma_f32_16x16x32_bf16 v[46:49], v[188:191], v[196:199], v[46:49]
	v_mfma_f32_16x16x32_bf16 v[38:41], v[180:183], v[204:207], v[38:41]
	v_mfma_f32_16x16x32_bf16 v[26:29], v[188:191], v[204:207], v[26:29]
	v_mfma_f32_16x16x32_bf16 v[22:25], v[180:183], v[212:215], v[22:25]
	v_mfma_f32_16x16x32_bf16 v[18:21], v[188:191], v[212:215], v[18:21]
	v_mfma_f32_16x16x32_bf16 v[10:13], v[180:183], v[220:223], v[10:13]
	v_mfma_f32_16x16x32_bf16 v[6:9], v[188:191], v[220:223], v[6:9]
	v_mfma_f32_16x16x32_bf16 v[54:57], v[184:187], v[200:203], v[54:57]
	v_mfma_f32_16x16x32_bf16 v[46:49], v[192:195], v[200:203], v[46:49]
	v_mfma_f32_16x16x32_bf16 v[38:41], v[184:187], v[208:211], v[38:41]
	v_mfma_f32_16x16x32_bf16 v[26:29], v[192:195], v[208:211], v[26:29]
	v_mfma_f32_16x16x32_bf16 v[22:25], v[184:187], v[216:219], v[22:25]
	v_mfma_f32_16x16x32_bf16 v[18:21], v[192:195], v[216:219], v[18:21]
	v_mfma_f32_16x16x32_bf16 v[10:13], v[184:187], v[224:227], v[10:13]
	v_mfma_f32_16x16x32_bf16 v[6:9], v[192:195], v[224:227], v[6:9]
	s_barrier
	s_add_i32 s88, 0, 0x18000
	v_add_u32_e32 v134, s88, v143
	s_add_i32 s89, 0, 0x1c000
	ds_read_b128 v[164:167], v134
	ds_read_b128 v[168:171], v134 offset:1024
	ds_read_b128 v[172:175], v134 offset:2048
	ds_read_b128 v[176:179], v134 offset:3072
	v_add_u32_e32 v134, s89, v143
	ds_read_b128 v[180:183], v134
	ds_read_b128 v[184:187], v134 offset:1024
	ds_read_b128 v[188:191], v134 offset:2048
	ds_read_b128 v[192:195], v134 offset:3072
	s_mov_b32 m0, s73
	ds_read_b128 v[196:199], v147 offset:32768
	ds_read_b128 v[200:203], v147 offset:33792
	ds_read_b128 v[204:207], v147 offset:34816
	ds_read_b128 v[208:211], v147 offset:35840
	ds_read_b128 v[212:215], v147 offset:36864
	ds_read_b128 v[216:219], v147 offset:37888
	ds_read_b128 v[220:223], v147 offset:38912
	ds_read_b128 v[224:227], v147 offset:39936
	global_load_lds_dwordx4 v153, s[58:59]
	s_mov_b32 m0, s74
	s_nop 0
	global_load_lds_dwordx4 v155, s[58:59]
	s_waitcnt vmcnt(8)
	s_waitcnt lgkmcnt(0)
	v_mfma_f32_16x16x32_bf16 v[126:129], v[164:167], v[196:199], v[126:129]
	s_barrier
	v_mfma_f32_16x16x32_bf16 v[122:125], v[172:175], v[196:199], v[122:125]
	v_mfma_f32_16x16x32_bf16 v[110:113], v[164:167], v[204:207], v[110:113]
	v_mfma_f32_16x16x32_bf16 v[106:109], v[172:175], v[204:207], v[106:109]
	v_mfma_f32_16x16x32_bf16 v[94:97], v[164:167], v[212:215], v[94:97]
	v_mfma_f32_16x16x32_bf16 v[90:93], v[172:175], v[212:215], v[90:93]
	v_mfma_f32_16x16x32_bf16 v[78:81], v[164:167], v[220:223], v[78:81]
	v_mfma_f32_16x16x32_bf16 v[74:77], v[172:175], v[220:223], v[74:77]
	v_mfma_f32_16x16x32_bf16 v[126:129], v[168:171], v[200:203], v[126:129]
	v_mfma_f32_16x16x32_bf16 v[122:125], v[176:179], v[200:203], v[122:125]
	v_mfma_f32_16x16x32_bf16 v[110:113], v[168:171], v[208:211], v[110:113]
	v_mfma_f32_16x16x32_bf16 v[106:109], v[176:179], v[208:211], v[106:109]
	v_mfma_f32_16x16x32_bf16 v[94:97], v[168:171], v[216:219], v[94:97]
	v_mfma_f32_16x16x32_bf16 v[90:93], v[176:179], v[216:219], v[90:93]
	v_mfma_f32_16x16x32_bf16 v[78:81], v[168:171], v[224:227], v[78:81]
	v_mfma_f32_16x16x32_bf16 v[74:77], v[176:179], v[224:227], v[74:77]
	v_mfma_f32_16x16x32_bf16 v[118:121], v[180:183], v[196:199], v[118:121]
	v_mfma_f32_16x16x32_bf16 v[114:117], v[188:191], v[196:199], v[114:117]
	v_mfma_f32_16x16x32_bf16 v[102:105], v[180:183], v[204:207], v[102:105]
	v_mfma_f32_16x16x32_bf16 v[98:101], v[188:191], v[204:207], v[98:101]
	v_mfma_f32_16x16x32_bf16 v[86:89], v[180:183], v[212:215], v[86:89]
	v_mfma_f32_16x16x32_bf16 v[82:85], v[188:191], v[212:215], v[82:85]
	v_mfma_f32_16x16x32_bf16 v[70:73], v[180:183], v[220:223], v[70:73]
	v_mfma_f32_16x16x32_bf16 v[66:69], v[188:191], v[220:223], v[66:69]
	v_mfma_f32_16x16x32_bf16 v[118:121], v[184:187], v[200:203], v[118:121]
	v_mfma_f32_16x16x32_bf16 v[114:117], v[192:195], v[200:203], v[114:117]
	v_mfma_f32_16x16x32_bf16 v[102:105], v[184:187], v[208:211], v[102:105]
	v_mfma_f32_16x16x32_bf16 v[98:101], v[192:195], v[208:211], v[98:101]
	v_mfma_f32_16x16x32_bf16 v[86:89], v[184:187], v[216:219], v[86:89]
	v_mfma_f32_16x16x32_bf16 v[82:85], v[192:195], v[216:219], v[82:85]
	v_mfma_f32_16x16x32_bf16 v[70:73], v[184:187], v[224:227], v[70:73]
	v_mfma_f32_16x16x32_bf16 v[66:69], v[192:195], v[224:227], v[66:69]
	s_barrier
; #define PG8_STAGE(bufoff, gbase, voff) do { _Pragma("unroll") for (int _i = 0; _i < 2; ++_i) \
;         __builtin_amdgcn_global_load_lds((const unsigned*)((const char*)(gbase) + (voff)[_i]), (PG8_LAS unsigned*)(lds + (bufoff) + ldsw + _i * 8192), 16, 0, 0); } while (0)
; #define PG8_LDA(dst, b, h) do { _Pragma("unroll") for (int m = 0; m < 4; ++m) _Pragma("unroll") for (int k = 0; k < 2; ++k) dst[m][k] = *(const PG8_LAS bf16x8*)(lds + PG8_SA(b, h) + aoff + m * 2048 + k * 1024); } while (0)
; #define PG8_MMA(ai, bj, At, Bt) do { __builtin_amdgcn_s_setprio(1); _Pragma("unroll") for (int m = 0; m < 4; ++m) _Pragma("unroll") for (int n = 0; n < 2; ++n) _Pragma("unroll") for (int k = 0; k < 2; ++k) \
;         acc[ai][bj][m][n] = __builtin_amdgcn_mfma_f32_16x16x32_bf16(Bt[n][k], At[m][k], acc[ai][bj][m][n], 0, 0, 0); __builtin_amdgcn_s_setprio(0); } while (0)
; #define PG8_WAIT_V(n) asm volatile("s_waitcnt vmcnt(" #n ")" ::: "memory")
; #define PG8_WAIT_L(n) asm volatile("s_waitcnt lgkmcnt(" #n ")" ::: "memory")
; #define PG8_BAR __builtin_amdgcn_s_barrier()
; #define PG8_SCHED __builtin_amdgcn_sched_barrier(0)
; template <class Epi, class Sched, bool ALIGN_EPI = false>
; __device__ __forceinline__ void gemm_phase(PG8_LAS unsigned char* lds, const Gemm g, const Sched& S, const Epi& E) {
;     ...
;             PG8_LDA(At, 1, 1); PG8_STAGE(PG8_SB(1, 0), b3, voffB); PG8_STAGE(PG8_SB(1, 1), b3 + hstep, voffB); PG8_STAGE(PG8_SA(1, 0), a3, w0);
;             PG8_WAIT_V(8); PG8_WAIT_L(0); PG8_BAR; PG8_MMA(1, 0, At, B0); PG8_MMA(1, 1, At, B1); PG8_BAR; PG8_SCHED;
;             if constexpr (Epi::KSCALE) { if (((t + 2) & 7) == 0 && t + 2 < nt) { E.kscale(acc, pf, ((t + 2) >> 3) - 1, wr, fr); PG8_SCHED; } }
;         }
;         if constexpr (ALIGN_EPI) { if (wr == 0) PG8_BAR; }
	s_add_i32 s58, s88, s71
	v_lshl_add_u64 v[230:231], v[230:231], 0, s[42:43]
	s_mov_b32 m0, s58
	ds_read_b128 v[196:199], v147 offset:49152
	ds_read_b128 v[200:203], v147 offset:50176
	ds_read_b128 v[204:207], v147 offset:51200
	ds_read_b128 v[208:211], v147 offset:52224
	ds_read_b128 v[212:215], v147 offset:53248
	ds_read_b128 v[216:219], v147 offset:54272
	ds_read_b128 v[220:223], v147 offset:55296
	ds_read_b128 v[224:227], v147 offset:56320
	global_load_lds_dwordx4 v[230:231], off
	s_add_i32 m0, s58, 0x2000
	s_add_u32 s56, s56, 0x80080
	v_lshl_add_u64 v[230:231], v[232:233], 0, s[42:43]
	s_addc_u32 s57, s57, 0
	s_add_i32 s58, s89, s71
	global_load_lds_dwordx4 v[230:231], off
	v_lshl_add_u64 v[230:231], s[56:57], 0, v[130:131]
	s_mov_b32 m0, s58
	v_lshl_add_u64 v[228:229], v[228:229], 0, s[42:43]
	global_load_lds_dwordx4 v[230:231], off
	v_lshl_add_u64 v[230:231], s[56:57], 0, v[132:133]
	s_add_i32 m0, s58, 0x2000
	s_nop 0
	global_load_lds_dwordx4 v[230:231], off
	v_lshl_add_u64 v[230:231], v[234:235], 0, s[42:43]
	s_mov_b32 m0, s77
	s_nop 0
	global_load_lds_dwordx4 v[230:231], off
	s_mov_b32 m0, s78
	s_nop 0
	global_load_lds_dwordx4 v[228:229], off
	s_waitcnt vmcnt(8)
	s_waitcnt lgkmcnt(0)
	v_mfma_f32_16x16x32_bf16 v[62:65], v[164:167], v[196:199], v[62:65]
	s_barrier
	v_mfma_f32_16x16x32_bf16 v[58:61], v[172:175], v[196:199], v[58:61]
	v_mfma_f32_16x16x32_bf16 v[50:53], v[164:167], v[204:207], v[50:53]
	v_mfma_f32_16x16x32_bf16 v[42:45], v[172:175], v[204:207], v[42:45]
	v_mfma_f32_16x16x32_bf16 v[34:37], v[164:167], v[212:215], v[34:37]
	v_mfma_f32_16x16x32_bf16 v[30:33], v[172:175], v[212:215], v[30:33]
	v_mfma_f32_16x16x32_bf16 v[14:17], v[164:167], v[220:223], v[14:17]
	v_mfma_f32_16x16x32_bf16 v[2:5], v[172:175], v[220:223], v[2:5]
	v_mfma_f32_16x16x32_bf16 v[62:65], v[168:171], v[200:203], v[62:65]
	v_mfma_f32_16x16x32_bf16 v[58:61], v[176:179], v[200:203], v[58:61]
	v_mfma_f32_16x16x32_bf16 v[50:53], v[168:171], v[208:211], v[50:53]
	v_mfma_f32_16x16x32_bf16 v[42:45], v[176:179], v[208:211], v[42:45]
	v_mfma_f32_16x16x32_bf16 v[34:37], v[168:171], v[216:219], v[34:37]
	v_mfma_f32_16x16x32_bf16 v[30:33], v[176:179], v[216:219], v[30:33]
	v_mfma_f32_16x16x32_bf16 v[14:17], v[168:171], v[224:227], v[14:17]
	v_mfma_f32_16x16x32_bf16 v[2:5], v[176:179], v[224:227], v[2:5]
	v_mfma_f32_16x16x32_bf16 v[54:57], v[180:183], v[196:199], v[54:57]
	v_mfma_f32_16x16x32_bf16 v[46:49], v[188:191], v[196:199], v[46:49]
	v_mfma_f32_16x16x32_bf16 v[38:41], v[180:183], v[204:207], v[38:41]
	v_mfma_f32_16x16x32_bf16 v[26:29], v[188:191], v[204:207], v[26:29]
	v_mfma_f32_16x16x32_bf16 v[22:25], v[180:183], v[212:215], v[22:25]
	v_mfma_f32_16x16x32_bf16 v[18:21], v[188:191], v[212:215], v[18:21]
	v_mfma_f32_16x16x32_bf16 v[10:13], v[180:183], v[220:223], v[10:13]
	v_mfma_f32_16x16x32_bf16 v[6:9], v[188:191], v[220:223], v[6:9]
	v_mfma_f32_16x16x32_bf16 v[54:57], v[184:187], v[200:203], v[54:57]
	v_mfma_f32_16x16x32_bf16 v[46:49], v[192:195], v[200:203], v[46:49]
	v_mfma_f32_16x16x32_bf16 v[38:41], v[184:187], v[208:211], v[38:41]
	v_mfma_f32_16x16x32_bf16 v[26:29], v[192:195], v[208:211], v[26:29]
	v_mfma_f32_16x16x32_bf16 v[22:25], v[184:187], v[216:219], v[22:25]
	v_mfma_f32_16x16x32_bf16 v[18:21], v[192:195], v[216:219], v[18:21]
	v_mfma_f32_16x16x32_bf16 v[10:13], v[184:187], v[224:227], v[10:13]
	v_mfma_f32_16x16x32_bf16 v[6:9], v[192:195], v[224:227], v[6:9]
	s_barrier
	s_add_i32 s87, s87, 2
	s_add_u32 s54, s54, 0x100
	s_addc_u32 s55, s55, 0
	s_cmp_gt_u32 s87, 29
	s_cbranch_scc0 .LBB0_1414
	s_and_b64 vcc, exec, s[44:45]
	s_cbranch_vccz .LBB0_1417
	s_barrier

; #define PG8_STAGE(bufoff, gbase, voff) do { _Pragma("unroll") for (int _i = 0; _i < 2; ++_i) \
;         __builtin_amdgcn_global_load_lds((const unsigned*)((const char*)(gbase) + (voff)[_i]), (PG8_LAS unsigned*)(lds + (bufoff) + ldsw + _i * 8192), 16, 0, 0); } while (0)
; #define PG8_LDA(dst, b, h) do { _Pragma("unroll") for (int m = 0; m < 4; ++m) _Pragma("unroll") for (int k = 0; k < 2; ++k) dst[m][k] = *(const PG8_LAS bf16x8*)(lds + PG8_SA(b, h) + aoff + m * 2048 + k * 1024); } while (0)
; #define PG8_LDB(dst, b, h) do { _Pragma("unroll") for (int n = 0; n < 2; ++n) _Pragma("unroll") for (int k = 0; k < 2; ++k) dst[n][k] = *(const PG8_LAS bf16x8*)(lds + PG8_SB(b, h) + boff + n * 2048 + k * 1024); } while (0)
; #define PG8_MMA(ai, bj, At, Bt) do { __builtin_amdgcn_s_setprio(1); _Pragma("unroll") for (int m = 0; m < 4; ++m) _Pragma("unroll") for (int n = 0; n < 2; ++n) _Pragma("unroll") for (int k = 0; k < 2; ++k) \
;         acc[ai][bj][m][n] = __builtin_amdgcn_mfma_f32_16x16x32_bf16(Bt[n][k], At[m][k], acc[ai][bj][m][n], 0, 0, 0); __builtin_amdgcn_s_setprio(0); } while (0)
; template <class Epi, class Sched, bool ALIGN_EPI = false>
; __device__ __forceinline__ void gemm_phase(PG8_LAS unsigned char* lds, const Gemm g, const Sched& S, const Epi& E) {
;     ...
;         for (int t = 0; t < nt; t += 2) {
;             const bool last = (t == nt - 2);
;             const char* a1 = cA + (size_t)(t + 1) * kstep;
;             const char* a2 = last ? nA : cA + (size_t)(t + 2) * kstep; const char* b2 = last ? nB : cB + (size_t)(t + 2) * kstep;
;             const char* a3 = a2 + kstep; const char* b3 = b2 + kstep;
;             unsigned w0[2], w1[2];
; #pragma unroll
;             for (int i = 0; i < 2; ++i) { w0[i] = (Sched::GATHER && last) ? vn0[i] : vc0[i]; w1[i] = (Sched::GATHER && last) ? vn1[i] : vc1[i]; }
;             if (last && has_next) S.a_ready(nxt);
;             PG8_LDB(B0, 0, 0); PG8_LDB(B1, 0, 1); PG8_SCHED; PG8_LDA(At, 0, 0); PG8_STAGE(PG8_SA(1, 1), a1 + hstepA, vc1);
;             PG8_WAIT_V(8); PG8_WAIT_L(0); PG8_BAR; PG8_MMA(0, 0, At, B0); PG8_MMA(0, 1, At, B1); PG8_BAR; PG8_SCHED;
;             PG8_LDA(At, 0, 1); PG8_STAGE(PG8_SB(0, 0), b2, voffB); PG8_STAGE(PG8_SB(0, 1), b2 + hstep, voffB); PG8_STAGE(PG8_SA(0, 0), a2, w0);
;             PG8_WAIT_V(8); PG8_WAIT_L(0); PG8_BAR; PG8_MMA(1, 0, At, B0); PG8_MMA(1, 1, At, B1); PG8_BAR; PG8_SCHED;
.LBB0_1480:
	ds_read_b128 v[172:175], v167
	ds_read_b128 v[176:179], v167 offset:1024
	ds_read_b128 v[180:183], v167 offset:2048
	ds_read_b128 v[184:187], v167 offset:3072
	ds_read_b128 v[188:191], v168
	ds_read_b128 v[192:195], v168 offset:1024
	ds_read_b128 v[196:199], v168 offset:2048
	ds_read_b128 v[200:203], v168 offset:3072
	s_add_u32 s16, s14, 0x3c800100
	s_addc_u32 s17, s15, 0
	s_add_u32 s56, s14, s43
	s_addc_u32 s57, s15, s44
	s_cmp_eq_u32 s45, 28
	s_cselect_b32 s19, s21, s17
	s_cselect_b32 s18, s20, s16
	s_cselect_b32 s17, s11, s57
	s_cselect_b32 s16, s10, s56
	s_mov_b32 m0, s46
	v_lshl_add_u64 v[236:237], s[14:15], 0, v[160:161]
	ds_read_b128 v[204:207], v169
	ds_read_b128 v[208:211], v169 offset:1024
	ds_read_b128 v[212:215], v169 offset:2048
	ds_read_b128 v[216:219], v169 offset:3072
	ds_read_b128 v[220:223], v169 offset:4096
	ds_read_b128 v[224:227], v169 offset:5120
	ds_read_b128 v[228:231], v169 offset:6144
	ds_read_b128 v[232:235], v169 offset:7168
	global_load_lds_dwordx4 v[236:237], off
	v_lshl_add_u64 v[236:237], s[14:15], 0, v[158:159]
	s_mov_b32 m0, s47
	s_nop 0
	global_load_lds_dwordx4 v[236:237], off
	s_waitcnt vmcnt(8)
	s_waitcnt lgkmcnt(0)
	v_mfma_f32_16x16x32_bf16 v[126:129], v[172:175], v[204:207], v[126:129]
	s_barrier
	v_mfma_f32_16x16x32_bf16 v[122:125], v[180:183], v[204:207], v[122:125]
	v_mfma_f32_16x16x32_bf16 v[110:113], v[172:175], v[212:215], v[110:113]
	v_mfma_f32_16x16x32_bf16 v[106:109], v[180:183], v[212:215], v[106:109]
	v_mfma_f32_16x16x32_bf16 v[94:97], v[172:175], v[220:223], v[94:97]
	v_mfma_f32_16x16x32_bf16 v[90:93], v[180:183], v[220:223], v[90:93]
	v_mfma_f32_16x16x32_bf16 v[78:81], v[172:175], v[228:231], v[78:81]
	v_mfma_f32_16x16x32_bf16 v[74:77], v[180:183], v[228:231], v[74:77]
	v_mfma_f32_16x16x32_bf16 v[126:129], v[176:179], v[208:211], v[126:129]
	v_mfma_f32_16x16x32_bf16 v[122:125], v[184:187], v[208:211], v[122:125]
	v_mfma_f32_16x16x32_bf16 v[110:113], v[176:179], v[216:219], v[110:113]
	v_mfma_f32_16x16x32_bf16 v[106:109], v[184:187], v[216:219], v[106:109]
	v_mfma_f32_16x16x32_bf16 v[94:97], v[176:179], v[224:227], v[94:97]
	v_mfma_f32_16x16x32_bf16 v[90:93], v[184:187], v[224:227], v[90:93]
	v_mfma_f32_16x16x32_bf16 v[78:81], v[176:179], v[232:235], v[78:81]
	v_mfma_f32_16x16x32_bf16 v[74:77], v[184:187], v[232:235], v[74:77]
	v_mfma_f32_16x16x32_bf16 v[118:121], v[188:191], v[204:207], v[118:121]
	v_mfma_f32_16x16x32_bf16 v[114:117], v[196:199], v[204:207], v[114:117]
	v_mfma_f32_16x16x32_bf16 v[102:105], v[188:191], v[212:215], v[102:105]
	v_mfma_f32_16x16x32_bf16 v[98:101], v[196:199], v[212:215], v[98:101]
	v_mfma_f32_16x16x32_bf16 v[86:89], v[188:191], v[220:223], v[86:89]
	v_mfma_f32_16x16x32_bf16 v[82:85], v[196:199], v[220:223], v[82:85]
	v_mfma_f32_16x16x32_bf16 v[70:73], v[188:191], v[228:231], v[70:73]
	v_mfma_f32_16x16x32_bf16 v[66:69], v[196:199], v[228:231], v[66:69]
	v_mfma_f32_16x16x32_bf16 v[118:121], v[192:195], v[208:211], v[118:121]
	v_mfma_f32_16x16x32_bf16 v[114:117], v[200:203], v[208:211], v[114:117]
	v_mfma_f32_16x16x32_bf16 v[102:105], v[192:195], v[216:219], v[102:105]
	v_mfma_f32_16x16x32_bf16 v[98:101], v[200:203], v[216:219], v[98:101]
	v_mfma_f32_16x16x32_bf16 v[86:89], v[192:195], v[224:227], v[86:89]
	v_mfma_f32_16x16x32_bf16 v[82:85], v[200:203], v[224:227], v[82:85]
	v_mfma_f32_16x16x32_bf16 v[70:73], v[192:195], v[232:235], v[70:73]
	v_mfma_f32_16x16x32_bf16 v[66:69], v[200:203], v[232:235], v[66:69]
	s_barrier
	s_mov_b32 m0, s48
	v_lshl_add_u64 v[236:237], s[16:17], 0, v[146:147]
	s_add_u32 s56, s16, 0x80000
	ds_read_b128 v[204:207], v169 offset:16384
	ds_read_b128 v[208:211], v169 offset:17408
	ds_read_b128 v[212:215], v169 offset:18432
	ds_read_b128 v[216:219], v169 offset:19456
	ds_read_b128 v[220:223], v169 offset:20480
	ds_read_b128 v[224:227], v169 offset:21504
	ds_read_b128 v[228:231], v169 offset:22528
	ds_read_b128 v[232:235], v169 offset:23552
	global_load_lds_dwordx4 v[236:237], off
	v_lshl_add_u64 v[238:239], s[16:17], 0, v[144:145]
	s_mov_b32 m0, s49
	s_addc_u32 s57, s17, 0
	global_load_lds_dwordx4 v[238:239], off
	v_lshl_add_u64 v[240:241], s[56:57], 0, v[146:147]
	s_mov_b32 m0, s50
	v_lshl_add_u64 v[242:243], s[18:19], 0, v[150:151]
	global_load_lds_dwordx4 v[240:241], off
	v_lshl_add_u64 v[240:241], s[56:57], 0, v[144:145]
	s_mov_b32 m0, s51
	s_nop 0
	global_load_lds_dwordx4 v[240:241], off
	v_lshl_add_u64 v[240:241], s[18:19], 0, v[148:149]
	s_mov_b32 m0, s25
	s_nop 0
	global_load_lds_dwordx4 v[240:241], off
	s_mov_b32 m0, s26
	s_nop 0
	global_load_lds_dwordx4 v[242:243], off
	s_waitcnt vmcnt(8)
	s_waitcnt lgkmcnt(0)
	v_mfma_f32_16x16x32_bf16 v[62:65], v[172:175], v[204:207], v[62:65]
	s_barrier
; #define PG8_STAGE(bufoff, gbase, voff) do { _Pragma("unroll") for (int _i = 0; _i < 2; ++_i) \
;         __builtin_amdgcn_global_load_lds((const unsigned*)((const char*)(gbase) + (voff)[_i]), (PG8_LAS unsigned*)(lds + (bufoff) + ldsw + _i * 8192), 16, 0, 0); } while (0)
; #define PG8_LDA(dst, b, h) do { _Pragma("unroll") for (int m = 0; m < 4; ++m) _Pragma("unroll") for (int k = 0; k < 2; ++k) dst[m][k] = *(const PG8_LAS bf16x8*)(lds + PG8_SA(b, h) + aoff + m * 2048 + k * 1024); } while (0)
; #define PG8_LDB(dst, b, h) do { _Pragma("unroll") for (int n = 0; n < 2; ++n) _Pragma("unroll") for (int k = 0; k < 2; ++k) dst[n][k] = *(const PG8_LAS bf16x8*)(lds + PG8_SB(b, h) + boff + n * 2048 + k * 1024); } while (0)
; #define PG8_MMA(ai, bj, At, Bt) do { __builtin_amdgcn_s_setprio(1); _Pragma("unroll") for (int m = 0; m < 4; ++m) _Pragma("unroll") for (int n = 0; n < 2; ++n) _Pragma("unroll") for (int k = 0; k < 2; ++k) \
;         acc[ai][bj][m][n] = __builtin_amdgcn_mfma_f32_16x16x32_bf16(Bt[n][k], At[m][k], acc[ai][bj][m][n], 0, 0, 0); __builtin_amdgcn_s_setprio(0); } while (0)
; #define PG8_WAIT_V(n) asm volatile("s_waitcnt vmcnt(" #n ")" ::: "memory")
; #define PG8_WAIT_L(n) asm volatile("s_waitcnt lgkmcnt(" #n ")" ::: "memory")
; #define PG8_BAR __builtin_amdgcn_s_barrier()
; #define PG8_SCHED __builtin_amdgcn_sched_barrier(0)
; template <class Epi, class Sched, bool ALIGN_EPI = false>
; __device__ __forceinline__ void gemm_phase(PG8_LAS unsigned char* lds, const Gemm g, const Sched& S, const Epi& E) {
;     ...
;             PG8_WAIT_V(8); PG8_WAIT_L(0); PG8_BAR; PG8_MMA(1, 0, At, B0); PG8_MMA(1, 1, At, B1); PG8_BAR; PG8_SCHED;
;             PG8_LDB(B0, 1, 0); PG8_LDB(B1, 1, 1); PG8_SCHED; PG8_LDA(At, 1, 0); PG8_STAGE(PG8_SA(0, 1), a2 + hstepA, w1);
;             PG8_WAIT_V(8); PG8_WAIT_L(0); PG8_BAR; PG8_MMA(0, 0, At, B0); PG8_MMA(0, 1, At, B1); PG8_BAR; PG8_SCHED;
	v_mfma_f32_16x16x32_bf16 v[58:61], v[180:183], v[204:207], v[58:61]
	v_mfma_f32_16x16x32_bf16 v[50:53], v[172:175], v[212:215], v[50:53]
	v_mfma_f32_16x16x32_bf16 v[42:45], v[180:183], v[212:215], v[42:45]
	v_mfma_f32_16x16x32_bf16 v[34:37], v[172:175], v[220:223], v[34:37]
	v_mfma_f32_16x16x32_bf16 v[26:29], v[180:183], v[220:223], v[26:29]
	v_mfma_f32_16x16x32_bf16 v[14:17], v[172:175], v[228:231], v[14:17]
	v_mfma_f32_16x16x32_bf16 v[2:5], v[180:183], v[228:231], v[2:5]
	v_mfma_f32_16x16x32_bf16 v[62:65], v[176:179], v[208:211], v[62:65]
	v_mfma_f32_16x16x32_bf16 v[58:61], v[184:187], v[208:211], v[58:61]
	v_mfma_f32_16x16x32_bf16 v[50:53], v[176:179], v[216:219], v[50:53]
	v_mfma_f32_16x16x32_bf16 v[42:45], v[184:187], v[216:219], v[42:45]
	v_mfma_f32_16x16x32_bf16 v[34:37], v[176:179], v[224:227], v[34:37]
	v_mfma_f32_16x16x32_bf16 v[26:29], v[184:187], v[224:227], v[26:29]
	v_mfma_f32_16x16x32_bf16 v[14:17], v[176:179], v[232:235], v[14:17]
	v_mfma_f32_16x16x32_bf16 v[2:5], v[184:187], v[232:235], v[2:5]
	v_mfma_f32_16x16x32_bf16 v[54:57], v[188:191], v[204:207], v[54:57]
	v_mfma_f32_16x16x32_bf16 v[46:49], v[196:199], v[204:207], v[46:49]
	v_mfma_f32_16x16x32_bf16 v[38:41], v[188:191], v[212:215], v[38:41]
	v_mfma_f32_16x16x32_bf16 v[30:33], v[196:199], v[212:215], v[30:33]
	v_mfma_f32_16x16x32_bf16 v[22:25], v[188:191], v[220:223], v[22:25]
	v_mfma_f32_16x16x32_bf16 v[18:21], v[196:199], v[220:223], v[18:21]
	v_mfma_f32_16x16x32_bf16 v[10:13], v[188:191], v[228:231], v[10:13]
	v_mfma_f32_16x16x32_bf16 v[6:9], v[196:199], v[228:231], v[6:9]
	v_mfma_f32_16x16x32_bf16 v[54:57], v[192:195], v[208:211], v[54:57]
	v_mfma_f32_16x16x32_bf16 v[46:49], v[200:203], v[208:211], v[46:49]
	v_mfma_f32_16x16x32_bf16 v[38:41], v[192:195], v[216:219], v[38:41]
	v_mfma_f32_16x16x32_bf16 v[30:33], v[200:203], v[216:219], v[30:33]
	v_mfma_f32_16x16x32_bf16 v[22:25], v[192:195], v[224:227], v[22:25]
	v_mfma_f32_16x16x32_bf16 v[18:21], v[200:203], v[224:227], v[18:21]
	v_mfma_f32_16x16x32_bf16 v[10:13], v[192:195], v[232:235], v[10:13]
	v_mfma_f32_16x16x32_bf16 v[6:9], v[200:203], v[232:235], v[6:9]
	s_barrier
	ds_read_b128 v[172:175], v170
	ds_read_b128 v[176:179], v170 offset:1024
	ds_read_b128 v[180:183], v170 offset:2048
	ds_read_b128 v[184:187], v170 offset:3072
	ds_read_b128 v[188:191], v171
	ds_read_b128 v[192:195], v171 offset:1024
	ds_read_b128 v[196:199], v171 offset:2048
	ds_read_b128 v[200:203], v171 offset:3072
	s_mov_b32 m0, s27
	v_lshl_add_u64 v[244:245], s[18:19], 0, v[152:153]
	ds_read_b128 v[204:207], v169 offset:32768
	ds_read_b128 v[208:211], v169 offset:33792
	ds_read_b128 v[212:215], v169 offset:34816
	ds_read_b128 v[216:219], v169 offset:35840
	ds_read_b128 v[220:223], v169 offset:36864
	ds_read_b128 v[224:227], v169 offset:37888
	ds_read_b128 v[228:231], v169 offset:38912
	ds_read_b128 v[232:235], v169 offset:39936
	global_load_lds_dwordx4 v[244:245], off
	v_lshl_add_u64 v[244:245], s[18:19], 0, v[154:155]
	s_mov_b32 m0, s35
	s_nop 0
	global_load_lds_dwordx4 v[244:245], off
	s_waitcnt vmcnt(8)
	s_waitcnt lgkmcnt(0)
	v_mfma_f32_16x16x32_bf16 v[126:129], v[172:175], v[204:207], v[126:129]
	s_barrier
	v_mfma_f32_16x16x32_bf16 v[122:125], v[180:183], v[204:207], v[122:125]
	v_mfma_f32_16x16x32_bf16 v[110:113], v[172:175], v[212:215], v[110:113]
	v_mfma_f32_16x16x32_bf16 v[106:109], v[180:183], v[212:215], v[106:109]
	v_mfma_f32_16x16x32_bf16 v[94:97], v[172:175], v[220:223], v[94:97]
	v_mfma_f32_16x16x32_bf16 v[90:93], v[180:183], v[220:223], v[90:93]
	v_mfma_f32_16x16x32_bf16 v[78:81], v[172:175], v[228:231], v[78:81]
	v_mfma_f32_16x16x32_bf16 v[74:77], v[180:183], v[228:231], v[74:77]
	v_mfma_f32_16x16x32_bf16 v[126:129], v[176:179], v[208:211], v[126:129]
	v_mfma_f32_16x16x32_bf16 v[122:125], v[184:187], v[208:211], v[122:125]
	v_mfma_f32_16x16x32_bf16 v[110:113], v[176:179], v[216:219], v[110:113]
	v_mfma_f32_16x16x32_bf16 v[106:109], v[184:187], v[216:219], v[106:109]
	v_mfma_f32_16x16x32_bf16 v[94:97], v[176:179], v[224:227], v[94:97]
	v_mfma_f32_16x16x32_bf16 v[90:93], v[184:187], v[224:227], v[90:93]
	v_mfma_f32_16x16x32_bf16 v[78:81], v[176:179], v[232:235], v[78:81]
	v_mfma_f32_16x16x32_bf16 v[74:77], v[184:187], v[232:235], v[74:77]
	v_mfma_f32_16x16x32_bf16 v[118:121], v[188:191], v[204:207], v[118:121]
	v_mfma_f32_16x16x32_bf16 v[114:117], v[196:199], v[204:207], v[114:117]
	v_mfma_f32_16x16x32_bf16 v[102:105], v[188:191], v[212:215], v[102:105]
	v_mfma_f32_16x16x32_bf16 v[98:101], v[196:199], v[212:215], v[98:101]
	v_mfma_f32_16x16x32_bf16 v[86:89], v[188:191], v[220:223], v[86:89]
	v_mfma_f32_16x16x32_bf16 v[82:85], v[196:199], v[220:223], v[82:85]
	v_mfma_f32_16x16x32_bf16 v[70:73], v[188:191], v[228:231], v[70:73]
	v_mfma_f32_16x16x32_bf16 v[66:69], v[196:199], v[228:231], v[66:69]
	v_mfma_f32_16x16x32_bf16 v[118:121], v[192:195], v[208:211], v[118:121]
	v_mfma_f32_16x16x32_bf16 v[114:117], v[200:203], v[208:211], v[114:117]
	v_mfma_f32_16x16x32_bf16 v[102:105], v[192:195], v[216:219], v[102:105]
	v_mfma_f32_16x16x32_bf16 v[98:101], v[200:203], v[216:219], v[98:101]
	v_mfma_f32_16x16x32_bf16 v[86:89], v[192:195], v[224:227], v[86:89]
	v_mfma_f32_16x16x32_bf16 v[82:85], v[200:203], v[224:227], v[82:85]
	v_mfma_f32_16x16x32_bf16 v[70:73], v[192:195], v[232:235], v[70:73]
	v_mfma_f32_16x16x32_bf16 v[66:69], v[200:203], v[232:235], v[66:69]
	s_barrier
; #define PG8_STAGE(bufoff, gbase, voff) do { _Pragma("unroll") for (int _i = 0; _i < 2; ++_i) \
;         __builtin_amdgcn_global_load_lds((const unsigned*)((const char*)(gbase) + (voff)[_i]), (PG8_LAS unsigned*)(lds + (bufoff) + ldsw + _i * 8192), 16, 0, 0); } while (0)
; #define PG8_LDA(dst, b, h) do { _Pragma("unroll") for (int m = 0; m < 4; ++m) _Pragma("unroll") for (int k = 0; k < 2; ++k) dst[m][k] = *(const PG8_LAS bf16x8*)(lds + PG8_SA(b, h) + aoff + m * 2048 + k * 1024); } while (0)
; #define PG8_MMA(ai, bj, At, Bt) do { __builtin_amdgcn_s_setprio(1); _Pragma("unroll") for (int m = 0; m < 4; ++m) _Pragma("unroll") for (int n = 0; n < 2; ++n) _Pragma("unroll") for (int k = 0; k < 2; ++k) \
;         acc[ai][bj][m][n] = __builtin_amdgcn_mfma_f32_16x16x32_bf16(Bt[n][k], At[m][k], acc[ai][bj][m][n], 0, 0, 0); __builtin_amdgcn_s_setprio(0); } while (0)
; #define PG8_WAIT_V(n) asm volatile("s_waitcnt vmcnt(" #n ")" ::: "memory")
; #define PG8_WAIT_L(n) asm volatile("s_waitcnt lgkmcnt(" #n ")" ::: "memory")
; #define PG8_BAR __builtin_amdgcn_s_barrier()
; #define PG8_SCHED __builtin_amdgcn_sched_barrier(0)
; template <class Epi, class Sched, bool ALIGN_EPI = false>
; __device__ __forceinline__ void gemm_phase(PG8_LAS unsigned char* lds, const Gemm g, const Sched& S, const Epi& E) {
;     ...
;             PG8_LDA(At, 1, 1); PG8_STAGE(PG8_SB(1, 0), b3, voffB); PG8_STAGE(PG8_SB(1, 1), b3 + hstep, voffB); PG8_STAGE(PG8_SA(1, 0), a3, w0);
;             PG8_WAIT_V(8); PG8_WAIT_L(0); PG8_BAR; PG8_MMA(1, 0, At, B0); PG8_MMA(1, 1, At, B1); PG8_BAR; PG8_SCHED;
;             if constexpr (Epi::KSCALE) { if (((t + 2) & 7) == 0 && t + 2 < nt) { E.kscale(acc, pf, ((t + 2) >> 3) - 1, wr, fr); PG8_SCHED; } }
;         }
;         if constexpr (ALIGN_EPI) { if (wr == 0) PG8_BAR; }
	s_mov_b32 m0, s52
	v_lshl_add_u64 v[236:237], v[236:237], 0, s[12:13]
	s_add_u32 s16, s16, 0x80080
	ds_read_b128 v[204:207], v169 offset:49152
	ds_read_b128 v[208:211], v169 offset:50176
	ds_read_b128 v[212:215], v169 offset:51200
	ds_read_b128 v[216:219], v169 offset:52224
	ds_read_b128 v[220:223], v169 offset:53248
	ds_read_b128 v[224:227], v169 offset:54272
	ds_read_b128 v[228:231], v169 offset:55296
	ds_read_b128 v[232:235], v169 offset:56320
	global_load_lds_dwordx4 v[236:237], off
	v_lshl_add_u64 v[236:237], v[238:239], 0, s[12:13]
	s_mov_b32 m0, s53
	s_addc_u32 s17, s17, 0
	global_load_lds_dwordx4 v[236:237], off
	v_lshl_add_u64 v[236:237], s[16:17], 0, v[146:147]
	s_mov_b32 m0, s54
	s_nop 0
	global_load_lds_dwordx4 v[236:237], off
	v_lshl_add_u64 v[236:237], s[16:17], 0, v[144:145]
	s_mov_b32 m0, s55
	s_nop 0
	global_load_lds_dwordx4 v[236:237], off
	v_lshl_add_u64 v[236:237], v[240:241], 0, s[12:13]
	s_mov_b32 m0, s41
	s_nop 0
	global_load_lds_dwordx4 v[236:237], off
	v_lshl_add_u64 v[236:237], v[242:243], 0, s[12:13]
	s_mov_b32 m0, s42
	s_nop 0
	global_load_lds_dwordx4 v[236:237], off
	s_waitcnt vmcnt(8)
	s_waitcnt lgkmcnt(0)
	v_mfma_f32_16x16x32_bf16 v[62:65], v[172:175], v[204:207], v[62:65]
	s_barrier
	v_mfma_f32_16x16x32_bf16 v[58:61], v[180:183], v[204:207], v[58:61]
	v_mfma_f32_16x16x32_bf16 v[50:53], v[172:175], v[212:215], v[50:53]
	v_mfma_f32_16x16x32_bf16 v[42:45], v[180:183], v[212:215], v[42:45]
	v_mfma_f32_16x16x32_bf16 v[34:37], v[172:175], v[220:223], v[34:37]
	v_mfma_f32_16x16x32_bf16 v[26:29], v[180:183], v[220:223], v[26:29]
	v_mfma_f32_16x16x32_bf16 v[14:17], v[172:175], v[228:231], v[14:17]
	v_mfma_f32_16x16x32_bf16 v[2:5], v[180:183], v[228:231], v[2:5]
	v_mfma_f32_16x16x32_bf16 v[62:65], v[176:179], v[208:211], v[62:65]
	v_mfma_f32_16x16x32_bf16 v[58:61], v[184:187], v[208:211], v[58:61]
	v_mfma_f32_16x16x32_bf16 v[50:53], v[176:179], v[216:219], v[50:53]
	v_mfma_f32_16x16x32_bf16 v[42:45], v[184:187], v[216:219], v[42:45]
	v_mfma_f32_16x16x32_bf16 v[34:37], v[176:179], v[224:227], v[34:37]
	v_mfma_f32_16x16x32_bf16 v[26:29], v[184:187], v[224:227], v[26:29]
	v_mfma_f32_16x16x32_bf16 v[14:17], v[176:179], v[232:235], v[14:17]
	v_mfma_f32_16x16x32_bf16 v[2:5], v[184:187], v[232:235], v[2:5]
	v_mfma_f32_16x16x32_bf16 v[54:57], v[188:191], v[204:207], v[54:57]
	v_mfma_f32_16x16x32_bf16 v[46:49], v[196:199], v[204:207], v[46:49]
	v_mfma_f32_16x16x32_bf16 v[38:41], v[188:191], v[212:215], v[38:41]
	v_mfma_f32_16x16x32_bf16 v[30:33], v[196:199], v[212:215], v[30:33]
	v_mfma_f32_16x16x32_bf16 v[22:25], v[188:191], v[220:223], v[22:25]
	v_mfma_f32_16x16x32_bf16 v[18:21], v[196:199], v[220:223], v[18:21]
	v_mfma_f32_16x16x32_bf16 v[10:13], v[188:191], v[228:231], v[10:13]
	v_mfma_f32_16x16x32_bf16 v[6:9], v[196:199], v[228:231], v[6:9]
	v_mfma_f32_16x16x32_bf16 v[54:57], v[192:195], v[208:211], v[54:57]
	v_mfma_f32_16x16x32_bf16 v[46:49], v[200:203], v[208:211], v[46:49]
	v_mfma_f32_16x16x32_bf16 v[38:41], v[192:195], v[216:219], v[38:41]
	v_mfma_f32_16x16x32_bf16 v[30:33], v[200:203], v[216:219], v[30:33]
	v_mfma_f32_16x16x32_bf16 v[22:25], v[192:195], v[224:227], v[22:25]
	v_mfma_f32_16x16x32_bf16 v[18:21], v[200:203], v[224:227], v[18:21]
	v_mfma_f32_16x16x32_bf16 v[10:13], v[192:195], v[232:235], v[10:13]
	v_mfma_f32_16x16x32_bf16 v[6:9], v[200:203], v[232:235], v[6:9]
	s_barrier
	s_add_i32 s45, s45, 2
	s_add_u32 s14, s14, 0x100
	s_addc_u32 s15, s15, 0
	s_cmp_gt_u32 s45, 29
	s_cbranch_scc0 .LBB0_1480
	s_cmpk_lt_u32 s22, 0x100
	s_cbranch_scc0 .LBB0_1483
	s_barrier

; #define PG8_STAGE(bufoff, gbase, voff) do { _Pragma("unroll") for (int _i = 0; _i < 2; ++_i) \
;         __builtin_amdgcn_global_load_lds((const unsigned*)((const char*)(gbase) + (voff)[_i]), (PG8_LAS unsigned*)(lds + (bufoff) + ldsw + _i * 8192), 16, 0, 0); } while (0)
; #define PG8_LDA(dst, b, h) do { _Pragma("unroll") for (int m = 0; m < 4; ++m) _Pragma("unroll") for (int k = 0; k < 2; ++k) dst[m][k] = *(const PG8_LAS bf16x8*)(lds + PG8_SA(b, h) + aoff + m * 2048 + k * 1024); } while (0)
; #define PG8_LDB(dst, b, h) do { _Pragma("unroll") for (int n = 0; n < 2; ++n) _Pragma("unroll") for (int k = 0; k < 2; ++k) dst[n][k] = *(const PG8_LAS bf16x8*)(lds + PG8_SB(b, h) + boff + n * 2048 + k * 1024); } while (0)
; #define PG8_MMA(ai, bj, At, Bt) do { __builtin_amdgcn_s_setprio(1); _Pragma("unroll") for (int m = 0; m < 4; ++m) _Pragma("unroll") for (int n = 0; n < 2; ++n) _Pragma("unroll") for (int k = 0; k < 2; ++k) \
;         acc[ai][bj][m][n] = __builtin_amdgcn_mfma_f32_16x16x32_bf16(Bt[n][k], At[m][k], acc[ai][bj][m][n], 0, 0, 0); __builtin_amdgcn_s_setprio(0); } while (0)
; template <class Epi, class Sched, bool ALIGN_EPI = false>
; __device__ __forceinline__ void gemm_phase(PG8_LAS unsigned char* lds, const Gemm g, const Sched& S, const Epi& E) {
;     ...
;         for (int t = 0; t < nt; t += 2) {
;             const bool last = (t == nt - 2);
;             const char* a1 = cA + (size_t)(t + 1) * kstep;
;             const char* a2 = last ? nA : cA + (size_t)(t + 2) * kstep; const char* b2 = last ? nB : cB + (size_t)(t + 2) * kstep;
;             const char* a3 = a2 + kstep; const char* b3 = b2 + kstep;
;             unsigned w0[2], w1[2];
; #pragma unroll
;             for (int i = 0; i < 2; ++i) { w0[i] = (Sched::GATHER && last) ? vn0[i] : vc0[i]; w1[i] = (Sched::GATHER && last) ? vn1[i] : vc1[i]; }
;             if (last && has_next) S.a_ready(nxt);
;             PG8_LDB(B0, 0, 0); PG8_LDB(B1, 0, 1); PG8_SCHED; PG8_LDA(At, 0, 0); PG8_STAGE(PG8_SA(1, 1), a1 + hstepA, vc1);
;             PG8_WAIT_V(8); PG8_WAIT_L(0); PG8_BAR; PG8_MMA(0, 0, At, B0); PG8_MMA(0, 1, At, B1); PG8_BAR; PG8_SCHED;
;             PG8_LDA(At, 0, 1); PG8_STAGE(PG8_SB(0, 0), b2, voffB); PG8_STAGE(PG8_SB(0, 1), b2 + hstep, voffB); PG8_STAGE(PG8_SA(0, 0), a2, w0);
;             PG8_WAIT_V(8); PG8_WAIT_L(0); PG8_BAR; PG8_MMA(1, 0, At, B0); PG8_MMA(1, 1, At, B1); PG8_BAR; PG8_SCHED;
.LBB0_1498:
	ds_read_b128 v[142:145], v1
	ds_read_b128 v[158:161], v1 offset:1024
	ds_read_b128 v[162:165], v1 offset:2048
	ds_read_b128 v[166:169], v1 offset:3072
	ds_read_b128 v[170:173], v156
	ds_read_b128 v[174:177], v156 offset:1024
	ds_read_b128 v[178:181], v156 offset:2048
	ds_read_b128 v[182:185], v156 offset:3072
	s_add_u32 s58, s56, 0xfffe0080
	s_addc_u32 s59, s57, -1
	s_cmp_eq_u32 s87, 4
	s_cselect_b32 s61, s41, s59
	s_cselect_b32 s60, s53, s58
	s_cselect_b32 s59, s43, s86
	s_cselect_b32 s58, s84, s85
	v_lshl_add_u64 v[218:219], s[56:57], 0, v[140:141]
	s_add_i32 m0, s55, 0xc000
	ds_read_b128 v[186:189], v157
	ds_read_b128 v[190:193], v157 offset:1024
	ds_read_b128 v[194:197], v157 offset:2048
	ds_read_b128 v[198:201], v157 offset:3072
	ds_read_b128 v[202:205], v157 offset:4096
	ds_read_b128 v[206:209], v157 offset:5120
	ds_read_b128 v[210:213], v157 offset:6144
	ds_read_b128 v[214:217], v157 offset:7168
	global_load_lds_dwordx4 v[218:219], off
	v_lshl_add_u64 v[218:219], s[56:57], 0, v[138:139]
	s_add_i32 m0, s55, 0xe000
	s_nop 0
	global_load_lds_dwordx4 v[218:219], off
	s_waitcnt vmcnt(8)
	s_waitcnt lgkmcnt(0)
	v_mfma_f32_16x16x32_bf16 v[126:129], v[142:145], v[186:189], v[126:129]
	s_barrier
	v_mfma_f32_16x16x32_bf16 v[122:125], v[162:165], v[186:189], v[122:125]
	v_mfma_f32_16x16x32_bf16 v[114:117], v[142:145], v[194:197], v[114:117]
	v_mfma_f32_16x16x32_bf16 v[106:109], v[162:165], v[194:197], v[106:109]
	v_mfma_f32_16x16x32_bf16 v[98:101], v[142:145], v[202:205], v[98:101]
	v_mfma_f32_16x16x32_bf16 v[90:93], v[162:165], v[202:205], v[90:93]
	v_mfma_f32_16x16x32_bf16 v[82:85], v[142:145], v[210:213], v[82:85]
	v_mfma_f32_16x16x32_bf16 v[74:77], v[162:165], v[210:213], v[74:77]
	v_mfma_f32_16x16x32_bf16 v[126:129], v[158:161], v[190:193], v[126:129]
	v_mfma_f32_16x16x32_bf16 v[122:125], v[166:169], v[190:193], v[122:125]
	v_mfma_f32_16x16x32_bf16 v[114:117], v[158:161], v[198:201], v[114:117]
	v_mfma_f32_16x16x32_bf16 v[106:109], v[166:169], v[198:201], v[106:109]
	v_mfma_f32_16x16x32_bf16 v[98:101], v[158:161], v[206:209], v[98:101]
	v_mfma_f32_16x16x32_bf16 v[90:93], v[166:169], v[206:209], v[90:93]
	v_mfma_f32_16x16x32_bf16 v[82:85], v[158:161], v[214:217], v[82:85]
	v_mfma_f32_16x16x32_bf16 v[74:77], v[166:169], v[214:217], v[74:77]
	v_mfma_f32_16x16x32_bf16 v[118:121], v[170:173], v[186:189], v[118:121]
	v_mfma_f32_16x16x32_bf16 v[110:113], v[178:181], v[186:189], v[110:113]
	v_mfma_f32_16x16x32_bf16 v[102:105], v[170:173], v[194:197], v[102:105]
	v_mfma_f32_16x16x32_bf16 v[94:97], v[178:181], v[194:197], v[94:97]
	v_mfma_f32_16x16x32_bf16 v[86:89], v[170:173], v[202:205], v[86:89]
	v_mfma_f32_16x16x32_bf16 v[78:81], v[178:181], v[202:205], v[78:81]
	v_mfma_f32_16x16x32_bf16 v[62:65], v[170:173], v[210:213], v[62:65]
	v_mfma_f32_16x16x32_bf16 v[58:61], v[178:181], v[210:213], v[58:61]
	v_mfma_f32_16x16x32_bf16 v[118:121], v[174:177], v[190:193], v[118:121]
	v_mfma_f32_16x16x32_bf16 v[110:113], v[182:185], v[190:193], v[110:113]
	v_mfma_f32_16x16x32_bf16 v[102:105], v[174:177], v[198:201], v[102:105]
	v_mfma_f32_16x16x32_bf16 v[94:97], v[182:185], v[198:201], v[94:97]
	v_mfma_f32_16x16x32_bf16 v[86:89], v[174:177], v[206:209], v[86:89]
	v_mfma_f32_16x16x32_bf16 v[78:81], v[182:185], v[206:209], v[78:81]
	v_mfma_f32_16x16x32_bf16 v[62:65], v[174:177], v[214:217], v[62:65]
	v_mfma_f32_16x16x32_bf16 v[58:61], v[182:185], v[214:217], v[58:61]
	s_barrier
	s_add_i32 s88, s74, s62
	v_lshl_add_u64 v[218:219], s[58:59], 0, v[132:133]
	s_mov_b32 m0, s88
	ds_read_b128 v[186:189], v157 offset:16384
	ds_read_b128 v[190:193], v157 offset:17408
	ds_read_b128 v[194:197], v157 offset:18432
	ds_read_b128 v[198:201], v157 offset:19456
	ds_read_b128 v[202:205], v157 offset:20480
	ds_read_b128 v[206:209], v157 offset:21504
	ds_read_b128 v[210:213], v157 offset:22528
	ds_read_b128 v[214:217], v157 offset:23552
	global_load_lds_dwordx4 v[218:219], off
	s_add_i32 m0, s88, 0x2000
	s_add_u32 s88, s58, 0x20000
	v_lshl_add_u64 v[220:221], s[58:59], 0, v[136:137]
	s_addc_u32 s89, s59, 0
	s_add_i32 s90, s75, s62
	global_load_lds_dwordx4 v[220:221], off
	v_lshl_add_u64 v[222:223], s[88:89], 0, v[132:133]
	s_mov_b32 m0, s90
	v_lshl_add_u64 v[224:225], s[60:61], 0, v[134:135]
	global_load_lds_dwordx4 v[222:223], off
	v_lshl_add_u64 v[222:223], s[88:89], 0, v[136:137]
	s_add_i32 m0, s90, 0x2000
	s_nop 0
	global_load_lds_dwordx4 v[222:223], off
	v_lshl_add_u64 v[222:223], s[60:61], 0, v[130:131]
	s_mov_b32 m0, s55
	s_nop 0
	global_load_lds_dwordx4 v[222:223], off
	s_mov_b32 m0, s63
	s_nop 0
	global_load_lds_dwordx4 v[224:225], off
	s_waitcnt vmcnt(8)
	s_waitcnt lgkmcnt(0)
	v_mfma_f32_16x16x32_bf16 v[54:57], v[142:145], v[186:189], v[54:57]
	s_barrier
; #define PG8_STAGE(bufoff, gbase, voff) do { _Pragma("unroll") for (int _i = 0; _i < 2; ++_i) \
;         __builtin_amdgcn_global_load_lds((const unsigned*)((const char*)(gbase) + (voff)[_i]), (PG8_LAS unsigned*)(lds + (bufoff) + ldsw + _i * 8192), 16, 0, 0); } while (0)
; #define PG8_LDA(dst, b, h) do { _Pragma("unroll") for (int m = 0; m < 4; ++m) _Pragma("unroll") for (int k = 0; k < 2; ++k) dst[m][k] = *(const PG8_LAS bf16x8*)(lds + PG8_SA(b, h) + aoff + m * 2048 + k * 1024); } while (0)
; #define PG8_LDB(dst, b, h) do { _Pragma("unroll") for (int n = 0; n < 2; ++n) _Pragma("unroll") for (int k = 0; k < 2; ++k) dst[n][k] = *(const PG8_LAS bf16x8*)(lds + PG8_SB(b, h) + boff + n * 2048 + k * 1024); } while (0)
; #define PG8_MMA(ai, bj, At, Bt) do { __builtin_amdgcn_s_setprio(1); _Pragma("unroll") for (int m = 0; m < 4; ++m) _Pragma("unroll") for (int n = 0; n < 2; ++n) _Pragma("unroll") for (int k = 0; k < 2; ++k) \
;         acc[ai][bj][m][n] = __builtin_amdgcn_mfma_f32_16x16x32_bf16(Bt[n][k], At[m][k], acc[ai][bj][m][n], 0, 0, 0); __builtin_amdgcn_s_setprio(0); } while (0)
; #define PG8_WAIT_V(n) asm volatile("s_waitcnt vmcnt(" #n ")" ::: "memory")
; #define PG8_WAIT_L(n) asm volatile("s_waitcnt lgkmcnt(" #n ")" ::: "memory")
; #define PG8_BAR __builtin_amdgcn_s_barrier()
; #define PG8_SCHED __builtin_amdgcn_sched_barrier(0)
; template <class Epi, class Sched, bool ALIGN_EPI = false>
; __device__ __forceinline__ void gemm_phase(PG8_LAS unsigned char* lds, const Gemm g, const Sched& S, const Epi& E) {
;     ...
;             PG8_WAIT_V(8); PG8_WAIT_L(0); PG8_BAR; PG8_MMA(1, 0, At, B0); PG8_MMA(1, 1, At, B1); PG8_BAR; PG8_SCHED;
;             PG8_LDB(B0, 1, 0); PG8_LDB(B1, 1, 1); PG8_SCHED; PG8_LDA(At, 1, 0); PG8_STAGE(PG8_SA(0, 1), a2 + hstepA, w1);
;             PG8_WAIT_V(8); PG8_WAIT_L(0); PG8_BAR; PG8_MMA(0, 0, At, B0); PG8_MMA(0, 1, At, B1); PG8_BAR; PG8_SCHED;
	v_mfma_f32_16x16x32_bf16 v[42:45], v[162:165], v[186:189], v[42:45]
	v_mfma_f32_16x16x32_bf16 v[30:33], v[142:145], v[194:197], v[30:33]
	v_mfma_f32_16x16x32_bf16 v[26:29], v[162:165], v[194:197], v[26:29]
	v_mfma_f32_16x16x32_bf16 v[14:17], v[142:145], v[202:205], v[14:17]
	v_mfma_f32_16x16x32_bf16 v[10:13], v[162:165], v[202:205], v[10:13]
	v_mfma_f32_16x16x32_bf16 v[6:9], v[142:145], v[210:213], v[6:9]
	v_mfma_f32_16x16x32_bf16 v[2:5], v[162:165], v[210:213], v[2:5]
	v_mfma_f32_16x16x32_bf16 v[54:57], v[158:161], v[190:193], v[54:57]
	v_mfma_f32_16x16x32_bf16 v[42:45], v[166:169], v[190:193], v[42:45]
	v_mfma_f32_16x16x32_bf16 v[30:33], v[158:161], v[198:201], v[30:33]
	v_mfma_f32_16x16x32_bf16 v[26:29], v[166:169], v[198:201], v[26:29]
	v_mfma_f32_16x16x32_bf16 v[14:17], v[158:161], v[206:209], v[14:17]
	v_mfma_f32_16x16x32_bf16 v[10:13], v[166:169], v[206:209], v[10:13]
	v_mfma_f32_16x16x32_bf16 v[6:9], v[158:161], v[214:217], v[6:9]
	v_mfma_f32_16x16x32_bf16 v[2:5], v[166:169], v[214:217], v[2:5]
	v_mfma_f32_16x16x32_bf16 v[70:73], v[170:173], v[186:189], v[70:73]
	v_mfma_f32_16x16x32_bf16 v[66:69], v[178:181], v[186:189], v[66:69]
	v_mfma_f32_16x16x32_bf16 v[50:53], v[170:173], v[194:197], v[50:53]
	v_mfma_f32_16x16x32_bf16 v[46:49], v[178:181], v[194:197], v[46:49]
	v_mfma_f32_16x16x32_bf16 v[38:41], v[170:173], v[202:205], v[38:41]
	v_mfma_f32_16x16x32_bf16 v[34:37], v[178:181], v[202:205], v[34:37]
	v_mfma_f32_16x16x32_bf16 v[22:25], v[170:173], v[210:213], v[22:25]
	v_mfma_f32_16x16x32_bf16 v[18:21], v[178:181], v[210:213], v[18:21]
	v_mfma_f32_16x16x32_bf16 v[70:73], v[174:177], v[190:193], v[70:73]
	v_mfma_f32_16x16x32_bf16 v[66:69], v[182:185], v[190:193], v[66:69]
	v_mfma_f32_16x16x32_bf16 v[50:53], v[174:177], v[198:201], v[50:53]
	v_mfma_f32_16x16x32_bf16 v[46:49], v[182:185], v[198:201], v[46:49]
	v_mfma_f32_16x16x32_bf16 v[38:41], v[174:177], v[206:209], v[38:41]
	v_mfma_f32_16x16x32_bf16 v[34:37], v[182:185], v[206:209], v[34:37]
	v_mfma_f32_16x16x32_bf16 v[22:25], v[174:177], v[214:217], v[22:25]
	v_mfma_f32_16x16x32_bf16 v[18:21], v[182:185], v[214:217], v[18:21]
	s_barrier
	s_add_i32 s88, 0, 0x18000
	s_add_i32 s89, 0, 0x1c000
	v_add_u32_e32 v166, s88, v147
	v_add_u32_e32 v182, s89, v147
	ds_read_b128 v[142:145], v166
	ds_read_b128 v[158:161], v166 offset:1024
	ds_read_b128 v[162:165], v166 offset:2048
	ds_read_b128 v[166:169], v166 offset:3072
	ds_read_b128 v[170:173], v182
	ds_read_b128 v[174:177], v182 offset:1024
	ds_read_b128 v[178:181], v182 offset:2048
	ds_read_b128 v[182:185], v182 offset:3072
	s_add_u32 s60, s60, 0x20000
	s_addc_u32 s61, s61, 0
	s_mov_b32 m0, s64
	v_lshl_add_u64 v[226:227], s[60:61], 0, v[130:131]
	ds_read_b128 v[186:189], v157 offset:32768
	ds_read_b128 v[190:193], v157 offset:33792
	ds_read_b128 v[194:197], v157 offset:34816
	ds_read_b128 v[198:201], v157 offset:35840
	ds_read_b128 v[202:205], v157 offset:36864
	ds_read_b128 v[206:209], v157 offset:37888
	ds_read_b128 v[210:213], v157 offset:38912
	ds_read_b128 v[214:217], v157 offset:39936
	global_load_lds_dwordx4 v[226:227], off
	v_lshl_add_u64 v[226:227], s[60:61], 0, v[134:135]
	s_mov_b32 m0, s65
	s_nop 0
	global_load_lds_dwordx4 v[226:227], off
	s_waitcnt vmcnt(8)
	s_waitcnt lgkmcnt(0)
	v_mfma_f32_16x16x32_bf16 v[126:129], v[142:145], v[186:189], v[126:129]
	s_barrier
	v_mfma_f32_16x16x32_bf16 v[122:125], v[162:165], v[186:189], v[122:125]
	v_mfma_f32_16x16x32_bf16 v[114:117], v[142:145], v[194:197], v[114:117]
	v_mfma_f32_16x16x32_bf16 v[106:109], v[162:165], v[194:197], v[106:109]
	v_mfma_f32_16x16x32_bf16 v[98:101], v[142:145], v[202:205], v[98:101]
	v_mfma_f32_16x16x32_bf16 v[90:93], v[162:165], v[202:205], v[90:93]
	v_mfma_f32_16x16x32_bf16 v[82:85], v[142:145], v[210:213], v[82:85]
	v_mfma_f32_16x16x32_bf16 v[74:77], v[162:165], v[210:213], v[74:77]
	v_mfma_f32_16x16x32_bf16 v[126:129], v[158:161], v[190:193], v[126:129]
	v_mfma_f32_16x16x32_bf16 v[122:125], v[166:169], v[190:193], v[122:125]
	v_mfma_f32_16x16x32_bf16 v[114:117], v[158:161], v[198:201], v[114:117]
	v_mfma_f32_16x16x32_bf16 v[106:109], v[166:169], v[198:201], v[106:109]
	v_mfma_f32_16x16x32_bf16 v[98:101], v[158:161], v[206:209], v[98:101]
	v_mfma_f32_16x16x32_bf16 v[90:93], v[166:169], v[206:209], v[90:93]
	v_mfma_f32_16x16x32_bf16 v[82:85], v[158:161], v[214:217], v[82:85]
	v_mfma_f32_16x16x32_bf16 v[74:77], v[166:169], v[214:217], v[74:77]
	v_mfma_f32_16x16x32_bf16 v[118:121], v[170:173], v[186:189], v[118:121]
	v_mfma_f32_16x16x32_bf16 v[110:113], v[178:181], v[186:189], v[110:113]
	v_mfma_f32_16x16x32_bf16 v[102:105], v[170:173], v[194:197], v[102:105]
	v_mfma_f32_16x16x32_bf16 v[94:97], v[178:181], v[194:197], v[94:97]
	v_mfma_f32_16x16x32_bf16 v[86:89], v[170:173], v[202:205], v[86:89]
	v_mfma_f32_16x16x32_bf16 v[78:81], v[178:181], v[202:205], v[78:81]
	v_mfma_f32_16x16x32_bf16 v[62:65], v[170:173], v[210:213], v[62:65]
	v_mfma_f32_16x16x32_bf16 v[58:61], v[178:181], v[210:213], v[58:61]
	v_mfma_f32_16x16x32_bf16 v[118:121], v[174:177], v[190:193], v[118:121]
	v_mfma_f32_16x16x32_bf16 v[110:113], v[182:185], v[190:193], v[110:113]
	v_mfma_f32_16x16x32_bf16 v[102:105], v[174:177], v[198:201], v[102:105]
	v_mfma_f32_16x16x32_bf16 v[94:97], v[182:185], v[198:201], v[94:97]
	v_mfma_f32_16x16x32_bf16 v[86:89], v[174:177], v[206:209], v[86:89]
	v_mfma_f32_16x16x32_bf16 v[78:81], v[182:185], v[206:209], v[78:81]
	v_mfma_f32_16x16x32_bf16 v[62:65], v[174:177], v[214:217], v[62:65]
	v_mfma_f32_16x16x32_bf16 v[58:61], v[182:185], v[214:217], v[58:61]
	s_barrier
; #define PG8_STAGE(bufoff, gbase, voff) do { _Pragma("unroll") for (int _i = 0; _i < 2; ++_i) \
;         __builtin_amdgcn_global_load_lds((const unsigned*)((const char*)(gbase) + (voff)[_i]), (PG8_LAS unsigned*)(lds + (bufoff) + ldsw + _i * 8192), 16, 0, 0); } while (0)
; #define PG8_LDA(dst, b, h) do { _Pragma("unroll") for (int m = 0; m < 4; ++m) _Pragma("unroll") for (int k = 0; k < 2; ++k) dst[m][k] = *(const PG8_LAS bf16x8*)(lds + PG8_SA(b, h) + aoff + m * 2048 + k * 1024); } while (0)
; #define PG8_MMA(ai, bj, At, Bt) do { __builtin_amdgcn_s_setprio(1); _Pragma("unroll") for (int m = 0; m < 4; ++m) _Pragma("unroll") for (int n = 0; n < 2; ++n) _Pragma("unroll") for (int k = 0; k < 2; ++k) \
;         acc[ai][bj][m][n] = __builtin_amdgcn_mfma_f32_16x16x32_bf16(Bt[n][k], At[m][k], acc[ai][bj][m][n], 0, 0, 0); __builtin_amdgcn_s_setprio(0); } while (0)
; #define PG8_WAIT_V(n) asm volatile("s_waitcnt vmcnt(" #n ")" ::: "memory")
; #define PG8_WAIT_L(n) asm volatile("s_waitcnt lgkmcnt(" #n ")" ::: "memory")
; #define PG8_BAR __builtin_amdgcn_s_barrier()
; #define PG8_SCHED __builtin_amdgcn_sched_barrier(0)
; template <class Epi, class Sched, bool ALIGN_EPI = false>
; __device__ __forceinline__ void gemm_phase(PG8_LAS unsigned char* lds, const Gemm g, const Sched& S, const Epi& E) {
;     ...
;             PG8_LDA(At, 1, 1); PG8_STAGE(PG8_SB(1, 0), b3, voffB); PG8_STAGE(PG8_SB(1, 1), b3 + hstep, voffB); PG8_STAGE(PG8_SA(1, 0), a3, w0);
;             PG8_WAIT_V(8); PG8_WAIT_L(0); PG8_BAR; PG8_MMA(1, 0, At, B0); PG8_MMA(1, 1, At, B1); PG8_BAR; PG8_SCHED;
;             if constexpr (Epi::KSCALE) { if (((t + 2) & 7) == 0 && t + 2 < nt) { E.kscale(acc, pf, ((t + 2) >> 3) - 1, wr, fr); PG8_SCHED; } }
;         }
;         if constexpr (ALIGN_EPI) { if (wr == 0) PG8_BAR; }
	s_add_i32 s60, s88, s62
	v_lshl_add_u64 v[218:219], v[218:219], 0, s[16:17]
	s_mov_b32 m0, s60
	ds_read_b128 v[186:189], v157 offset:49152
	ds_read_b128 v[190:193], v157 offset:50176
	ds_read_b128 v[194:197], v157 offset:51200
	ds_read_b128 v[198:201], v157 offset:52224
	ds_read_b128 v[202:205], v157 offset:53248
	ds_read_b128 v[206:209], v157 offset:54272
	ds_read_b128 v[210:213], v157 offset:55296
	ds_read_b128 v[214:217], v157 offset:56320
	global_load_lds_dwordx4 v[218:219], off
	s_add_i32 m0, s60, 0x2000
	s_add_u32 s58, s58, 0x20080
	v_lshl_add_u64 v[218:219], v[220:221], 0, s[16:17]
	s_addc_u32 s59, s59, 0
	s_add_i32 s60, s89, s62
	global_load_lds_dwordx4 v[218:219], off
	v_lshl_add_u64 v[218:219], s[58:59], 0, v[132:133]
	s_mov_b32 m0, s60
	s_nop 0
	global_load_lds_dwordx4 v[218:219], off
	v_lshl_add_u64 v[218:219], s[58:59], 0, v[136:137]
	s_add_i32 m0, s60, 0x2000
	s_nop 0
	global_load_lds_dwordx4 v[218:219], off
	v_lshl_add_u64 v[218:219], v[222:223], 0, s[16:17]
	s_mov_b32 m0, s67
	s_nop 0
	global_load_lds_dwordx4 v[218:219], off
	v_lshl_add_u64 v[218:219], v[224:225], 0, s[16:17]
	s_mov_b32 m0, s68
	s_nop 0
	global_load_lds_dwordx4 v[218:219], off
	s_waitcnt vmcnt(8)
	s_waitcnt lgkmcnt(0)
	v_mfma_f32_16x16x32_bf16 v[54:57], v[142:145], v[186:189], v[54:57]
	s_barrier
	v_mfma_f32_16x16x32_bf16 v[42:45], v[162:165], v[186:189], v[42:45]
	v_mfma_f32_16x16x32_bf16 v[30:33], v[142:145], v[194:197], v[30:33]
	v_mfma_f32_16x16x32_bf16 v[26:29], v[162:165], v[194:197], v[26:29]
	v_mfma_f32_16x16x32_bf16 v[14:17], v[142:145], v[202:205], v[14:17]
	v_mfma_f32_16x16x32_bf16 v[10:13], v[162:165], v[202:205], v[10:13]
	v_mfma_f32_16x16x32_bf16 v[6:9], v[142:145], v[210:213], v[6:9]
	v_mfma_f32_16x16x32_bf16 v[2:5], v[162:165], v[210:213], v[2:5]
	v_mfma_f32_16x16x32_bf16 v[54:57], v[158:161], v[190:193], v[54:57]
	v_mfma_f32_16x16x32_bf16 v[42:45], v[166:169], v[190:193], v[42:45]
	v_mfma_f32_16x16x32_bf16 v[30:33], v[158:161], v[198:201], v[30:33]
	v_mfma_f32_16x16x32_bf16 v[26:29], v[166:169], v[198:201], v[26:29]
	v_mfma_f32_16x16x32_bf16 v[14:17], v[158:161], v[206:209], v[14:17]
	v_mfma_f32_16x16x32_bf16 v[10:13], v[166:169], v[206:209], v[10:13]
	v_mfma_f32_16x16x32_bf16 v[6:9], v[158:161], v[214:217], v[6:9]
	v_mfma_f32_16x16x32_bf16 v[2:5], v[166:169], v[214:217], v[2:5]
	v_mfma_f32_16x16x32_bf16 v[70:73], v[170:173], v[186:189], v[70:73]
	v_mfma_f32_16x16x32_bf16 v[66:69], v[178:181], v[186:189], v[66:69]
	v_mfma_f32_16x16x32_bf16 v[50:53], v[170:173], v[194:197], v[50:53]
	v_mfma_f32_16x16x32_bf16 v[46:49], v[178:181], v[194:197], v[46:49]
	v_mfma_f32_16x16x32_bf16 v[38:41], v[170:173], v[202:205], v[38:41]
	v_mfma_f32_16x16x32_bf16 v[34:37], v[178:181], v[202:205], v[34:37]
	v_mfma_f32_16x16x32_bf16 v[22:25], v[170:173], v[210:213], v[22:25]
	v_mfma_f32_16x16x32_bf16 v[18:21], v[178:181], v[210:213], v[18:21]
	v_mfma_f32_16x16x32_bf16 v[70:73], v[174:177], v[190:193], v[70:73]
	v_mfma_f32_16x16x32_bf16 v[66:69], v[182:185], v[190:193], v[66:69]
	v_mfma_f32_16x16x32_bf16 v[50:53], v[174:177], v[198:201], v[50:53]
	v_mfma_f32_16x16x32_bf16 v[46:49], v[182:185], v[198:201], v[46:49]
	v_mfma_f32_16x16x32_bf16 v[38:41], v[174:177], v[206:209], v[38:41]
	v_mfma_f32_16x16x32_bf16 v[34:37], v[182:185], v[206:209], v[34:37]
	v_mfma_f32_16x16x32_bf16 v[22:25], v[174:177], v[214:217], v[22:25]
	v_mfma_f32_16x16x32_bf16 v[18:21], v[182:185], v[214:217], v[18:21]
	s_barrier
	s_add_i32 s87, s87, 2
	s_add_u32 s85, s85, 0x100
	s_addc_u32 s86, s86, 0
	s_add_u32 s56, s56, 0x100
	s_addc_u32 s57, s57, 0
	s_cmp_gt_u32 s87, 5
	s_cbranch_scc0 .LBB0_1498
	s_and_b64 vcc, exec, s[18:19]
	s_cbranch_vccz .LBB0_1501
	s_barrier

; #define PG8_STAGE(bufoff, gbase, voff) do { _Pragma("unroll") for (int _i = 0; _i < 2; ++_i) \
;         __builtin_amdgcn_global_load_lds((const unsigned*)((const char*)(gbase) + (voff)[_i]), (PG8_LAS unsigned*)(lds + (bufoff) + ldsw + _i * 8192), 16, 0, 0); } while (0)
; #define PG8_LDA(dst, b, h) do { _Pragma("unroll") for (int m = 0; m < 4; ++m) _Pragma("unroll") for (int k = 0; k < 2; ++k) dst[m][k] = *(const PG8_LAS bf16x8*)(lds + PG8_SA(b, h) + aoff + m * 2048 + k * 1024); } while (0)
; #define PG8_LDB(dst, b, h) do { _Pragma("unroll") for (int n = 0; n < 2; ++n) _Pragma("unroll") for (int k = 0; k < 2; ++k) dst[n][k] = *(const PG8_LAS bf16x8*)(lds + PG8_SB(b, h) + boff + n * 2048 + k * 1024); } while (0)
; #define PG8_MMA(ai, bj, At, Bt) do { __builtin_amdgcn_s_setprio(1); _Pragma("unroll") for (int m = 0; m < 4; ++m) _Pragma("unroll") for (int n = 0; n < 2; ++n) _Pragma("unroll") for (int k = 0; k < 2; ++k) \
;         acc[ai][bj][m][n] = __builtin_amdgcn_mfma_f32_16x16x32_bf16(Bt[n][k], At[m][k], acc[ai][bj][m][n], 0, 0, 0); __builtin_amdgcn_s_setprio(0); } while (0)
; template <class Epi, class Sched, bool ALIGN_EPI = false>
; __device__ __forceinline__ void gemm_phase(PG8_LAS unsigned char* lds, const Gemm g, const Sched& S, const Epi& E) {
;     ...
;         for (int t = 0; t < nt; t += 2) {
;             const bool last = (t == nt - 2);
;             const char* a1 = cA + (size_t)(t + 1) * kstep;
;             const char* a2 = last ? nA : cA + (size_t)(t + 2) * kstep; const char* b2 = last ? nB : cB + (size_t)(t + 2) * kstep;
;             const char* a3 = a2 + kstep; const char* b3 = b2 + kstep;
;             unsigned w0[2], w1[2];
; #pragma unroll
;             for (int i = 0; i < 2; ++i) { w0[i] = (Sched::GATHER && last) ? vn0[i] : vc0[i]; w1[i] = (Sched::GATHER && last) ? vn1[i] : vc1[i]; }
;             if (last && has_next) S.a_ready(nxt);
;             PG8_LDB(B0, 0, 0); PG8_LDB(B1, 0, 1); PG8_SCHED; PG8_LDA(At, 0, 0); PG8_STAGE(PG8_SA(1, 1), a1 + hstepA, vc1);
;             PG8_WAIT_V(8); PG8_WAIT_L(0); PG8_BAR; PG8_MMA(0, 0, At, B0); PG8_MMA(0, 1, At, B1); PG8_BAR; PG8_SCHED;
;             PG8_LDA(At, 0, 1); PG8_STAGE(PG8_SB(0, 0), b2, voffB); PG8_STAGE(PG8_SB(0, 1), b2 + hstep, voffB); PG8_STAGE(PG8_SA(0, 0), a2, w0);
;             PG8_WAIT_V(8); PG8_WAIT_L(0); PG8_BAR; PG8_MMA(1, 0, At, B0); PG8_MMA(1, 1, At, B1); PG8_BAR; PG8_SCHED;
.LBB0_1601:
	ds_read_b128 v[144:147], v157
	ds_read_b128 v[160:163], v157 offset:1024
	ds_read_b128 v[164:167], v157 offset:2048
	ds_read_b128 v[168:171], v157 offset:3072
	ds_read_b128 v[172:175], v158
	ds_read_b128 v[176:179], v158 offset:1024
	ds_read_b128 v[180:183], v158 offset:2048
	ds_read_b128 v[184:187], v158 offset:3072
	s_add_u32 s54, s52, 0xfffe0080
	s_addc_u32 s55, s53, -1
	s_cmp_eq_u32 s87, 4
	s_cselect_b32 s57, s25, s55
	s_cselect_b32 s56, s43, s54
	s_cselect_b32 s55, s27, s86
	s_cselect_b32 s54, s84, s85
	v_lshl_add_u64 v[220:221], s[52:53], 0, v[142:143]
	s_add_i32 m0, s45, 0xc000
	ds_read_b128 v[188:191], v159
	ds_read_b128 v[192:195], v159 offset:1024
	ds_read_b128 v[196:199], v159 offset:2048
	ds_read_b128 v[200:203], v159 offset:3072
	ds_read_b128 v[204:207], v159 offset:4096
	ds_read_b128 v[208:211], v159 offset:5120
	ds_read_b128 v[212:215], v159 offset:6144
	ds_read_b128 v[216:219], v159 offset:7168
	global_load_lds_dwordx4 v[220:221], off
	v_lshl_add_u64 v[220:221], s[52:53], 0, v[140:141]
	s_add_i32 m0, s45, 0xe000
	s_nop 0
	global_load_lds_dwordx4 v[220:221], off
	s_waitcnt vmcnt(8)
	s_waitcnt lgkmcnt(0)
	v_mfma_f32_16x16x32_bf16 v[126:129], v[144:147], v[188:191], v[126:129]
	s_barrier
	v_mfma_f32_16x16x32_bf16 v[122:125], v[164:167], v[188:191], v[122:125]
	v_mfma_f32_16x16x32_bf16 v[114:117], v[144:147], v[196:199], v[114:117]
	v_mfma_f32_16x16x32_bf16 v[106:109], v[164:167], v[196:199], v[106:109]
	v_mfma_f32_16x16x32_bf16 v[98:101], v[144:147], v[204:207], v[98:101]
	v_mfma_f32_16x16x32_bf16 v[90:93], v[164:167], v[204:207], v[90:93]
	v_mfma_f32_16x16x32_bf16 v[82:85], v[144:147], v[212:215], v[82:85]
	v_mfma_f32_16x16x32_bf16 v[74:77], v[164:167], v[212:215], v[74:77]
	v_mfma_f32_16x16x32_bf16 v[126:129], v[160:163], v[192:195], v[126:129]
	v_mfma_f32_16x16x32_bf16 v[122:125], v[168:171], v[192:195], v[122:125]
	v_mfma_f32_16x16x32_bf16 v[114:117], v[160:163], v[200:203], v[114:117]
	v_mfma_f32_16x16x32_bf16 v[106:109], v[168:171], v[200:203], v[106:109]
	v_mfma_f32_16x16x32_bf16 v[98:101], v[160:163], v[208:211], v[98:101]
	v_mfma_f32_16x16x32_bf16 v[90:93], v[168:171], v[208:211], v[90:93]
	v_mfma_f32_16x16x32_bf16 v[82:85], v[160:163], v[216:219], v[82:85]
	v_mfma_f32_16x16x32_bf16 v[74:77], v[168:171], v[216:219], v[74:77]
	v_mfma_f32_16x16x32_bf16 v[118:121], v[172:175], v[188:191], v[118:121]
	v_mfma_f32_16x16x32_bf16 v[110:113], v[180:183], v[188:191], v[110:113]
	v_mfma_f32_16x16x32_bf16 v[102:105], v[172:175], v[196:199], v[102:105]
	v_mfma_f32_16x16x32_bf16 v[94:97], v[180:183], v[196:199], v[94:97]
	v_mfma_f32_16x16x32_bf16 v[86:89], v[172:175], v[204:207], v[86:89]
	v_mfma_f32_16x16x32_bf16 v[78:81], v[180:183], v[204:207], v[78:81]
	v_mfma_f32_16x16x32_bf16 v[62:65], v[172:175], v[212:215], v[62:65]
	v_mfma_f32_16x16x32_bf16 v[58:61], v[180:183], v[212:215], v[58:61]
	v_mfma_f32_16x16x32_bf16 v[118:121], v[176:179], v[192:195], v[118:121]
	v_mfma_f32_16x16x32_bf16 v[110:113], v[184:187], v[192:195], v[110:113]
	v_mfma_f32_16x16x32_bf16 v[102:105], v[176:179], v[200:203], v[102:105]
	v_mfma_f32_16x16x32_bf16 v[94:97], v[184:187], v[200:203], v[94:97]
	v_mfma_f32_16x16x32_bf16 v[86:89], v[176:179], v[208:211], v[86:89]
	v_mfma_f32_16x16x32_bf16 v[78:81], v[184:187], v[208:211], v[78:81]
	v_mfma_f32_16x16x32_bf16 v[62:65], v[176:179], v[216:219], v[62:65]
	v_mfma_f32_16x16x32_bf16 v[58:61], v[184:187], v[216:219], v[58:61]
	s_barrier
	s_add_i32 s88, s74, s62
	v_lshl_add_u64 v[220:221], s[54:55], 0, v[134:135]
	s_mov_b32 m0, s88
	ds_read_b128 v[188:191], v159 offset:16384
	ds_read_b128 v[192:195], v159 offset:17408
	ds_read_b128 v[196:199], v159 offset:18432
	ds_read_b128 v[200:203], v159 offset:19456
	ds_read_b128 v[204:207], v159 offset:20480
	ds_read_b128 v[208:211], v159 offset:21504
	ds_read_b128 v[212:215], v159 offset:22528
	ds_read_b128 v[216:219], v159 offset:23552
	global_load_lds_dwordx4 v[220:221], off
	s_add_i32 m0, s88, 0x2000
	s_add_u32 s88, s54, 0x20000
	v_lshl_add_u64 v[222:223], s[54:55], 0, v[138:139]
	s_addc_u32 s89, s55, 0
	s_add_i32 s90, s75, s62
	global_load_lds_dwordx4 v[222:223], off
	v_lshl_add_u64 v[224:225], s[88:89], 0, v[134:135]
	s_mov_b32 m0, s90
	v_lshl_add_u64 v[226:227], s[56:57], 0, v[136:137]
	global_load_lds_dwordx4 v[224:225], off
	v_lshl_add_u64 v[224:225], s[88:89], 0, v[138:139]
	s_add_i32 m0, s90, 0x2000
	s_nop 0
	global_load_lds_dwordx4 v[224:225], off
	v_lshl_add_u64 v[224:225], s[56:57], 0, v[132:133]
	s_mov_b32 m0, s45
	s_nop 0
	global_load_lds_dwordx4 v[224:225], off
	s_mov_b32 m0, s63
	s_nop 0
	global_load_lds_dwordx4 v[226:227], off
	s_waitcnt vmcnt(8)
	s_waitcnt lgkmcnt(0)
	v_mfma_f32_16x16x32_bf16 v[54:57], v[144:147], v[188:191], v[54:57]
	s_barrier
; #define PG8_STAGE(bufoff, gbase, voff) do { _Pragma("unroll") for (int _i = 0; _i < 2; ++_i) \
;         __builtin_amdgcn_global_load_lds((const unsigned*)((const char*)(gbase) + (voff)[_i]), (PG8_LAS unsigned*)(lds + (bufoff) + ldsw + _i * 8192), 16, 0, 0); } while (0)
; #define PG8_LDA(dst, b, h) do { _Pragma("unroll") for (int m = 0; m < 4; ++m) _Pragma("unroll") for (int k = 0; k < 2; ++k) dst[m][k] = *(const PG8_LAS bf16x8*)(lds + PG8_SA(b, h) + aoff + m * 2048 + k * 1024); } while (0)
; #define PG8_LDB(dst, b, h) do { _Pragma("unroll") for (int n = 0; n < 2; ++n) _Pragma("unroll") for (int k = 0; k < 2; ++k) dst[n][k] = *(const PG8_LAS bf16x8*)(lds + PG8_SB(b, h) + boff + n * 2048 + k * 1024); } while (0)
; #define PG8_MMA(ai, bj, At, Bt) do { __builtin_amdgcn_s_setprio(1); _Pragma("unroll") for (int m = 0; m < 4; ++m) _Pragma("unroll") for (int n = 0; n < 2; ++n) _Pragma("unroll") for (int k = 0; k < 2; ++k) \
;         acc[ai][bj][m][n] = __builtin_amdgcn_mfma_f32_16x16x32_bf16(Bt[n][k], At[m][k], acc[ai][bj][m][n], 0, 0, 0); __builtin_amdgcn_s_setprio(0); } while (0)
; #define PG8_WAIT_V(n) asm volatile("s_waitcnt vmcnt(" #n ")" ::: "memory")
; #define PG8_WAIT_L(n) asm volatile("s_waitcnt lgkmcnt(" #n ")" ::: "memory")
; #define PG8_BAR __builtin_amdgcn_s_barrier()
; #define PG8_SCHED __builtin_amdgcn_sched_barrier(0)
; template <class Epi, class Sched, bool ALIGN_EPI = false>
; __device__ __forceinline__ void gemm_phase(PG8_LAS unsigned char* lds, const Gemm g, const Sched& S, const Epi& E) {
;     ...
;             PG8_WAIT_V(8); PG8_WAIT_L(0); PG8_BAR; PG8_MMA(1, 0, At, B0); PG8_MMA(1, 1, At, B1); PG8_BAR; PG8_SCHED;
;             PG8_LDB(B0, 1, 0); PG8_LDB(B1, 1, 1); PG8_SCHED; PG8_LDA(At, 1, 0); PG8_STAGE(PG8_SA(0, 1), a2 + hstepA, w1);
;             PG8_WAIT_V(8); PG8_WAIT_L(0); PG8_BAR; PG8_MMA(0, 0, At, B0); PG8_MMA(0, 1, At, B1); PG8_BAR; PG8_SCHED;
	v_mfma_f32_16x16x32_bf16 v[42:45], v[164:167], v[188:191], v[42:45]
	v_mfma_f32_16x16x32_bf16 v[30:33], v[144:147], v[196:199], v[30:33]
	v_mfma_f32_16x16x32_bf16 v[26:29], v[164:167], v[196:199], v[26:29]
	v_mfma_f32_16x16x32_bf16 v[14:17], v[144:147], v[204:207], v[14:17]
	v_mfma_f32_16x16x32_bf16 v[10:13], v[164:167], v[204:207], v[10:13]
	v_mfma_f32_16x16x32_bf16 v[6:9], v[144:147], v[212:215], v[6:9]
	v_mfma_f32_16x16x32_bf16 v[2:5], v[164:167], v[212:215], v[2:5]
	v_mfma_f32_16x16x32_bf16 v[54:57], v[160:163], v[192:195], v[54:57]
	v_mfma_f32_16x16x32_bf16 v[42:45], v[168:171], v[192:195], v[42:45]
	v_mfma_f32_16x16x32_bf16 v[30:33], v[160:163], v[200:203], v[30:33]
	v_mfma_f32_16x16x32_bf16 v[26:29], v[168:171], v[200:203], v[26:29]
	v_mfma_f32_16x16x32_bf16 v[14:17], v[160:163], v[208:211], v[14:17]
	v_mfma_f32_16x16x32_bf16 v[10:13], v[168:171], v[208:211], v[10:13]
	v_mfma_f32_16x16x32_bf16 v[6:9], v[160:163], v[216:219], v[6:9]
	v_mfma_f32_16x16x32_bf16 v[2:5], v[168:171], v[216:219], v[2:5]
	v_mfma_f32_16x16x32_bf16 v[70:73], v[172:175], v[188:191], v[70:73]
	v_mfma_f32_16x16x32_bf16 v[66:69], v[180:183], v[188:191], v[66:69]
	v_mfma_f32_16x16x32_bf16 v[50:53], v[172:175], v[196:199], v[50:53]
	v_mfma_f32_16x16x32_bf16 v[46:49], v[180:183], v[196:199], v[46:49]
	v_mfma_f32_16x16x32_bf16 v[38:41], v[172:175], v[204:207], v[38:41]
	v_mfma_f32_16x16x32_bf16 v[34:37], v[180:183], v[204:207], v[34:37]
	v_mfma_f32_16x16x32_bf16 v[22:25], v[172:175], v[212:215], v[22:25]
	v_mfma_f32_16x16x32_bf16 v[18:21], v[180:183], v[212:215], v[18:21]
	v_mfma_f32_16x16x32_bf16 v[70:73], v[176:179], v[192:195], v[70:73]
	v_mfma_f32_16x16x32_bf16 v[66:69], v[184:187], v[192:195], v[66:69]
	v_mfma_f32_16x16x32_bf16 v[50:53], v[176:179], v[200:203], v[50:53]
	v_mfma_f32_16x16x32_bf16 v[46:49], v[184:187], v[200:203], v[46:49]
	v_mfma_f32_16x16x32_bf16 v[38:41], v[176:179], v[208:211], v[38:41]
	v_mfma_f32_16x16x32_bf16 v[34:37], v[184:187], v[208:211], v[34:37]
	v_mfma_f32_16x16x32_bf16 v[22:25], v[176:179], v[216:219], v[22:25]
	v_mfma_f32_16x16x32_bf16 v[18:21], v[184:187], v[216:219], v[18:21]
	s_barrier
	s_add_i32 s88, 0, 0x18000
	s_add_i32 s89, 0, 0x1c000
	v_add_u32_e32 v168, s88, v148
	v_add_u32_e32 v184, s89, v148
	ds_read_b128 v[144:147], v168
	ds_read_b128 v[160:163], v168 offset:1024
	ds_read_b128 v[164:167], v168 offset:2048
	ds_read_b128 v[168:171], v168 offset:3072
	ds_read_b128 v[172:175], v184
	ds_read_b128 v[176:179], v184 offset:1024
	ds_read_b128 v[180:183], v184 offset:2048
	ds_read_b128 v[184:187], v184 offset:3072
	s_add_u32 s56, s56, 0x20000
	s_addc_u32 s57, s57, 0
	s_mov_b32 m0, s64
	v_lshl_add_u64 v[228:229], s[56:57], 0, v[132:133]
	ds_read_b128 v[188:191], v159 offset:32768
	ds_read_b128 v[192:195], v159 offset:33792
	ds_read_b128 v[196:199], v159 offset:34816
	ds_read_b128 v[200:203], v159 offset:35840
	ds_read_b128 v[204:207], v159 offset:36864
	ds_read_b128 v[208:211], v159 offset:37888
	ds_read_b128 v[212:215], v159 offset:38912
	ds_read_b128 v[216:219], v159 offset:39936
	global_load_lds_dwordx4 v[228:229], off
	v_lshl_add_u64 v[228:229], s[56:57], 0, v[136:137]
	s_mov_b32 m0, s65
	s_nop 0
	global_load_lds_dwordx4 v[228:229], off
	s_waitcnt vmcnt(8)
	s_waitcnt lgkmcnt(0)
	v_mfma_f32_16x16x32_bf16 v[126:129], v[144:147], v[188:191], v[126:129]
	s_barrier
	v_mfma_f32_16x16x32_bf16 v[122:125], v[164:167], v[188:191], v[122:125]
	v_mfma_f32_16x16x32_bf16 v[114:117], v[144:147], v[196:199], v[114:117]
	v_mfma_f32_16x16x32_bf16 v[106:109], v[164:167], v[196:199], v[106:109]
	v_mfma_f32_16x16x32_bf16 v[98:101], v[144:147], v[204:207], v[98:101]
	v_mfma_f32_16x16x32_bf16 v[90:93], v[164:167], v[204:207], v[90:93]
	v_mfma_f32_16x16x32_bf16 v[82:85], v[144:147], v[212:215], v[82:85]
	v_mfma_f32_16x16x32_bf16 v[74:77], v[164:167], v[212:215], v[74:77]
	v_mfma_f32_16x16x32_bf16 v[126:129], v[160:163], v[192:195], v[126:129]
	v_mfma_f32_16x16x32_bf16 v[122:125], v[168:171], v[192:195], v[122:125]
	v_mfma_f32_16x16x32_bf16 v[114:117], v[160:163], v[200:203], v[114:117]
	v_mfma_f32_16x16x32_bf16 v[106:109], v[168:171], v[200:203], v[106:109]
	v_mfma_f32_16x16x32_bf16 v[98:101], v[160:163], v[208:211], v[98:101]
	v_mfma_f32_16x16x32_bf16 v[90:93], v[168:171], v[208:211], v[90:93]
	v_mfma_f32_16x16x32_bf16 v[82:85], v[160:163], v[216:219], v[82:85]
	v_mfma_f32_16x16x32_bf16 v[74:77], v[168:171], v[216:219], v[74:77]
	v_mfma_f32_16x16x32_bf16 v[118:121], v[172:175], v[188:191], v[118:121]
	v_mfma_f32_16x16x32_bf16 v[110:113], v[180:183], v[188:191], v[110:113]
	v_mfma_f32_16x16x32_bf16 v[102:105], v[172:175], v[196:199], v[102:105]
	v_mfma_f32_16x16x32_bf16 v[94:97], v[180:183], v[196:199], v[94:97]
	v_mfma_f32_16x16x32_bf16 v[86:89], v[172:175], v[204:207], v[86:89]
	v_mfma_f32_16x16x32_bf16 v[78:81], v[180:183], v[204:207], v[78:81]
	v_mfma_f32_16x16x32_bf16 v[62:65], v[172:175], v[212:215], v[62:65]
	v_mfma_f32_16x16x32_bf16 v[58:61], v[180:183], v[212:215], v[58:61]
	v_mfma_f32_16x16x32_bf16 v[118:121], v[176:179], v[192:195], v[118:121]
	v_mfma_f32_16x16x32_bf16 v[110:113], v[184:187], v[192:195], v[110:113]
	v_mfma_f32_16x16x32_bf16 v[102:105], v[176:179], v[200:203], v[102:105]
	v_mfma_f32_16x16x32_bf16 v[94:97], v[184:187], v[200:203], v[94:97]
	v_mfma_f32_16x16x32_bf16 v[86:89], v[176:179], v[208:211], v[86:89]
	v_mfma_f32_16x16x32_bf16 v[78:81], v[184:187], v[208:211], v[78:81]
	v_mfma_f32_16x16x32_bf16 v[62:65], v[176:179], v[216:219], v[62:65]
	v_mfma_f32_16x16x32_bf16 v[58:61], v[184:187], v[216:219], v[58:61]
	s_barrier
; #define PG8_STAGE(bufoff, gbase, voff) do { _Pragma("unroll") for (int _i = 0; _i < 2; ++_i) \
;         __builtin_amdgcn_global_load_lds((const unsigned*)((const char*)(gbase) + (voff)[_i]), (PG8_LAS unsigned*)(lds + (bufoff) + ldsw + _i * 8192), 16, 0, 0); } while (0)
; #define PG8_LDA(dst, b, h) do { _Pragma("unroll") for (int m = 0; m < 4; ++m) _Pragma("unroll") for (int k = 0; k < 2; ++k) dst[m][k] = *(const PG8_LAS bf16x8*)(lds + PG8_SA(b, h) + aoff + m * 2048 + k * 1024); } while (0)
; #define PG8_MMA(ai, bj, At, Bt) do { __builtin_amdgcn_s_setprio(1); _Pragma("unroll") for (int m = 0; m < 4; ++m) _Pragma("unroll") for (int n = 0; n < 2; ++n) _Pragma("unroll") for (int k = 0; k < 2; ++k) \
;         acc[ai][bj][m][n] = __builtin_amdgcn_mfma_f32_16x16x32_bf16(Bt[n][k], At[m][k], acc[ai][bj][m][n], 0, 0, 0); __builtin_amdgcn_s_setprio(0); } while (0)
; #define PG8_WAIT_V(n) asm volatile("s_waitcnt vmcnt(" #n ")" ::: "memory")
; #define PG8_WAIT_L(n) asm volatile("s_waitcnt lgkmcnt(" #n ")" ::: "memory")
; #define PG8_BAR __builtin_amdgcn_s_barrier()
; #define PG8_SCHED __builtin_amdgcn_sched_barrier(0)
; template <class Epi, class Sched, bool ALIGN_EPI = false>
; __device__ __forceinline__ void gemm_phase(PG8_LAS unsigned char* lds, const Gemm g, const Sched& S, const Epi& E) {
;     ...
;             PG8_LDA(At, 1, 1); PG8_STAGE(PG8_SB(1, 0), b3, voffB); PG8_STAGE(PG8_SB(1, 1), b3 + hstep, voffB); PG8_STAGE(PG8_SA(1, 0), a3, w0);
;             PG8_WAIT_V(8); PG8_WAIT_L(0); PG8_BAR; PG8_MMA(1, 0, At, B0); PG8_MMA(1, 1, At, B1); PG8_BAR; PG8_SCHED;
;             if constexpr (Epi::KSCALE) { if (((t + 2) & 7) == 0 && t + 2 < nt) { E.kscale(acc, pf, ((t + 2) >> 3) - 1, wr, fr); PG8_SCHED; } }
;         }
;         if constexpr (ALIGN_EPI) { if (wr == 0) PG8_BAR; }
	s_add_i32 s56, s88, s62
	v_lshl_add_u64 v[220:221], v[220:221], 0, s[12:13]
	s_mov_b32 m0, s56
	ds_read_b128 v[188:191], v159 offset:49152
	ds_read_b128 v[192:195], v159 offset:50176
	ds_read_b128 v[196:199], v159 offset:51200
	ds_read_b128 v[200:203], v159 offset:52224
	ds_read_b128 v[204:207], v159 offset:53248
	ds_read_b128 v[208:211], v159 offset:54272
	ds_read_b128 v[212:215], v159 offset:55296
	ds_read_b128 v[216:219], v159 offset:56320
	global_load_lds_dwordx4 v[220:221], off
	s_add_i32 m0, s56, 0x2000
	s_add_u32 s54, s54, 0x20080
	v_lshl_add_u64 v[220:221], v[222:223], 0, s[12:13]
	s_addc_u32 s55, s55, 0
	s_add_i32 s56, s89, s62
	global_load_lds_dwordx4 v[220:221], off
	v_lshl_add_u64 v[220:221], s[54:55], 0, v[134:135]
	s_mov_b32 m0, s56
	s_nop 0
	global_load_lds_dwordx4 v[220:221], off
	v_lshl_add_u64 v[220:221], s[54:55], 0, v[138:139]
	s_add_i32 m0, s56, 0x2000
	s_nop 0
	global_load_lds_dwordx4 v[220:221], off
	v_lshl_add_u64 v[220:221], v[224:225], 0, s[12:13]
	s_mov_b32 m0, s68
	s_nop 0
	global_load_lds_dwordx4 v[220:221], off
	v_lshl_add_u64 v[220:221], v[226:227], 0, s[12:13]
	s_mov_b32 m0, s69
	s_nop 0
	global_load_lds_dwordx4 v[220:221], off
	s_waitcnt vmcnt(8)
	s_waitcnt lgkmcnt(0)
	v_mfma_f32_16x16x32_bf16 v[54:57], v[144:147], v[188:191], v[54:57]
	s_barrier
	v_mfma_f32_16x16x32_bf16 v[42:45], v[164:167], v[188:191], v[42:45]
	v_mfma_f32_16x16x32_bf16 v[30:33], v[144:147], v[196:199], v[30:33]
	v_mfma_f32_16x16x32_bf16 v[26:29], v[164:167], v[196:199], v[26:29]
	v_mfma_f32_16x16x32_bf16 v[14:17], v[144:147], v[204:207], v[14:17]
	v_mfma_f32_16x16x32_bf16 v[10:13], v[164:167], v[204:207], v[10:13]
	v_mfma_f32_16x16x32_bf16 v[6:9], v[144:147], v[212:215], v[6:9]
	v_mfma_f32_16x16x32_bf16 v[2:5], v[164:167], v[212:215], v[2:5]
	v_mfma_f32_16x16x32_bf16 v[54:57], v[160:163], v[192:195], v[54:57]
	v_mfma_f32_16x16x32_bf16 v[42:45], v[168:171], v[192:195], v[42:45]
	v_mfma_f32_16x16x32_bf16 v[30:33], v[160:163], v[200:203], v[30:33]
	v_mfma_f32_16x16x32_bf16 v[26:29], v[168:171], v[200:203], v[26:29]
	v_mfma_f32_16x16x32_bf16 v[14:17], v[160:163], v[208:211], v[14:17]
	v_mfma_f32_16x16x32_bf16 v[10:13], v[168:171], v[208:211], v[10:13]
	v_mfma_f32_16x16x32_bf16 v[6:9], v[160:163], v[216:219], v[6:9]
	v_mfma_f32_16x16x32_bf16 v[2:5], v[168:171], v[216:219], v[2:5]
	v_mfma_f32_16x16x32_bf16 v[70:73], v[172:175], v[188:191], v[70:73]
	v_mfma_f32_16x16x32_bf16 v[66:69], v[180:183], v[188:191], v[66:69]
	v_mfma_f32_16x16x32_bf16 v[50:53], v[172:175], v[196:199], v[50:53]
	v_mfma_f32_16x16x32_bf16 v[46:49], v[180:183], v[196:199], v[46:49]
	v_mfma_f32_16x16x32_bf16 v[38:41], v[172:175], v[204:207], v[38:41]
	v_mfma_f32_16x16x32_bf16 v[34:37], v[180:183], v[204:207], v[34:37]
	v_mfma_f32_16x16x32_bf16 v[22:25], v[172:175], v[212:215], v[22:25]
	v_mfma_f32_16x16x32_bf16 v[18:21], v[180:183], v[212:215], v[18:21]
	v_mfma_f32_16x16x32_bf16 v[70:73], v[176:179], v[192:195], v[70:73]
	v_mfma_f32_16x16x32_bf16 v[66:69], v[184:187], v[192:195], v[66:69]
	v_mfma_f32_16x16x32_bf16 v[50:53], v[176:179], v[200:203], v[50:53]
	v_mfma_f32_16x16x32_bf16 v[46:49], v[184:187], v[200:203], v[46:49]
	v_mfma_f32_16x16x32_bf16 v[38:41], v[176:179], v[208:211], v[38:41]
	v_mfma_f32_16x16x32_bf16 v[34:37], v[184:187], v[208:211], v[34:37]
	v_mfma_f32_16x16x32_bf16 v[22:25], v[176:179], v[216:219], v[22:25]
	v_mfma_f32_16x16x32_bf16 v[18:21], v[184:187], v[216:219], v[18:21]
	s_barrier
	s_add_i32 s87, s87, 2
	s_add_u32 s85, s85, 0x100
	s_addc_u32 s86, s86, 0
	s_add_u32 s52, s52, 0x100
	s_addc_u32 s53, s53, 0
	s_cmp_gt_u32 s87, 5
	s_cbranch_scc0 .LBB0_1601
	s_and_b64 vcc, exec, s[14:15]
	s_cbranch_vccz .LBB0_1604
	s_barrier
